# on top of the loop-edge edit: 52 redundant post-barrier lgkmcnt(0) waits removed from the GEMM main loops (the same wait already precedes the barrier, no LDS op in between)
# baseline (speedup 1.0000x reference)
; #define PG8_STAGE(bufoff, gbase, voff) do { _Pragma("unroll") for (int _i = 0; _i < 2; ++_i) \
;         __builtin_amdgcn_global_load_lds((const unsigned*)((const char*)(gbase) + (voff)[_i]), (LAS unsigned*)(lds + (bufoff) + ldsw + _i * 8192), 16, 0, 0); } while (0)
; #define PG8_LDA(dst, b, h) do { _Pragma("unroll") for (int m = 0; m < 4; ++m) _Pragma("unroll") for (int k = 0; k < 2; ++k) dst[m][k] = *(const LAS bf16x8*)(lds + PG8_SA(b, h) + aoff + m * 2048 + k * 1024); } while (0)
; #define PG8_LDB(dst, b, h) do { _Pragma("unroll") for (int n = 0; n < 2; ++n) _Pragma("unroll") for (int k = 0; k < 2; ++k) dst[n][k] = *(const LAS bf16x8*)(lds + PG8_SB(b, h) + boff + n * 2048 + k * 1024); } while (0)
; #define PG8_MMA(ai, bj, At, Bt) do { __builtin_amdgcn_s_setprio(1); _Pragma("unroll") for (int m = 0; m < 4; ++m) _Pragma("unroll") for (int n = 0; n < 2; ++n) _Pragma("unroll") for (int k = 0; k < 2; ++k) \
;         acc[ai][bj][m][n] = __builtin_amdgcn_mfma_f32_16x16x32_bf16(Bt[n][k], At[m][k], acc[ai][bj][m][n], 0, 0, 0); __builtin_amdgcn_s_setprio(0); } while (0)
; #define PG8_WAIT_V(n) asm volatile("s_waitcnt vmcnt(" #n ")" ::: "memory")
; #define PG8_WAIT_L(n) asm volatile("s_waitcnt lgkmcnt(" #n ")" ::: "memory")
; #define PG8_BAR __builtin_amdgcn_s_barrier()
; #define PG8_SCHED __builtin_amdgcn_sched_barrier(0)
; #define PG8_LDA(dst, b, h) do { _Pragma("unroll") for (int m = 0; m < 4; ++m) PG8_LD1(dst[m], PG8_SA(b, h) + aoff0 + m * 2048, PG8_SA(b, h) + aoff1 + m * 2048); } while (0)
;     ...
;             const bool last = (t == nt - 2);
;             const char* a1 = cA + (size_t)(t + 1) * kstep;
;             const char* a2 = last ? nA : cA + (size_t)(t + 2) * kstep; const char* b2 = last ? nB : cB + (size_t)(t + 2) * kstep;
;             const char* a3 = a2 + kstep; const char* b3 = b2 + kstep;
;             if (last && has_next) S.a_ready(nxt);
;             PG8_LDB(B0, 0, 0); PG8_LDB(B1, 0, 1); PG8_SCHED; PG8_LDA(At, 0, 0); PG8_STAGE(PG8_SA(1, 1), a1 + hstepA, voffA);
;             PG8_WAIT_V(8); PG8_WAIT_L(0); PG8_BAR; PG8_MMA(0, 0, At, B0); PG8_MMA(0, 1, At, B1); PG8_BAR; PG8_SCHED;
;             PG8_LDA(At, 0, 1); PG8_STAGE(PG8_SB(0, 0), b2, voffB); PG8_STAGE(PG8_SB(0, 1), b2 + hstepB, voffB); PG8_STAGE(PG8_SA(0, 0), a2, voffA);
;             PG8_WAIT_V(8); PG8_WAIT_L(0); PG8_BAR; PG8_MMA(1, 0, At, B0); PG8_MMA(1, 1, At, B1); PG8_BAR; PG8_SCHED;
.LBB0_143:
	ds_read_b128 v[158:161], v187
	ds_read_b128 v[146:149], v188
	ds_read_b128 v[154:157], v195
	ds_read_b128 v[150:153], v196
	ds_read_b128 v[142:145], v189
	ds_read_b128 v[130:133], v190
	ds_read_b128 v[138:141], v197
	ds_read_b128 v[134:137], v198
	s_add_u32 s84, s82, 0x100
	s_addc_u32 s85, s83, 0
	s_cmp_eq_u32 vcc_lo, 12
	s_cselect_b32 s89, s45, s85
	s_cselect_b32 s88, s47, s84
	s_cselect_b32 s87, s75, s95
	s_cselect_b32 s86, s93, s94
	v_lshl_add_u64 v[230:231], s[82:83], 0, v[170:171]
	s_add_i32 m0, s0, 0xc000
	ds_read_b128 v[178:181], v204
	ds_read_b128 v[182:185], v204 offset:2048
	ds_read_b128 v[206:209], v205
	ds_read_b128 v[210:213], v205 offset:2048
	ds_read_b128 v[214:217], v204 offset:4096
	ds_read_b128 v[218:221], v204 offset:6144
	ds_read_b128 v[222:225], v205 offset:4096
	ds_read_b128 v[226:229], v205 offset:6144
	global_load_lds_dwordx4 v[230:231], off
	v_lshl_add_u64 v[230:231], s[82:83], 0, v[172:173]
	s_add_i32 m0, s0, 0xe000
	s_nop 0
	global_load_lds_dwordx4 v[230:231], off
	s_waitcnt vmcnt(8)
	s_waitcnt lgkmcnt(0)
	s_barrier
	s_setprio 1
	v_mfma_i32_16x16x64_i8 v[126:129], v[158:161], v[178:181], v[126:129]
	v_mfma_i32_16x16x64_i8 v[122:125], v[154:157], v[178:181], v[122:125]
	v_mfma_i32_16x16x64_i8 v[118:121], v[158:161], v[182:185], v[118:121]
	v_mfma_i32_16x16x64_i8 v[114:117], v[154:157], v[182:185], v[114:117]
	v_mfma_i32_16x16x64_i8 v[110:113], v[158:161], v[214:217], v[110:113]
	v_mfma_i32_16x16x64_i8 v[106:109], v[154:157], v[214:217], v[106:109]
	v_mfma_i32_16x16x64_i8 v[102:105], v[158:161], v[218:221], v[102:105]
	v_mfma_i32_16x16x64_i8 v[98:101], v[154:157], v[218:221], v[98:101]
	s_nop 0
	v_mfma_i32_16x16x64_i8 v[126:129], v[146:149], v[206:209], v[126:129]
	v_mfma_i32_16x16x64_i8 v[122:125], v[150:153], v[206:209], v[122:125]
	v_mfma_i32_16x16x64_i8 v[118:121], v[146:149], v[210:213], v[118:121]
	v_mfma_i32_16x16x64_i8 v[114:117], v[150:153], v[210:213], v[114:117]
	v_mfma_i32_16x16x64_i8 v[110:113], v[146:149], v[222:225], v[110:113]
	v_mfma_i32_16x16x64_i8 v[106:109], v[150:153], v[222:225], v[106:109]
	v_mfma_i32_16x16x64_i8 v[102:105], v[146:149], v[226:229], v[102:105]
	v_mfma_i32_16x16x64_i8 v[98:101], v[150:153], v[226:229], v[98:101]
	s_setprio 0
	s_setprio 1
	v_mfma_i32_16x16x64_i8 v[94:97], v[142:145], v[178:181], v[94:97]
	v_mfma_i32_16x16x64_i8 v[90:93], v[138:141], v[178:181], v[90:93]
	v_mfma_i32_16x16x64_i8 v[86:89], v[142:145], v[182:185], v[86:89]
	v_mfma_i32_16x16x64_i8 v[82:85], v[138:141], v[182:185], v[82:85]
	v_mfma_i32_16x16x64_i8 v[78:81], v[142:145], v[214:217], v[78:81]
	v_mfma_i32_16x16x64_i8 v[74:77], v[138:141], v[214:217], v[74:77]
	v_mfma_i32_16x16x64_i8 v[70:73], v[142:145], v[218:221], v[70:73]
	v_mfma_i32_16x16x64_i8 v[66:69], v[138:141], v[218:221], v[66:69]
	s_nop 0
	v_mfma_i32_16x16x64_i8 v[94:97], v[130:133], v[206:209], v[94:97]
	v_mfma_i32_16x16x64_i8 v[90:93], v[134:137], v[206:209], v[90:93]
	v_mfma_i32_16x16x64_i8 v[86:89], v[130:133], v[210:213], v[86:89]
	v_mfma_i32_16x16x64_i8 v[82:85], v[134:137], v[210:213], v[82:85]
	v_mfma_i32_16x16x64_i8 v[78:81], v[130:133], v[222:225], v[78:81]
	v_mfma_i32_16x16x64_i8 v[74:77], v[134:137], v[222:225], v[74:77]
	v_mfma_i32_16x16x64_i8 v[70:73], v[130:133], v[226:229], v[70:73]
	v_mfma_i32_16x16x64_i8 v[66:69], v[134:137], v[226:229], v[66:69]
	s_setprio 0
	s_barrier
	s_mov_b32 m0, s1
	v_lshl_add_u64 v[178:179], s[86:87], 0, v[166:167]
	s_add_u32 s8, s86, 0x40000
	ds_read_b128 v[206:209], v204 offset:16384
	ds_read_b128 v[210:213], v204 offset:18432
	ds_read_b128 v[214:217], v205 offset:16384
	ds_read_b128 v[218:221], v205 offset:18432
	ds_read_b128 v[222:225], v204 offset:20480
	ds_read_b128 v[226:229], v204 offset:22528
	ds_read_b128 v[230:233], v205 offset:20480
	ds_read_b128 v[234:237], v205 offset:22528
	global_load_lds_dwordx4 v[178:179], off
	v_lshl_add_u64 v[180:181], s[86:87], 0, v[162:163]
	s_mov_b32 m0, s10
	s_addc_u32 s9, s87, 0
	global_load_lds_dwordx4 v[180:181], off
	v_lshl_add_u64 v[182:183], s[8:9], 0, v[166:167]
	s_mov_b32 m0, s11
	v_lshl_add_u64 v[184:185], s[88:89], 0, v[164:165]
	global_load_lds_dwordx4 v[182:183], off
	v_lshl_add_u64 v[182:183], s[8:9], 0, v[162:163]
	s_mov_b32 m0, s24
	s_nop 0
	global_load_lds_dwordx4 v[182:183], off
	v_lshl_add_u64 v[182:183], s[88:89], 0, v[168:169]
	s_mov_b32 m0, s0
	s_nop 0
	global_load_lds_dwordx4 v[182:183], off
	s_mov_b32 m0, s25
	s_nop 0
	global_load_lds_dwordx4 v[184:185], off
	s_waitcnt vmcnt(8)
	s_waitcnt lgkmcnt(0)
	s_barrier
	s_setprio 1
	v_mfma_i32_16x16x64_i8 v[62:65], v[158:161], v[206:209], v[62:65]
	v_mfma_i32_16x16x64_i8 v[58:61], v[154:157], v[206:209], v[58:61]
	v_mfma_i32_16x16x64_i8 v[54:57], v[158:161], v[210:213], v[54:57]
	v_mfma_i32_16x16x64_i8 v[50:53], v[154:157], v[210:213], v[50:53]
	v_mfma_i32_16x16x64_i8 v[46:49], v[158:161], v[222:225], v[46:49]
	v_mfma_i32_16x16x64_i8 v[42:45], v[154:157], v[222:225], v[42:45]
	v_mfma_i32_16x16x64_i8 v[38:41], v[158:161], v[226:229], v[38:41]
	v_mfma_i32_16x16x64_i8 v[34:37], v[154:157], v[226:229], v[34:37]
	s_nop 0
	v_mfma_i32_16x16x64_i8 v[62:65], v[146:149], v[214:217], v[62:65]
	v_mfma_i32_16x16x64_i8 v[58:61], v[150:153], v[214:217], v[58:61]
	v_mfma_i32_16x16x64_i8 v[54:57], v[146:149], v[218:221], v[54:57]
	v_mfma_i32_16x16x64_i8 v[50:53], v[150:153], v[218:221], v[50:53]
	v_mfma_i32_16x16x64_i8 v[46:49], v[146:149], v[230:233], v[46:49]
	v_mfma_i32_16x16x64_i8 v[42:45], v[150:153], v[230:233], v[42:45]
	v_mfma_i32_16x16x64_i8 v[38:41], v[146:149], v[234:237], v[38:41]
	v_mfma_i32_16x16x64_i8 v[34:37], v[150:153], v[234:237], v[34:37]
	s_setprio 0
	s_setprio 1
	v_mfma_i32_16x16x64_i8 v[30:33], v[142:145], v[206:209], v[30:33]
	v_mfma_i32_16x16x64_i8 v[26:29], v[138:141], v[206:209], v[26:29]
	v_mfma_i32_16x16x64_i8 v[22:25], v[142:145], v[210:213], v[22:25]
	v_mfma_i32_16x16x64_i8 v[18:21], v[138:141], v[210:213], v[18:21]
	v_mfma_i32_16x16x64_i8 v[14:17], v[142:145], v[222:225], v[14:17]
	v_mfma_i32_16x16x64_i8 v[10:13], v[138:141], v[222:225], v[10:13]
	v_mfma_i32_16x16x64_i8 v[6:9], v[142:145], v[226:229], v[6:9]
	v_mfma_i32_16x16x64_i8 v[2:5], v[138:141], v[226:229], v[2:5]
	s_nop 0
	v_mfma_i32_16x16x64_i8 v[30:33], v[130:133], v[214:217], v[30:33]
	v_mfma_i32_16x16x64_i8 v[26:29], v[134:137], v[214:217], v[26:29]
	v_mfma_i32_16x16x64_i8 v[22:25], v[130:133], v[218:221], v[22:25]
	v_mfma_i32_16x16x64_i8 v[18:21], v[134:137], v[218:221], v[18:21]
	v_mfma_i32_16x16x64_i8 v[14:17], v[130:133], v[230:233], v[14:17]
	v_mfma_i32_16x16x64_i8 v[10:13], v[134:137], v[230:233], v[10:13]
	v_mfma_i32_16x16x64_i8 v[6:9], v[130:133], v[234:237], v[6:9]
	v_mfma_i32_16x16x64_i8 v[2:5], v[134:137], v[234:237], v[2:5]
	s_setprio 0
	s_barrier
; #define PG8_STAGE(bufoff, gbase, voff) do { _Pragma("unroll") for (int _i = 0; _i < 2; ++_i) \
;         __builtin_amdgcn_global_load_lds((const unsigned*)((const char*)(gbase) + (voff)[_i]), (LAS unsigned*)(lds + (bufoff) + ldsw + _i * 8192), 16, 0, 0); } while (0)
; #define PG8_LDA(dst, b, h) do { _Pragma("unroll") for (int m = 0; m < 4; ++m) _Pragma("unroll") for (int k = 0; k < 2; ++k) dst[m][k] = *(const LAS bf16x8*)(lds + PG8_SA(b, h) + aoff + m * 2048 + k * 1024); } while (0)
; #define PG8_LDB(dst, b, h) do { _Pragma("unroll") for (int n = 0; n < 2; ++n) _Pragma("unroll") for (int k = 0; k < 2; ++k) dst[n][k] = *(const LAS bf16x8*)(lds + PG8_SB(b, h) + boff + n * 2048 + k * 1024); } while (0)
; #define PG8_MMA(ai, bj, At, Bt) do { __builtin_amdgcn_s_setprio(1); _Pragma("unroll") for (int m = 0; m < 4; ++m) _Pragma("unroll") for (int n = 0; n < 2; ++n) _Pragma("unroll") for (int k = 0; k < 2; ++k) \
;         acc[ai][bj][m][n] = __builtin_amdgcn_mfma_f32_16x16x32_bf16(Bt[n][k], At[m][k], acc[ai][bj][m][n], 0, 0, 0); __builtin_amdgcn_s_setprio(0); } while (0)
; #define PG8_WAIT_V(n) asm volatile("s_waitcnt vmcnt(" #n ")" ::: "memory")
; #define PG8_WAIT_L(n) asm volatile("s_waitcnt lgkmcnt(" #n ")" ::: "memory")
; #define PG8_BAR __builtin_amdgcn_s_barrier()
; #define PG8_SCHED __builtin_amdgcn_sched_barrier(0)
; #define PG8_STAGE(bufoff, gbase, voff) do { _Pragma("unroll") for (int _i = 0; _i < 2; ++_i) \
;         __builtin_amdgcn_global_load_lds((const unsigned*)((const char*)(gbase) + (voff)[_i]), (LAS unsigned*)(lds + (bufoff) + ldsw + _i * 8192), 16, 0, 0); } while (0)
; #define PG8_WAIT_V(n) asm volatile("s_waitcnt vmcnt(" #n ")" ::: "memory")
; #define PG8_WAIT_L(n) asm volatile("s_waitcnt lgkmcnt(" #n ")" ::: "memory")
;     ...
;             PG8_LDB(B0, 1, 0); PG8_LDB(B1, 1, 1); PG8_SCHED; PG8_LDA(At, 1, 0); PG8_STAGE(PG8_SA(0, 1), a2 + hstepA, voffA);
;             PG8_WAIT_V(8); PG8_WAIT_L(0); PG8_BAR; PG8_MMA(0, 0, At, B0); PG8_MMA(0, 1, At, B1); PG8_BAR; PG8_SCHED;
;             PG8_LDA(At, 1, 1); PG8_STAGE(PG8_SB(1, 0), b3, voffB); PG8_STAGE(PG8_SB(1, 1), b3 + hstepB, voffB); PG8_STAGE(PG8_SA(1, 0), a3, voffA);
;             PG8_WAIT_V(8); PG8_WAIT_L(0); PG8_BAR; PG8_MMA(1, 0, At, B0); PG8_MMA(1, 1, At, B1); PG8_BAR; PG8_SCHED;
;         }
;         asm volatile("s_nop 15\n\ts_nop 15" ::: "memory");
;         if (wr == 0) PG8_BAR;
	ds_read_b128 v[130:133], v191
	ds_read_b128 v[134:137], v192
	ds_read_b128 v[138:141], v199
	ds_read_b128 v[142:145], v200
	ds_read_b128 v[146:149], v193
	ds_read_b128 v[150:153], v194
	ds_read_b128 v[154:157], v201
	ds_read_b128 v[158:161], v202
	s_add_u32 s8, s88, 0x40000
	s_addc_u32 s9, s89, 0
	s_mov_b32 m0, s33
	v_lshl_add_u64 v[238:239], s[8:9], 0, v[168:169]
	ds_read_b128 v[206:209], v204 offset:32768
	ds_read_b128 v[210:213], v204 offset:34816
	ds_read_b128 v[214:217], v205 offset:32768
	ds_read_b128 v[218:221], v205 offset:34816
	ds_read_b128 v[222:225], v204 offset:36864
	ds_read_b128 v[226:229], v204 offset:38912
	ds_read_b128 v[230:233], v205 offset:36864
	ds_read_b128 v[234:237], v205 offset:38912
	global_load_lds_dwordx4 v[238:239], off
	v_lshl_add_u64 v[238:239], s[8:9], 0, v[164:165]
	s_mov_b32 m0, s43
	s_nop 0
	global_load_lds_dwordx4 v[238:239], off
	s_waitcnt vmcnt(8)
	s_waitcnt lgkmcnt(0)
	s_barrier
	s_setprio 1
	v_mfma_i32_16x16x64_i8 v[126:129], v[130:133], v[206:209], v[126:129]
	v_mfma_i32_16x16x64_i8 v[122:125], v[138:141], v[206:209], v[122:125]
	v_mfma_i32_16x16x64_i8 v[118:121], v[130:133], v[210:213], v[118:121]
	v_mfma_i32_16x16x64_i8 v[114:117], v[138:141], v[210:213], v[114:117]
	v_mfma_i32_16x16x64_i8 v[110:113], v[130:133], v[222:225], v[110:113]
	v_mfma_i32_16x16x64_i8 v[106:109], v[138:141], v[222:225], v[106:109]
	v_mfma_i32_16x16x64_i8 v[102:105], v[130:133], v[226:229], v[102:105]
	v_mfma_i32_16x16x64_i8 v[98:101], v[138:141], v[226:229], v[98:101]
	s_nop 0
	v_mfma_i32_16x16x64_i8 v[126:129], v[134:137], v[214:217], v[126:129]
	v_mfma_i32_16x16x64_i8 v[122:125], v[142:145], v[214:217], v[122:125]
	v_mfma_i32_16x16x64_i8 v[118:121], v[134:137], v[218:221], v[118:121]
	v_mfma_i32_16x16x64_i8 v[114:117], v[142:145], v[218:221], v[114:117]
	v_mfma_i32_16x16x64_i8 v[110:113], v[134:137], v[230:233], v[110:113]
	v_mfma_i32_16x16x64_i8 v[106:109], v[142:145], v[230:233], v[106:109]
	v_mfma_i32_16x16x64_i8 v[102:105], v[134:137], v[234:237], v[102:105]
	v_mfma_i32_16x16x64_i8 v[98:101], v[142:145], v[234:237], v[98:101]
	s_setprio 0
	s_setprio 1
	v_mfma_i32_16x16x64_i8 v[94:97], v[146:149], v[206:209], v[94:97]
	v_mfma_i32_16x16x64_i8 v[90:93], v[154:157], v[206:209], v[90:93]
	v_mfma_i32_16x16x64_i8 v[86:89], v[146:149], v[210:213], v[86:89]
	v_mfma_i32_16x16x64_i8 v[82:85], v[154:157], v[210:213], v[82:85]
	v_mfma_i32_16x16x64_i8 v[78:81], v[146:149], v[222:225], v[78:81]
	v_mfma_i32_16x16x64_i8 v[74:77], v[154:157], v[222:225], v[74:77]
	v_mfma_i32_16x16x64_i8 v[70:73], v[146:149], v[226:229], v[70:73]
	v_mfma_i32_16x16x64_i8 v[66:69], v[154:157], v[226:229], v[66:69]
	s_nop 0
	v_mfma_i32_16x16x64_i8 v[94:97], v[150:153], v[214:217], v[94:97]
	v_mfma_i32_16x16x64_i8 v[90:93], v[158:161], v[214:217], v[90:93]
	v_mfma_i32_16x16x64_i8 v[86:89], v[150:153], v[218:221], v[86:89]
	v_mfma_i32_16x16x64_i8 v[82:85], v[158:161], v[218:221], v[82:85]
	v_mfma_i32_16x16x64_i8 v[78:81], v[150:153], v[230:233], v[78:81]
	v_mfma_i32_16x16x64_i8 v[74:77], v[158:161], v[230:233], v[74:77]
	v_mfma_i32_16x16x64_i8 v[70:73], v[150:153], v[234:237], v[70:73]
	v_mfma_i32_16x16x64_i8 v[66:69], v[158:161], v[234:237], v[66:69]
	s_setprio 0
	s_barrier
	s_mov_b32 m0, s78
	v_lshl_add_u64 v[178:179], v[178:179], 0, s[22:23]
	s_add_u32 s8, s86, 0x40080
	ds_read_b128 v[206:209], v204 offset:49152
	ds_read_b128 v[210:213], v204 offset:51200
	ds_read_b128 v[214:217], v205 offset:49152
	ds_read_b128 v[218:221], v205 offset:51200
	ds_read_b128 v[222:225], v204 offset:53248
	ds_read_b128 v[226:229], v204 offset:55296
	ds_read_b128 v[230:233], v205 offset:53248
	ds_read_b128 v[234:237], v205 offset:55296
	global_load_lds_dwordx4 v[178:179], off
	v_lshl_add_u64 v[178:179], v[180:181], 0, s[22:23]
	s_mov_b32 m0, s79
	s_addc_u32 s9, s87, 0
	global_load_lds_dwordx4 v[178:179], off
	v_lshl_add_u64 v[178:179], s[8:9], 0, v[166:167]
	s_mov_b32 m0, s90
	s_nop 0
	global_load_lds_dwordx4 v[178:179], off
	v_lshl_add_u64 v[178:179], s[8:9], 0, v[162:163]
	s_mov_b32 m0, s91
	s_nop 0
	global_load_lds_dwordx4 v[178:179], off
	v_lshl_add_u64 v[178:179], v[182:183], 0, s[22:23]
	s_mov_b32 m0, s80
	s_nop 0
	global_load_lds_dwordx4 v[178:179], off
	v_lshl_add_u64 v[178:179], v[184:185], 0, s[22:23]
	s_mov_b32 m0, s81
	s_nop 0
	global_load_lds_dwordx4 v[178:179], off
	s_waitcnt vmcnt(8)
	s_waitcnt lgkmcnt(0)
	s_barrier
	s_setprio 1
	v_mfma_i32_16x16x64_i8 v[62:65], v[130:133], v[206:209], v[62:65]
	v_mfma_i32_16x16x64_i8 v[58:61], v[138:141], v[206:209], v[58:61]
	v_mfma_i32_16x16x64_i8 v[54:57], v[130:133], v[210:213], v[54:57]
	v_mfma_i32_16x16x64_i8 v[50:53], v[138:141], v[210:213], v[50:53]
	v_mfma_i32_16x16x64_i8 v[46:49], v[130:133], v[222:225], v[46:49]
	v_mfma_i32_16x16x64_i8 v[42:45], v[138:141], v[222:225], v[42:45]
	v_mfma_i32_16x16x64_i8 v[38:41], v[130:133], v[226:229], v[38:41]
	v_mfma_i32_16x16x64_i8 v[34:37], v[138:141], v[226:229], v[34:37]
	s_nop 0
	v_mfma_i32_16x16x64_i8 v[62:65], v[134:137], v[214:217], v[62:65]
	v_mfma_i32_16x16x64_i8 v[58:61], v[142:145], v[214:217], v[58:61]
	v_mfma_i32_16x16x64_i8 v[54:57], v[134:137], v[218:221], v[54:57]
	v_mfma_i32_16x16x64_i8 v[50:53], v[142:145], v[218:221], v[50:53]
	v_mfma_i32_16x16x64_i8 v[46:49], v[134:137], v[230:233], v[46:49]
	v_mfma_i32_16x16x64_i8 v[42:45], v[142:145], v[230:233], v[42:45]
	v_mfma_i32_16x16x64_i8 v[38:41], v[134:137], v[234:237], v[38:41]
	v_mfma_i32_16x16x64_i8 v[34:37], v[142:145], v[234:237], v[34:37]
	s_setprio 0
	s_setprio 1
	v_mfma_i32_16x16x64_i8 v[30:33], v[146:149], v[206:209], v[30:33]
	v_mfma_i32_16x16x64_i8 v[26:29], v[154:157], v[206:209], v[26:29]
	v_mfma_i32_16x16x64_i8 v[22:25], v[146:149], v[210:213], v[22:25]
	v_mfma_i32_16x16x64_i8 v[18:21], v[154:157], v[210:213], v[18:21]
	v_mfma_i32_16x16x64_i8 v[14:17], v[146:149], v[222:225], v[14:17]
	v_mfma_i32_16x16x64_i8 v[10:13], v[154:157], v[222:225], v[10:13]
	v_mfma_i32_16x16x64_i8 v[6:9], v[146:149], v[226:229], v[6:9]
	v_mfma_i32_16x16x64_i8 v[2:5], v[154:157], v[226:229], v[2:5]
	s_nop 0
	v_mfma_i32_16x16x64_i8 v[30:33], v[150:153], v[214:217], v[30:33]
	v_mfma_i32_16x16x64_i8 v[26:29], v[158:161], v[214:217], v[26:29]
	v_mfma_i32_16x16x64_i8 v[22:25], v[150:153], v[218:221], v[22:25]
	v_mfma_i32_16x16x64_i8 v[18:21], v[158:161], v[218:221], v[18:21]
	s_add_i32 vcc_lo, vcc_lo, 2
	s_add_u32 s94, s94, 0x100
	s_addc_u32 s95, s95, 0
	s_cmp_gt_u32 vcc_lo, 13
	s_mov_b64 s[82:83], s[84:85]
	v_mfma_i32_16x16x64_i8 v[14:17], v[150:153], v[230:233], v[14:17]
	v_mfma_i32_16x16x64_i8 v[10:13], v[158:161], v[230:233], v[10:13]
	v_mfma_i32_16x16x64_i8 v[6:9], v[150:153], v[234:237], v[6:9]
	v_mfma_i32_16x16x64_i8 v[2:5], v[158:161], v[234:237], v[2:5]
	s_setprio 0
	s_barrier
	s_cbranch_scc0 .LBB0_143
	s_nop 15
	s_nop 15
	s_and_b64 vcc, exec, s[38:39]
	s_cbranch_vccz .LBB0_146
	s_barrier

; #define PG8_STAGE(bufoff, gbase, voff) do { _Pragma("unroll") for (int _i = 0; _i < 2; ++_i) \
;         __builtin_amdgcn_global_load_lds((const unsigned*)((const char*)(gbase) + (voff)[_i]), (LAS unsigned*)(lds + (bufoff) + ldsw + _i * 8192), 16, 0, 0); } while (0)
; #define PG8_LDA(dst, b, h) do { _Pragma("unroll") for (int m = 0; m < 4; ++m) _Pragma("unroll") for (int k = 0; k < 2; ++k) dst[m][k] = *(const LAS bf16x8*)(lds + PG8_SA(b, h) + aoff + m * 2048 + k * 1024); } while (0)
; #define PG8_LDB(dst, b, h) do { _Pragma("unroll") for (int n = 0; n < 2; ++n) _Pragma("unroll") for (int k = 0; k < 2; ++k) dst[n][k] = *(const LAS bf16x8*)(lds + PG8_SB(b, h) + boff + n * 2048 + k * 1024); } while (0)
; #define PG8_MMA(ai, bj, At, Bt) do { __builtin_amdgcn_s_setprio(1); _Pragma("unroll") for (int m = 0; m < 4; ++m) _Pragma("unroll") for (int n = 0; n < 2; ++n) _Pragma("unroll") for (int k = 0; k < 2; ++k) \
;         acc[ai][bj][m][n] = __builtin_amdgcn_mfma_f32_16x16x32_bf16(Bt[n][k], At[m][k], acc[ai][bj][m][n], 0, 0, 0); __builtin_amdgcn_s_setprio(0); } while (0)
; #define PG8_WAIT_V(n) asm volatile("s_waitcnt vmcnt(" #n ")" ::: "memory")
; #define PG8_WAIT_L(n) asm volatile("s_waitcnt lgkmcnt(" #n ")" ::: "memory")
; #define PG8_BAR __builtin_amdgcn_s_barrier()
; template <class Epi, class Sched>
; __device__ __forceinline__ void gemm_phase(LAS unsigned char* lds, const Gemm g, const Sched& S, const Epi& E) {
;     ...
;         for (int t = 0; t < nt; t += 2) {
;             const bool last = (t == nt - 2);
;             const char* a1 = cA + (size_t)(t + 1) * kstep;
;             const char* a2 = last ? nA : cA + (size_t)(t + 2) * kstep; const char* b2 = last ? nB : cB + (size_t)(t + 2) * kstep;
;             const char* a3 = a2 + kstep; const char* b3 = b2 + kstep;
;             if (last && has_next) S.a_ready(nxt);
;             PG8_LDB(B0, 0, 0); PG8_LDB(B1, 0, 1); PG8_SCHED; PG8_LDA(At, 0, 0); PG8_STAGE(PG8_SA(1, 1), a1 + hstepA, voffA);
;             PG8_WAIT_V(8); PG8_WAIT_L(0); PG8_BAR; PG8_MMA(0, 0, At, B0); PG8_MMA(0, 1, At, B1); PG8_BAR; PG8_SCHED;
;             PG8_LDA(At, 0, 1); PG8_STAGE(PG8_SB(0, 0), b2, voffB); PG8_STAGE(PG8_SB(0, 1), b2 + hstepB, voffB); PG8_STAGE(PG8_SA(0, 0), a2, voffA);
;             PG8_WAIT_V(8); PG8_WAIT_L(0); PG8_BAR; PG8_MMA(1, 0, At, B0); PG8_MMA(1, 1, At, B1); PG8_BAR; PG8_SCHED;
.LBB0_273:
	s_add_u32 s12, s82, s88
	s_addc_u32 s13, s83, s89
	s_add_u32 s18, s12, 0x100
	s_addc_u32 s19, s13, 0
	s_and_b64 s[8:9], s[86:87], exec
	s_cselect_b32 s91, s47, s19
	s_cselect_b32 s90, s51, s18
	s_add_u32 s8, s64, s88
	s_addc_u32 s9, s65, s89
	s_add_u32 s18, s8, 0x100
	s_addc_u32 s19, s9, 0
	s_and_b64 s[8:9], s[86:87], exec
	s_cselect_b32 s93, s73, s19
	s_cselect_b32 s92, s74, s18
	s_add_u32 s96, s12, 0x80080
	ds_read_b128 v[126:129], v199
	ds_read_b128 v[146:149], v199 offset:1024
	ds_read_b128 v[150:153], v199 offset:2048
	ds_read_b128 v[154:157], v199 offset:3072
	ds_read_b128 v[158:161], v200
	ds_read_b128 v[162:165], v200 offset:1024
	ds_read_b128 v[166:169], v200 offset:2048
	ds_read_b128 v[170:173], v200 offset:3072
	s_addc_u32 s97, s13, 0
	s_add_i32 s21, s33, s24
	s_add_i32 m0, s40, 0xc000
	s_add_i32 s11, s40, 0xe000
	s_add_i32 s18, s21, 0x2000
	s_add_u32 s94, s92, 0x10000
	s_addc_u32 s95, s93, 0
	s_add_i32 s20, s1, s24
	s_add_i32 s19, s20, 0x2000
	s_add_i32 s13, 0, 0x18000
	s_add_i32 s12, 0, 0x1c000
	s_add_u32 s88, s90, 0x80000
	s_addc_u32 s89, s91, 0
	s_add_i32 s9, s13, s24
	s_add_i32 vcc_hi, s9, 0x2000
	s_add_u32 s86, s92, 0x10080
	s_addc_u32 s87, s93, 0
	s_add_i32 vcc_lo, s12, s24
	s_add_i32 s8, vcc_lo, 0x2000
	v_lshl_add_u64 v[194:195], s[96:97], 0, v[140:141]
	ds_read_b128 v[174:177], v201
	ds_read_b128 v[178:181], v201 offset:1024
	ds_read_b128 v[182:185], v201 offset:2048
	ds_read_b128 v[186:189], v201 offset:3072
	ds_read_b128 v[190:193], v201 offset:4096
	ds_read_b128 v[202:205], v201 offset:5120
	ds_read_b128 v[206:209], v201 offset:6144
	ds_read_b128 v[210:213], v201 offset:7168
	global_load_lds_dwordx4 v[194:195], off
	v_lshl_add_u64 v[194:195], s[96:97], 0, v[136:137]
	s_mov_b32 m0, s11
	s_nop 0
	global_load_lds_dwordx4 v[194:195], off
	s_waitcnt vmcnt(8)
	s_waitcnt lgkmcnt(0)
	s_barrier
	s_setprio 1
	v_mfma_f32_16x16x32_bf16 v[130:133], v[126:129], v[174:177], v[130:133]
	v_mfma_f32_16x16x32_bf16 v[62:65], v[150:153], v[174:177], v[62:65]
	v_mfma_f32_16x16x32_bf16 v[118:121], v[126:129], v[182:185], v[118:121]
	v_mfma_f32_16x16x32_bf16 v[54:57], v[150:153], v[182:185], v[54:57]
	v_mfma_f32_16x16x32_bf16 v[110:113], v[126:129], v[190:193], v[110:113]
	v_mfma_f32_16x16x32_bf16 v[46:49], v[150:153], v[190:193], v[46:49]
	v_mfma_f32_16x16x32_bf16 v[102:105], v[126:129], v[206:209], v[102:105]
	v_mfma_f32_16x16x32_bf16 v[38:41], v[150:153], v[206:209], v[38:41]
	v_mfma_f32_16x16x32_bf16 v[130:133], v[146:149], v[178:181], v[130:133]
	v_mfma_f32_16x16x32_bf16 v[62:65], v[154:157], v[178:181], v[62:65]
	v_mfma_f32_16x16x32_bf16 v[118:121], v[146:149], v[186:189], v[118:121]
	v_mfma_f32_16x16x32_bf16 v[54:57], v[154:157], v[186:189], v[54:57]
	v_mfma_f32_16x16x32_bf16 v[110:113], v[146:149], v[202:205], v[110:113]
	v_mfma_f32_16x16x32_bf16 v[46:49], v[154:157], v[202:205], v[46:49]
	v_mfma_f32_16x16x32_bf16 v[102:105], v[146:149], v[210:213], v[102:105]
	v_mfma_f32_16x16x32_bf16 v[38:41], v[154:157], v[210:213], v[38:41]
	s_setprio 0
	s_setprio 1
	v_mfma_f32_16x16x32_bf16 v[122:125], v[158:161], v[174:177], v[122:125]
	v_mfma_f32_16x16x32_bf16 v[58:61], v[166:169], v[174:177], v[58:61]
	v_mfma_f32_16x16x32_bf16 v[114:117], v[158:161], v[182:185], v[114:117]
	v_mfma_f32_16x16x32_bf16 v[50:53], v[166:169], v[182:185], v[50:53]
	v_mfma_f32_16x16x32_bf16 v[106:109], v[158:161], v[190:193], v[106:109]
	v_mfma_f32_16x16x32_bf16 v[42:45], v[166:169], v[190:193], v[42:45]
	v_mfma_f32_16x16x32_bf16 v[98:101], v[158:161], v[206:209], v[98:101]
	v_mfma_f32_16x16x32_bf16 v[34:37], v[166:169], v[206:209], v[34:37]
	v_mfma_f32_16x16x32_bf16 v[122:125], v[162:165], v[178:181], v[122:125]
	v_mfma_f32_16x16x32_bf16 v[58:61], v[170:173], v[178:181], v[58:61]
	v_mfma_f32_16x16x32_bf16 v[114:117], v[162:165], v[186:189], v[114:117]
	v_mfma_f32_16x16x32_bf16 v[50:53], v[170:173], v[186:189], v[50:53]
	v_mfma_f32_16x16x32_bf16 v[106:109], v[162:165], v[202:205], v[106:109]
	v_mfma_f32_16x16x32_bf16 v[42:45], v[170:173], v[202:205], v[42:45]
	v_mfma_f32_16x16x32_bf16 v[98:101], v[162:165], v[210:213], v[98:101]
	v_mfma_f32_16x16x32_bf16 v[34:37], v[170:173], v[210:213], v[34:37]
	s_setprio 0
	s_barrier
	s_mov_b32 m0, s21
	v_lshl_add_u64 v[194:195], s[92:93], 0, v[138:139]
	ds_read_b128 v[174:177], v201 offset:16384
	ds_read_b128 v[178:181], v201 offset:17408
	ds_read_b128 v[182:185], v201 offset:18432
	ds_read_b128 v[186:189], v201 offset:19456
	ds_read_b128 v[190:193], v201 offset:20480
	ds_read_b128 v[202:205], v201 offset:21504
	ds_read_b128 v[206:209], v201 offset:22528
	ds_read_b128 v[210:213], v201 offset:23552
	global_load_lds_dwordx4 v[194:195], off
	v_lshl_add_u64 v[214:215], s[92:93], 0, v[134:135]
	s_mov_b32 m0, s18
	v_lshl_add_u64 v[216:217], s[94:95], 0, v[138:139]
	global_load_lds_dwordx4 v[214:215], off
	s_mov_b32 m0, s20
	v_lshl_add_u64 v[218:219], s[90:91], 0, v[136:137]
	global_load_lds_dwordx4 v[216:217], off
	v_lshl_add_u64 v[216:217], s[94:95], 0, v[134:135]
	s_mov_b32 m0, s19
	s_nop 0
	global_load_lds_dwordx4 v[216:217], off
	v_lshl_add_u64 v[216:217], s[90:91], 0, v[140:141]
	s_mov_b32 m0, s40
	s_nop 0
	global_load_lds_dwordx4 v[216:217], off
	s_mov_b32 m0, s41
	s_nop 0
	global_load_lds_dwordx4 v[218:219], off
	s_waitcnt vmcnt(8)
	s_waitcnt lgkmcnt(0)
	s_barrier
; #define PG8_STAGE(bufoff, gbase, voff) do { _Pragma("unroll") for (int _i = 0; _i < 2; ++_i) \
;         __builtin_amdgcn_global_load_lds((const unsigned*)((const char*)(gbase) + (voff)[_i]), (LAS unsigned*)(lds + (bufoff) + ldsw + _i * 8192), 16, 0, 0); } while (0)
; #define PG8_LDA(dst, b, h) do { _Pragma("unroll") for (int m = 0; m < 4; ++m) _Pragma("unroll") for (int k = 0; k < 2; ++k) dst[m][k] = *(const LAS bf16x8*)(lds + PG8_SA(b, h) + aoff + m * 2048 + k * 1024); } while (0)
; #define PG8_LDB(dst, b, h) do { _Pragma("unroll") for (int n = 0; n < 2; ++n) _Pragma("unroll") for (int k = 0; k < 2; ++k) dst[n][k] = *(const LAS bf16x8*)(lds + PG8_SB(b, h) + boff + n * 2048 + k * 1024); } while (0)
; #define PG8_MMA(ai, bj, At, Bt) do { __builtin_amdgcn_s_setprio(1); _Pragma("unroll") for (int m = 0; m < 4; ++m) _Pragma("unroll") for (int n = 0; n < 2; ++n) _Pragma("unroll") for (int k = 0; k < 2; ++k) \
;         acc[ai][bj][m][n] = __builtin_amdgcn_mfma_f32_16x16x32_bf16(Bt[n][k], At[m][k], acc[ai][bj][m][n], 0, 0, 0); __builtin_amdgcn_s_setprio(0); } while (0)
; #define PG8_WAIT_V(n) asm volatile("s_waitcnt vmcnt(" #n ")" ::: "memory")
; #define PG8_WAIT_L(n) asm volatile("s_waitcnt lgkmcnt(" #n ")" ::: "memory")
; #define PG8_BAR __builtin_amdgcn_s_barrier()
; #define PG8_SCHED __builtin_amdgcn_sched_barrier(0)
; #define PG8_STAGE(bufoff, gbase, voff) do { _Pragma("unroll") for (int _i = 0; _i < 2; ++_i) \
;         __builtin_amdgcn_global_load_lds((const unsigned*)((const char*)(gbase) + (voff)[_i]), (LAS unsigned*)(lds + (bufoff) + ldsw + _i * 8192), 16, 0, 0); } while (0)
; #define PG8_LDA(dst, b, h) do { _Pragma("unroll") for (int m = 0; m < 4; ++m) PG8_LD1(dst[m], PG8_SA(b, h) + aoff0 + m * 2048, PG8_SA(b, h) + aoff1 + m * 2048); } while (0)
; #define PG8_WAIT_V(n) asm volatile("s_waitcnt vmcnt(" #n ")" ::: "memory")
; template <class Epi, class Sched>
; __device__ __forceinline__ void gemm_phase(LAS unsigned char* lds, const Gemm g, const Sched& S, const Epi& E) {
;     ...
;             PG8_WAIT_V(8); PG8_WAIT_L(0); PG8_BAR; PG8_MMA(1, 0, At, B0); PG8_MMA(1, 1, At, B1); PG8_BAR; PG8_SCHED;
;             PG8_LDB(B0, 1, 0); PG8_LDB(B1, 1, 1); PG8_SCHED; PG8_LDA(At, 1, 0); PG8_STAGE(PG8_SA(0, 1), a2 + hstepA, voffA);
;             PG8_WAIT_V(8); PG8_WAIT_L(0); PG8_BAR; PG8_MMA(0, 0, At, B0); PG8_MMA(0, 1, At, B1); PG8_BAR; PG8_SCHED;
	s_setprio 1
	v_mfma_f32_16x16x32_bf16 v[94:97], v[126:129], v[174:177], v[94:97]
	v_mfma_f32_16x16x32_bf16 v[30:33], v[150:153], v[174:177], v[30:33]
	v_mfma_f32_16x16x32_bf16 v[86:89], v[126:129], v[182:185], v[86:89]
	v_mfma_f32_16x16x32_bf16 v[22:25], v[150:153], v[182:185], v[22:25]
	v_mfma_f32_16x16x32_bf16 v[78:81], v[126:129], v[190:193], v[78:81]
	v_mfma_f32_16x16x32_bf16 v[14:17], v[150:153], v[190:193], v[14:17]
	v_mfma_f32_16x16x32_bf16 v[70:73], v[126:129], v[206:209], v[70:73]
	v_mfma_f32_16x16x32_bf16 v[6:9], v[150:153], v[206:209], v[6:9]
	v_mfma_f32_16x16x32_bf16 v[94:97], v[146:149], v[178:181], v[94:97]
	v_mfma_f32_16x16x32_bf16 v[30:33], v[154:157], v[178:181], v[30:33]
	v_mfma_f32_16x16x32_bf16 v[86:89], v[146:149], v[186:189], v[86:89]
	v_mfma_f32_16x16x32_bf16 v[22:25], v[154:157], v[186:189], v[22:25]
	v_mfma_f32_16x16x32_bf16 v[78:81], v[146:149], v[202:205], v[78:81]
	v_mfma_f32_16x16x32_bf16 v[14:17], v[154:157], v[202:205], v[14:17]
	v_mfma_f32_16x16x32_bf16 v[70:73], v[146:149], v[210:213], v[70:73]
	v_mfma_f32_16x16x32_bf16 v[6:9], v[154:157], v[210:213], v[6:9]
	s_setprio 0
	s_setprio 1
	v_mfma_f32_16x16x32_bf16 v[90:93], v[158:161], v[174:177], v[90:93]
	v_mfma_f32_16x16x32_bf16 v[26:29], v[166:169], v[174:177], v[26:29]
	v_mfma_f32_16x16x32_bf16 v[82:85], v[158:161], v[182:185], v[82:85]
	v_mfma_f32_16x16x32_bf16 v[18:21], v[166:169], v[182:185], v[18:21]
	v_mfma_f32_16x16x32_bf16 v[74:77], v[158:161], v[190:193], v[74:77]
	v_mfma_f32_16x16x32_bf16 v[10:13], v[166:169], v[190:193], v[10:13]
	v_mfma_f32_16x16x32_bf16 v[66:69], v[158:161], v[206:209], v[66:69]
	v_mfma_f32_16x16x32_bf16 v[2:5], v[166:169], v[206:209], v[2:5]
	v_mfma_f32_16x16x32_bf16 v[90:93], v[162:165], v[178:181], v[90:93]
	v_mfma_f32_16x16x32_bf16 v[26:29], v[170:173], v[178:181], v[26:29]
	v_mfma_f32_16x16x32_bf16 v[82:85], v[162:165], v[186:189], v[82:85]
	v_mfma_f32_16x16x32_bf16 v[18:21], v[170:173], v[186:189], v[18:21]
	v_mfma_f32_16x16x32_bf16 v[74:77], v[162:165], v[202:205], v[74:77]
	v_mfma_f32_16x16x32_bf16 v[10:13], v[170:173], v[202:205], v[10:13]
	v_mfma_f32_16x16x32_bf16 v[66:69], v[162:165], v[210:213], v[66:69]
	v_mfma_f32_16x16x32_bf16 v[2:5], v[170:173], v[210:213], v[2:5]
	s_setprio 0
	s_barrier
	v_add_u32_e32 v154, s13, v197
	v_add_u32_e32 v170, s12, v197
	ds_read_b128 v[126:129], v154
	ds_read_b128 v[146:149], v154 offset:1024
	ds_read_b128 v[150:153], v154 offset:2048
	ds_read_b128 v[154:157], v154 offset:3072
	ds_read_b128 v[158:161], v170
	ds_read_b128 v[162:165], v170 offset:1024
	ds_read_b128 v[166:169], v170 offset:2048
	ds_read_b128 v[170:173], v170 offset:3072
	s_mov_b32 m0, s0
	v_lshl_add_u64 v[220:221], s[88:89], 0, v[140:141]
	ds_read_b128 v[174:177], v201 offset:32768
	ds_read_b128 v[178:181], v201 offset:33792
	ds_read_b128 v[182:185], v201 offset:34816
	ds_read_b128 v[186:189], v201 offset:35840
	ds_read_b128 v[190:193], v201 offset:36864
	ds_read_b128 v[202:205], v201 offset:37888
	ds_read_b128 v[206:209], v201 offset:38912
	ds_read_b128 v[210:213], v201 offset:39936
	global_load_lds_dwordx4 v[220:221], off
	v_lshl_add_u64 v[220:221], s[88:89], 0, v[136:137]
	s_mov_b32 m0, s79
	s_nop 0
	global_load_lds_dwordx4 v[220:221], off
	s_waitcnt vmcnt(8)
	s_waitcnt lgkmcnt(0)
	s_barrier
	s_setprio 1
	v_mfma_f32_16x16x32_bf16 v[130:133], v[126:129], v[174:177], v[130:133]
	v_mfma_f32_16x16x32_bf16 v[62:65], v[150:153], v[174:177], v[62:65]
	v_mfma_f32_16x16x32_bf16 v[118:121], v[126:129], v[182:185], v[118:121]
	v_mfma_f32_16x16x32_bf16 v[54:57], v[150:153], v[182:185], v[54:57]
	v_mfma_f32_16x16x32_bf16 v[110:113], v[126:129], v[190:193], v[110:113]
	v_mfma_f32_16x16x32_bf16 v[46:49], v[150:153], v[190:193], v[46:49]
	v_mfma_f32_16x16x32_bf16 v[102:105], v[126:129], v[206:209], v[102:105]
	v_mfma_f32_16x16x32_bf16 v[38:41], v[150:153], v[206:209], v[38:41]
	v_mfma_f32_16x16x32_bf16 v[130:133], v[146:149], v[178:181], v[130:133]
	v_mfma_f32_16x16x32_bf16 v[62:65], v[154:157], v[178:181], v[62:65]
	v_mfma_f32_16x16x32_bf16 v[118:121], v[146:149], v[186:189], v[118:121]
	v_mfma_f32_16x16x32_bf16 v[54:57], v[154:157], v[186:189], v[54:57]
	v_mfma_f32_16x16x32_bf16 v[110:113], v[146:149], v[202:205], v[110:113]
	v_mfma_f32_16x16x32_bf16 v[46:49], v[154:157], v[202:205], v[46:49]
	v_mfma_f32_16x16x32_bf16 v[102:105], v[146:149], v[210:213], v[102:105]
	v_mfma_f32_16x16x32_bf16 v[38:41], v[154:157], v[210:213], v[38:41]
	s_setprio 0
	s_setprio 1
	v_mfma_f32_16x16x32_bf16 v[122:125], v[158:161], v[174:177], v[122:125]
	v_mfma_f32_16x16x32_bf16 v[58:61], v[166:169], v[174:177], v[58:61]
	v_mfma_f32_16x16x32_bf16 v[114:117], v[158:161], v[182:185], v[114:117]
	v_mfma_f32_16x16x32_bf16 v[50:53], v[166:169], v[182:185], v[50:53]
	v_mfma_f32_16x16x32_bf16 v[106:109], v[158:161], v[190:193], v[106:109]
	v_mfma_f32_16x16x32_bf16 v[42:45], v[166:169], v[190:193], v[42:45]
	v_mfma_f32_16x16x32_bf16 v[98:101], v[158:161], v[206:209], v[98:101]
	v_mfma_f32_16x16x32_bf16 v[34:37], v[166:169], v[206:209], v[34:37]
	v_mfma_f32_16x16x32_bf16 v[122:125], v[162:165], v[178:181], v[122:125]
	v_mfma_f32_16x16x32_bf16 v[58:61], v[170:173], v[178:181], v[58:61]
	v_mfma_f32_16x16x32_bf16 v[114:117], v[162:165], v[186:189], v[114:117]
	v_mfma_f32_16x16x32_bf16 v[50:53], v[170:173], v[186:189], v[50:53]
	v_mfma_f32_16x16x32_bf16 v[106:109], v[162:165], v[202:205], v[106:109]
	v_mfma_f32_16x16x32_bf16 v[42:45], v[170:173], v[202:205], v[42:45]
	v_mfma_f32_16x16x32_bf16 v[98:101], v[162:165], v[210:213], v[98:101]
	v_mfma_f32_16x16x32_bf16 v[34:37], v[170:173], v[210:213], v[34:37]
	s_setprio 0
	s_barrier
; #define PG8_STAGE(bufoff, gbase, voff) do { _Pragma("unroll") for (int _i = 0; _i < 2; ++_i) \
;         __builtin_amdgcn_global_load_lds((const unsigned*)((const char*)(gbase) + (voff)[_i]), (LAS unsigned*)(lds + (bufoff) + ldsw + _i * 8192), 16, 0, 0); } while (0)
; #define PG8_LDA(dst, b, h) do { _Pragma("unroll") for (int m = 0; m < 4; ++m) _Pragma("unroll") for (int k = 0; k < 2; ++k) dst[m][k] = *(const LAS bf16x8*)(lds + PG8_SA(b, h) + aoff + m * 2048 + k * 1024); } while (0)
; #define PG8_MMA(ai, bj, At, Bt) do { __builtin_amdgcn_s_setprio(1); _Pragma("unroll") for (int m = 0; m < 4; ++m) _Pragma("unroll") for (int n = 0; n < 2; ++n) _Pragma("unroll") for (int k = 0; k < 2; ++k) \
;         acc[ai][bj][m][n] = __builtin_amdgcn_mfma_f32_16x16x32_bf16(Bt[n][k], At[m][k], acc[ai][bj][m][n], 0, 0, 0); __builtin_amdgcn_s_setprio(0); } while (0)
; #define PG8_WAIT_V(n) asm volatile("s_waitcnt vmcnt(" #n ")" ::: "memory")
; #define PG8_WAIT_L(n) asm volatile("s_waitcnt lgkmcnt(" #n ")" ::: "memory")
; #define PG8_BAR __builtin_amdgcn_s_barrier()
; #define PG8_SCHED __builtin_amdgcn_sched_barrier(0)
; #define PG8_STAGE(bufoff, gbase, voff) do { _Pragma("unroll") for (int _i = 0; _i < 2; ++_i) \
;         __builtin_amdgcn_global_load_lds((const unsigned*)((const char*)(gbase) + (voff)[_i]), (LAS unsigned*)(lds + (bufoff) + ldsw + _i * 8192), 16, 0, 0); } while (0)
; #define PG8_LDA(dst, b, h) do { _Pragma("unroll") for (int m = 0; m < 4; ++m) PG8_LD1(dst[m], PG8_SA(b, h) + aoff0 + m * 2048, PG8_SA(b, h) + aoff1 + m * 2048); } while (0)
; #define PG8_WAIT_V(n) asm volatile("s_waitcnt vmcnt(" #n ")" ::: "memory")
; #define PG8_WAIT_L(n) asm volatile("s_waitcnt lgkmcnt(" #n ")" ::: "memory")
; #define PG8_BAR __builtin_amdgcn_s_barrier()
; #define PG8_SCHED __builtin_amdgcn_sched_barrier(0)
; template <class Epi, class Sched>
; __device__ __forceinline__ void gemm_phase(LAS unsigned char* lds, const Gemm g, const Sched& S, const Epi& E) {
;     ...
;             PG8_LDA(At, 1, 1); PG8_STAGE(PG8_SB(1, 0), b3, voffB); PG8_STAGE(PG8_SB(1, 1), b3 + hstepB, voffB); PG8_STAGE(PG8_SA(1, 0), a3, voffA);
;             PG8_WAIT_V(8); PG8_WAIT_L(0); PG8_BAR; PG8_MMA(1, 0, At, B0); PG8_MMA(1, 1, At, B1); PG8_BAR; PG8_SCHED;
;         }
;         if (wr == 0) PG8_BAR;
	s_mov_b32 m0, s9
	v_lshl_add_u64 v[194:195], v[194:195], 0, s[42:43]
	ds_read_b128 v[174:177], v201 offset:49152
	ds_read_b128 v[178:181], v201 offset:50176
	ds_read_b128 v[182:185], v201 offset:51200
	ds_read_b128 v[186:189], v201 offset:52224
	ds_read_b128 v[190:193], v201 offset:53248
	ds_read_b128 v[202:205], v201 offset:54272
	ds_read_b128 v[206:209], v201 offset:55296
	ds_read_b128 v[210:213], v201 offset:56320
	global_load_lds_dwordx4 v[194:195], off
	v_lshl_add_u64 v[194:195], v[214:215], 0, s[42:43]
	s_mov_b32 m0, vcc_hi
	s_nop 0
	global_load_lds_dwordx4 v[194:195], off
	v_lshl_add_u64 v[194:195], s[86:87], 0, v[138:139]
	s_mov_b32 m0, vcc_lo
	s_nop 0
	global_load_lds_dwordx4 v[194:195], off
	v_lshl_add_u64 v[194:195], s[86:87], 0, v[134:135]
	s_mov_b32 m0, s8
	s_nop 0
	global_load_lds_dwordx4 v[194:195], off
	v_lshl_add_u64 v[194:195], v[216:217], 0, s[42:43]
	s_mov_b32 m0, s80
	s_nop 0
	global_load_lds_dwordx4 v[194:195], off
	v_lshl_add_u64 v[194:195], v[218:219], 0, s[42:43]
	s_mov_b32 m0, s81
	s_nop 0
	global_load_lds_dwordx4 v[194:195], off
	s_waitcnt vmcnt(8)
	s_waitcnt lgkmcnt(0)
	s_barrier
	s_setprio 1
	v_mfma_f32_16x16x32_bf16 v[94:97], v[126:129], v[174:177], v[94:97]
	v_mfma_f32_16x16x32_bf16 v[30:33], v[150:153], v[174:177], v[30:33]
	v_mfma_f32_16x16x32_bf16 v[86:89], v[126:129], v[182:185], v[86:89]
	v_mfma_f32_16x16x32_bf16 v[22:25], v[150:153], v[182:185], v[22:25]
	v_mfma_f32_16x16x32_bf16 v[78:81], v[126:129], v[190:193], v[78:81]
	v_mfma_f32_16x16x32_bf16 v[14:17], v[150:153], v[190:193], v[14:17]
	v_mfma_f32_16x16x32_bf16 v[70:73], v[126:129], v[206:209], v[70:73]
	v_mfma_f32_16x16x32_bf16 v[6:9], v[150:153], v[206:209], v[6:9]
	v_mfma_f32_16x16x32_bf16 v[94:97], v[146:149], v[178:181], v[94:97]
	v_mfma_f32_16x16x32_bf16 v[30:33], v[154:157], v[178:181], v[30:33]
	v_mfma_f32_16x16x32_bf16 v[86:89], v[146:149], v[186:189], v[86:89]
	v_mfma_f32_16x16x32_bf16 v[22:25], v[154:157], v[186:189], v[22:25]
	v_mfma_f32_16x16x32_bf16 v[78:81], v[146:149], v[202:205], v[78:81]
	v_mfma_f32_16x16x32_bf16 v[14:17], v[154:157], v[202:205], v[14:17]
	v_mfma_f32_16x16x32_bf16 v[70:73], v[146:149], v[210:213], v[70:73]
	v_mfma_f32_16x16x32_bf16 v[6:9], v[154:157], v[210:213], v[6:9]
	s_setprio 0
	s_setprio 1
	v_mfma_f32_16x16x32_bf16 v[90:93], v[158:161], v[174:177], v[90:93]
	v_mfma_f32_16x16x32_bf16 v[26:29], v[166:169], v[174:177], v[26:29]
	v_mfma_f32_16x16x32_bf16 v[82:85], v[158:161], v[182:185], v[82:85]
	v_mfma_f32_16x16x32_bf16 v[18:21], v[166:169], v[182:185], v[18:21]
	v_mfma_f32_16x16x32_bf16 v[74:77], v[158:161], v[190:193], v[74:77]
	v_mfma_f32_16x16x32_bf16 v[10:13], v[166:169], v[190:193], v[10:13]
	v_mfma_f32_16x16x32_bf16 v[66:69], v[158:161], v[206:209], v[66:69]
	v_mfma_f32_16x16x32_bf16 v[2:5], v[166:169], v[206:209], v[2:5]
	v_mfma_f32_16x16x32_bf16 v[90:93], v[162:165], v[178:181], v[90:93]
	v_mfma_f32_16x16x32_bf16 v[26:29], v[170:173], v[178:181], v[26:29]
	v_mfma_f32_16x16x32_bf16 v[82:85], v[162:165], v[186:189], v[82:85]
	v_mfma_f32_16x16x32_bf16 v[18:21], v[170:173], v[186:189], v[18:21]
	v_mfma_f32_16x16x32_bf16 v[74:77], v[162:165], v[202:205], v[74:77]
	v_mfma_f32_16x16x32_bf16 v[10:13], v[170:173], v[202:205], v[10:13]
	v_mfma_f32_16x16x32_bf16 v[66:69], v[162:165], v[210:213], v[66:69]
	v_mfma_f32_16x16x32_bf16 v[2:5], v[170:173], v[210:213], v[2:5]
	s_setprio 0
	s_barrier
	s_andn2_b64 vcc, exec, s[84:85]
	s_mov_b64 s[86:87], -1
	s_mov_b64 s[84:85], 0
	s_mov_b64 s[88:89], 0x100
	s_cbranch_vccz .LBB0_273
	s_and_b64 vcc, exec, s[44:45]
	s_cbranch_vccz .LBB0_276
	s_barrier

; #define PG8_STAGE(bufoff, gbase, voff) do { _Pragma("unroll") for (int _i = 0; _i < 2; ++_i) \
;         __builtin_amdgcn_global_load_lds((const unsigned*)((const char*)(gbase) + (voff)[_i]), (LAS unsigned*)(lds + (bufoff) + ldsw + _i * 8192), 16, 0, 0); } while (0)
; #define PG8_LDA(dst, b, h) do { _Pragma("unroll") for (int m = 0; m < 4; ++m) _Pragma("unroll") for (int k = 0; k < 2; ++k) dst[m][k] = *(const LAS bf16x8*)(lds + PG8_SA(b, h) + aoff + m * 2048 + k * 1024); } while (0)
; #define PG8_LDB(dst, b, h) do { _Pragma("unroll") for (int n = 0; n < 2; ++n) _Pragma("unroll") for (int k = 0; k < 2; ++k) dst[n][k] = *(const LAS bf16x8*)(lds + PG8_SB(b, h) + boff + n * 2048 + k * 1024); } while (0)
; #define PG8_MMA(ai, bj, At, Bt) do { __builtin_amdgcn_s_setprio(1); _Pragma("unroll") for (int m = 0; m < 4; ++m) _Pragma("unroll") for (int n = 0; n < 2; ++n) _Pragma("unroll") for (int k = 0; k < 2; ++k) \
;         acc[ai][bj][m][n] = __builtin_amdgcn_mfma_f32_16x16x32_bf16(Bt[n][k], At[m][k], acc[ai][bj][m][n], 0, 0, 0); __builtin_amdgcn_s_setprio(0); } while (0)
; #define PG8_WAIT_V(n) asm volatile("s_waitcnt vmcnt(" #n ")" ::: "memory")
; #define PG8_WAIT_L(n) asm volatile("s_waitcnt lgkmcnt(" #n ")" ::: "memory")
; #define PG8_BAR __builtin_amdgcn_s_barrier()
; template <class Epi, class Sched>
; __device__ __forceinline__ void gemm_phase(LAS unsigned char* lds, const Gemm g, const Sched& S, const Epi& E) {
;     ...
;         for (int t = 0; t < nt; t += 2) {
;             const bool last = (t == nt - 2);
;             const char* a1 = cA + (size_t)(t + 1) * kstep;
;             const char* a2 = last ? nA : cA + (size_t)(t + 2) * kstep; const char* b2 = last ? nB : cB + (size_t)(t + 2) * kstep;
;             const char* a3 = a2 + kstep; const char* b3 = b2 + kstep;
;             if (last && has_next) S.a_ready(nxt);
;             PG8_LDB(B0, 0, 0); PG8_LDB(B1, 0, 1); PG8_SCHED; PG8_LDA(At, 0, 0); PG8_STAGE(PG8_SA(1, 1), a1 + hstepA, voffA);
;             PG8_WAIT_V(8); PG8_WAIT_L(0); PG8_BAR; PG8_MMA(0, 0, At, B0); PG8_MMA(0, 1, At, B1); PG8_BAR; PG8_SCHED;
;             PG8_LDA(At, 0, 1); PG8_STAGE(PG8_SB(0, 0), b2, voffB); PG8_STAGE(PG8_SB(0, 1), b2 + hstepB, voffB); PG8_STAGE(PG8_SA(0, 0), a2, voffA);
;             PG8_WAIT_V(8); PG8_WAIT_L(0); PG8_BAR; PG8_MMA(1, 0, At, B0); PG8_MMA(1, 1, At, B1); PG8_BAR; PG8_SCHED;
.LBB0_469:
	ds_read_b128 v[130:133], v191
	ds_read_b128 v[134:137], v191 offset:1024
	ds_read_b128 v[138:141], v191 offset:2048
	ds_read_b128 v[142:145], v191 offset:3072
	ds_read_b128 v[146:149], v192
	ds_read_b128 v[150:153], v192 offset:1024
	ds_read_b128 v[154:157], v192 offset:2048
	ds_read_b128 v[158:161], v192 offset:3072
	s_add_u32 s8, s60, 0xfff80080
	s_addc_u32 s9, s61, -1
	s_cmp_eq_u32 s82, 28
	s_cselect_b32 s65, s45, s9
	s_cselect_b32 s64, s47, s8
	s_cselect_b32 s63, s73, s81
	s_cselect_b32 s62, s74, s75
	v_lshl_add_u64 v[186:187], s[60:61], 0, v[166:167]
	s_add_i32 m0, s11, 0xc000
	ds_read_b128 v[174:177], v193
	ds_read_b128 v[178:181], v193 offset:1024
	ds_read_b128 v[182:185], v193 offset:2048
	ds_read_b128 v[194:197], v193 offset:3072
	ds_read_b128 v[198:201], v193 offset:4096
	ds_read_b128 v[202:205], v193 offset:5120
	ds_read_b128 v[206:209], v193 offset:6144
	ds_read_b128 v[210:213], v193 offset:7168
	global_load_lds_dwordx4 v[186:187], off
	v_lshl_add_u64 v[186:187], s[60:61], 0, v[168:169]
	s_add_i32 m0, s11, 0xe000
	s_nop 0
	global_load_lds_dwordx4 v[186:187], off
	s_waitcnt vmcnt(8)
	s_waitcnt lgkmcnt(0)
	s_barrier
	s_setprio 1
	v_mfma_f32_16x16x32_bf16 v[126:129], v[130:133], v[174:177], v[126:129]
	v_mfma_f32_16x16x32_bf16 v[122:125], v[138:141], v[174:177], v[122:125]
	v_mfma_f32_16x16x32_bf16 v[118:121], v[130:133], v[182:185], v[118:121]
	v_mfma_f32_16x16x32_bf16 v[114:117], v[138:141], v[182:185], v[114:117]
	v_mfma_f32_16x16x32_bf16 v[94:97], v[130:133], v[198:201], v[94:97]
	v_mfma_f32_16x16x32_bf16 v[90:93], v[138:141], v[198:201], v[90:93]
	v_mfma_f32_16x16x32_bf16 v[86:89], v[130:133], v[206:209], v[86:89]
	v_mfma_f32_16x16x32_bf16 v[82:85], v[138:141], v[206:209], v[82:85]
	v_mfma_f32_16x16x32_bf16 v[126:129], v[134:137], v[178:181], v[126:129]
	v_mfma_f32_16x16x32_bf16 v[122:125], v[142:145], v[178:181], v[122:125]
	v_mfma_f32_16x16x32_bf16 v[118:121], v[134:137], v[194:197], v[118:121]
	v_mfma_f32_16x16x32_bf16 v[114:117], v[142:145], v[194:197], v[114:117]
	v_mfma_f32_16x16x32_bf16 v[94:97], v[134:137], v[202:205], v[94:97]
	v_mfma_f32_16x16x32_bf16 v[90:93], v[142:145], v[202:205], v[90:93]
	v_mfma_f32_16x16x32_bf16 v[86:89], v[134:137], v[210:213], v[86:89]
	v_mfma_f32_16x16x32_bf16 v[82:85], v[142:145], v[210:213], v[82:85]
	s_setprio 0
	s_setprio 1
	v_mfma_f32_16x16x32_bf16 v[110:113], v[146:149], v[174:177], v[110:113]
	v_mfma_f32_16x16x32_bf16 v[106:109], v[154:157], v[174:177], v[106:109]
	v_mfma_f32_16x16x32_bf16 v[102:105], v[146:149], v[182:185], v[102:105]
	v_mfma_f32_16x16x32_bf16 v[98:101], v[154:157], v[182:185], v[98:101]
	v_mfma_f32_16x16x32_bf16 v[78:81], v[146:149], v[198:201], v[78:81]
	v_mfma_f32_16x16x32_bf16 v[74:77], v[154:157], v[198:201], v[74:77]
	v_mfma_f32_16x16x32_bf16 v[70:73], v[146:149], v[206:209], v[70:73]
	v_mfma_f32_16x16x32_bf16 v[66:69], v[154:157], v[206:209], v[66:69]
	v_mfma_f32_16x16x32_bf16 v[110:113], v[150:153], v[178:181], v[110:113]
	v_mfma_f32_16x16x32_bf16 v[106:109], v[158:161], v[178:181], v[106:109]
	v_mfma_f32_16x16x32_bf16 v[102:105], v[150:153], v[194:197], v[102:105]
	v_mfma_f32_16x16x32_bf16 v[98:101], v[158:161], v[194:197], v[98:101]
	v_mfma_f32_16x16x32_bf16 v[78:81], v[150:153], v[202:205], v[78:81]
	v_mfma_f32_16x16x32_bf16 v[74:77], v[158:161], v[202:205], v[74:77]
	v_mfma_f32_16x16x32_bf16 v[70:73], v[150:153], v[210:213], v[70:73]
	v_mfma_f32_16x16x32_bf16 v[66:69], v[158:161], v[210:213], v[66:69]
	s_setprio 0
	s_barrier
	s_add_i32 s8, s79, s10
	v_lshl_add_u64 v[186:187], s[62:63], 0, v[164:165]
	s_mov_b32 m0, s8
	ds_read_b128 v[174:177], v193 offset:16384
	ds_read_b128 v[178:181], v193 offset:17408
	ds_read_b128 v[182:185], v193 offset:18432
	ds_read_b128 v[194:197], v193 offset:19456
	ds_read_b128 v[198:201], v193 offset:20480
	ds_read_b128 v[202:205], v193 offset:21504
	ds_read_b128 v[206:209], v193 offset:22528
	ds_read_b128 v[210:213], v193 offset:23552
	global_load_lds_dwordx4 v[186:187], off
	s_add_i32 m0, s8, 0x2000
	s_add_u32 s8, s62, 0x80000
	v_lshl_add_u64 v[214:215], s[62:63], 0, v[162:163]
	s_addc_u32 s9, s63, 0
	s_add_i32 s12, s80, s10
	global_load_lds_dwordx4 v[214:215], off
	v_lshl_add_u64 v[216:217], s[8:9], 0, v[164:165]
	s_mov_b32 m0, s12
	v_lshl_add_u64 v[218:219], s[64:65], 0, v[162:163]
	global_load_lds_dwordx4 v[216:217], off
	v_lshl_add_u64 v[216:217], s[8:9], 0, v[162:163]
	s_add_i32 m0, s12, 0x2000
	s_nop 0
	global_load_lds_dwordx4 v[216:217], off
	v_lshl_add_u64 v[216:217], s[64:65], 0, v[164:165]
	s_mov_b32 m0, s11
	s_nop 0
	global_load_lds_dwordx4 v[216:217], off
	s_mov_b32 m0, s24
	s_nop 0
	global_load_lds_dwordx4 v[218:219], off
	s_waitcnt vmcnt(8)
	s_waitcnt lgkmcnt(0)
	s_barrier
; #define PG8_STAGE(bufoff, gbase, voff) do { _Pragma("unroll") for (int _i = 0; _i < 2; ++_i) \
;         __builtin_amdgcn_global_load_lds((const unsigned*)((const char*)(gbase) + (voff)[_i]), (LAS unsigned*)(lds + (bufoff) + ldsw + _i * 8192), 16, 0, 0); } while (0)
; #define PG8_LDA(dst, b, h) do { _Pragma("unroll") for (int m = 0; m < 4; ++m) _Pragma("unroll") for (int k = 0; k < 2; ++k) dst[m][k] = *(const LAS bf16x8*)(lds + PG8_SA(b, h) + aoff + m * 2048 + k * 1024); } while (0)
; #define PG8_LDB(dst, b, h) do { _Pragma("unroll") for (int n = 0; n < 2; ++n) _Pragma("unroll") for (int k = 0; k < 2; ++k) dst[n][k] = *(const LAS bf16x8*)(lds + PG8_SB(b, h) + boff + n * 2048 + k * 1024); } while (0)
; #define PG8_MMA(ai, bj, At, Bt) do { __builtin_amdgcn_s_setprio(1); _Pragma("unroll") for (int m = 0; m < 4; ++m) _Pragma("unroll") for (int n = 0; n < 2; ++n) _Pragma("unroll") for (int k = 0; k < 2; ++k) \
;         acc[ai][bj][m][n] = __builtin_amdgcn_mfma_f32_16x16x32_bf16(Bt[n][k], At[m][k], acc[ai][bj][m][n], 0, 0, 0); __builtin_amdgcn_s_setprio(0); } while (0)
; #define PG8_WAIT_V(n) asm volatile("s_waitcnt vmcnt(" #n ")" ::: "memory")
; #define PG8_WAIT_L(n) asm volatile("s_waitcnt lgkmcnt(" #n ")" ::: "memory")
; #define PG8_BAR __builtin_amdgcn_s_barrier()
; #define PG8_SCHED __builtin_amdgcn_sched_barrier(0)
; #define PG8_STAGE(bufoff, gbase, voff) do { _Pragma("unroll") for (int _i = 0; _i < 2; ++_i) \
;         __builtin_amdgcn_global_load_lds((const unsigned*)((const char*)(gbase) + (voff)[_i]), (LAS unsigned*)(lds + (bufoff) + ldsw + _i * 8192), 16, 0, 0); } while (0)
; #define PG8_LDA(dst, b, h) do { _Pragma("unroll") for (int m = 0; m < 4; ++m) PG8_LD1(dst[m], PG8_SA(b, h) + aoff0 + m * 2048, PG8_SA(b, h) + aoff1 + m * 2048); } while (0)
; #define PG8_WAIT_V(n) asm volatile("s_waitcnt vmcnt(" #n ")" ::: "memory")
; template <class Epi, class Sched>
; __device__ __forceinline__ void gemm_phase(LAS unsigned char* lds, const Gemm g, const Sched& S, const Epi& E) {
;     ...
;             PG8_WAIT_V(8); PG8_WAIT_L(0); PG8_BAR; PG8_MMA(1, 0, At, B0); PG8_MMA(1, 1, At, B1); PG8_BAR; PG8_SCHED;
;             PG8_LDB(B0, 1, 0); PG8_LDB(B1, 1, 1); PG8_SCHED; PG8_LDA(At, 1, 0); PG8_STAGE(PG8_SA(0, 1), a2 + hstepA, voffA);
;             PG8_WAIT_V(8); PG8_WAIT_L(0); PG8_BAR; PG8_MMA(0, 0, At, B0); PG8_MMA(0, 1, At, B1); PG8_BAR; PG8_SCHED;
	s_setprio 1
	v_mfma_f32_16x16x32_bf16 v[62:65], v[130:133], v[174:177], v[62:65]
	v_mfma_f32_16x16x32_bf16 v[58:61], v[138:141], v[174:177], v[58:61]
	v_mfma_f32_16x16x32_bf16 v[54:57], v[130:133], v[182:185], v[54:57]
	v_mfma_f32_16x16x32_bf16 v[42:45], v[138:141], v[182:185], v[42:45]
	v_mfma_f32_16x16x32_bf16 v[38:41], v[130:133], v[198:201], v[38:41]
	v_mfma_f32_16x16x32_bf16 v[26:29], v[138:141], v[198:201], v[26:29]
	v_mfma_f32_16x16x32_bf16 v[22:25], v[130:133], v[206:209], v[22:25]
	v_mfma_f32_16x16x32_bf16 v[10:13], v[138:141], v[206:209], v[10:13]
	v_mfma_f32_16x16x32_bf16 v[62:65], v[134:137], v[178:181], v[62:65]
	v_mfma_f32_16x16x32_bf16 v[58:61], v[142:145], v[178:181], v[58:61]
	v_mfma_f32_16x16x32_bf16 v[54:57], v[134:137], v[194:197], v[54:57]
	v_mfma_f32_16x16x32_bf16 v[42:45], v[142:145], v[194:197], v[42:45]
	v_mfma_f32_16x16x32_bf16 v[38:41], v[134:137], v[202:205], v[38:41]
	v_mfma_f32_16x16x32_bf16 v[26:29], v[142:145], v[202:205], v[26:29]
	v_mfma_f32_16x16x32_bf16 v[22:25], v[134:137], v[210:213], v[22:25]
	v_mfma_f32_16x16x32_bf16 v[10:13], v[142:145], v[210:213], v[10:13]
	s_setprio 0
	s_setprio 1
	v_mfma_f32_16x16x32_bf16 v[50:53], v[146:149], v[174:177], v[50:53]
	v_mfma_f32_16x16x32_bf16 v[46:49], v[154:157], v[174:177], v[46:49]
	v_mfma_f32_16x16x32_bf16 v[34:37], v[146:149], v[182:185], v[34:37]
	v_mfma_f32_16x16x32_bf16 v[30:33], v[154:157], v[182:185], v[30:33]
	v_mfma_f32_16x16x32_bf16 v[18:21], v[146:149], v[198:201], v[18:21]
	v_mfma_f32_16x16x32_bf16 v[14:17], v[154:157], v[198:201], v[14:17]
	v_mfma_f32_16x16x32_bf16 v[6:9], v[146:149], v[206:209], v[6:9]
	v_mfma_f32_16x16x32_bf16 v[2:5], v[154:157], v[206:209], v[2:5]
	v_mfma_f32_16x16x32_bf16 v[50:53], v[150:153], v[178:181], v[50:53]
	v_mfma_f32_16x16x32_bf16 v[46:49], v[158:161], v[178:181], v[46:49]
	v_mfma_f32_16x16x32_bf16 v[34:37], v[150:153], v[194:197], v[34:37]
	v_mfma_f32_16x16x32_bf16 v[30:33], v[158:161], v[194:197], v[30:33]
	v_mfma_f32_16x16x32_bf16 v[18:21], v[150:153], v[202:205], v[18:21]
	v_mfma_f32_16x16x32_bf16 v[14:17], v[158:161], v[202:205], v[14:17]
	v_mfma_f32_16x16x32_bf16 v[6:9], v[150:153], v[210:213], v[6:9]
	v_mfma_f32_16x16x32_bf16 v[2:5], v[158:161], v[210:213], v[2:5]
	s_setprio 0
	s_barrier
	s_add_i32 s12, 0, 0x18000
	s_add_i32 s13, 0, 0x1c000
	v_add_u32_e32 v142, s12, v189
	v_add_u32_e32 v158, s13, v189
	ds_read_b128 v[130:133], v142
	ds_read_b128 v[134:137], v142 offset:1024
	ds_read_b128 v[138:141], v142 offset:2048
	ds_read_b128 v[142:145], v142 offset:3072
	ds_read_b128 v[146:149], v158
	ds_read_b128 v[150:153], v158 offset:1024
	ds_read_b128 v[154:157], v158 offset:2048
	ds_read_b128 v[158:161], v158 offset:3072
	s_add_u32 s8, s64, 0x80000
	s_addc_u32 s9, s65, 0
	s_mov_b32 m0, s25
	v_lshl_add_u64 v[220:221], s[8:9], 0, v[164:165]
	ds_read_b128 v[174:177], v193 offset:32768
	ds_read_b128 v[178:181], v193 offset:33792
	ds_read_b128 v[182:185], v193 offset:34816
	ds_read_b128 v[194:197], v193 offset:35840
	ds_read_b128 v[198:201], v193 offset:36864
	ds_read_b128 v[202:205], v193 offset:37888
	ds_read_b128 v[206:209], v193 offset:38912
	ds_read_b128 v[210:213], v193 offset:39936
	global_load_lds_dwordx4 v[220:221], off
	v_lshl_add_u64 v[220:221], s[8:9], 0, v[162:163]
	s_mov_b32 m0, s33
	s_nop 0
	global_load_lds_dwordx4 v[220:221], off
	s_waitcnt vmcnt(8)
	s_waitcnt lgkmcnt(0)
	s_barrier
	s_setprio 1
	v_mfma_f32_16x16x32_bf16 v[126:129], v[130:133], v[174:177], v[126:129]
	v_mfma_f32_16x16x32_bf16 v[122:125], v[138:141], v[174:177], v[122:125]
	v_mfma_f32_16x16x32_bf16 v[118:121], v[130:133], v[182:185], v[118:121]
	v_mfma_f32_16x16x32_bf16 v[114:117], v[138:141], v[182:185], v[114:117]
	v_mfma_f32_16x16x32_bf16 v[94:97], v[130:133], v[198:201], v[94:97]
	v_mfma_f32_16x16x32_bf16 v[90:93], v[138:141], v[198:201], v[90:93]
	v_mfma_f32_16x16x32_bf16 v[86:89], v[130:133], v[206:209], v[86:89]
	v_mfma_f32_16x16x32_bf16 v[82:85], v[138:141], v[206:209], v[82:85]
	v_mfma_f32_16x16x32_bf16 v[126:129], v[134:137], v[178:181], v[126:129]
	v_mfma_f32_16x16x32_bf16 v[122:125], v[142:145], v[178:181], v[122:125]
	v_mfma_f32_16x16x32_bf16 v[118:121], v[134:137], v[194:197], v[118:121]
	v_mfma_f32_16x16x32_bf16 v[114:117], v[142:145], v[194:197], v[114:117]
	v_mfma_f32_16x16x32_bf16 v[94:97], v[134:137], v[202:205], v[94:97]
	v_mfma_f32_16x16x32_bf16 v[90:93], v[142:145], v[202:205], v[90:93]
	v_mfma_f32_16x16x32_bf16 v[86:89], v[134:137], v[210:213], v[86:89]
	v_mfma_f32_16x16x32_bf16 v[82:85], v[142:145], v[210:213], v[82:85]
	s_setprio 0
	s_setprio 1
	v_mfma_f32_16x16x32_bf16 v[110:113], v[146:149], v[174:177], v[110:113]
	v_mfma_f32_16x16x32_bf16 v[106:109], v[154:157], v[174:177], v[106:109]
	v_mfma_f32_16x16x32_bf16 v[102:105], v[146:149], v[182:185], v[102:105]
	v_mfma_f32_16x16x32_bf16 v[98:101], v[154:157], v[182:185], v[98:101]
	v_mfma_f32_16x16x32_bf16 v[78:81], v[146:149], v[198:201], v[78:81]
	v_mfma_f32_16x16x32_bf16 v[74:77], v[154:157], v[198:201], v[74:77]
	v_mfma_f32_16x16x32_bf16 v[70:73], v[146:149], v[206:209], v[70:73]
	v_mfma_f32_16x16x32_bf16 v[66:69], v[154:157], v[206:209], v[66:69]
	v_mfma_f32_16x16x32_bf16 v[110:113], v[150:153], v[178:181], v[110:113]
	v_mfma_f32_16x16x32_bf16 v[106:109], v[158:161], v[178:181], v[106:109]
	v_mfma_f32_16x16x32_bf16 v[102:105], v[150:153], v[194:197], v[102:105]
	v_mfma_f32_16x16x32_bf16 v[98:101], v[158:161], v[194:197], v[98:101]
	v_mfma_f32_16x16x32_bf16 v[78:81], v[150:153], v[202:205], v[78:81]
	v_mfma_f32_16x16x32_bf16 v[74:77], v[158:161], v[202:205], v[74:77]
	v_mfma_f32_16x16x32_bf16 v[70:73], v[150:153], v[210:213], v[70:73]
	v_mfma_f32_16x16x32_bf16 v[66:69], v[158:161], v[210:213], v[66:69]
	s_setprio 0
	s_barrier
; #define PG8_STAGE(bufoff, gbase, voff) do { _Pragma("unroll") for (int _i = 0; _i < 2; ++_i) \
;         __builtin_amdgcn_global_load_lds((const unsigned*)((const char*)(gbase) + (voff)[_i]), (LAS unsigned*)(lds + (bufoff) + ldsw + _i * 8192), 16, 0, 0); } while (0)
; #define PG8_LDA(dst, b, h) do { _Pragma("unroll") for (int m = 0; m < 4; ++m) _Pragma("unroll") for (int k = 0; k < 2; ++k) dst[m][k] = *(const LAS bf16x8*)(lds + PG8_SA(b, h) + aoff + m * 2048 + k * 1024); } while (0)
; #define PG8_MMA(ai, bj, At, Bt) do { __builtin_amdgcn_s_setprio(1); _Pragma("unroll") for (int m = 0; m < 4; ++m) _Pragma("unroll") for (int n = 0; n < 2; ++n) _Pragma("unroll") for (int k = 0; k < 2; ++k) \
;         acc[ai][bj][m][n] = __builtin_amdgcn_mfma_f32_16x16x32_bf16(Bt[n][k], At[m][k], acc[ai][bj][m][n], 0, 0, 0); __builtin_amdgcn_s_setprio(0); } while (0)
; #define PG8_WAIT_V(n) asm volatile("s_waitcnt vmcnt(" #n ")" ::: "memory")
; #define PG8_WAIT_L(n) asm volatile("s_waitcnt lgkmcnt(" #n ")" ::: "memory")
; #define PG8_BAR __builtin_amdgcn_s_barrier()
; #define PG8_SCHED __builtin_amdgcn_sched_barrier(0)
; #define PG8_STAGE(bufoff, gbase, voff) do { _Pragma("unroll") for (int _i = 0; _i < 2; ++_i) \
;         __builtin_amdgcn_global_load_lds((const unsigned*)((const char*)(gbase) + (voff)[_i]), (LAS unsigned*)(lds + (bufoff) + ldsw + _i * 8192), 16, 0, 0); } while (0)
; #define PG8_LDA(dst, b, h) do { _Pragma("unroll") for (int m = 0; m < 4; ++m) PG8_LD1(dst[m], PG8_SA(b, h) + aoff0 + m * 2048, PG8_SA(b, h) + aoff1 + m * 2048); } while (0)
; #define PG8_WAIT_V(n) asm volatile("s_waitcnt vmcnt(" #n ")" ::: "memory")
; #define PG8_WAIT_L(n) asm volatile("s_waitcnt lgkmcnt(" #n ")" ::: "memory")
; #define PG8_BAR __builtin_amdgcn_s_barrier()
; #define PG8_SCHED __builtin_amdgcn_sched_barrier(0)
; template <class Epi, class Sched>
; __device__ __forceinline__ void gemm_phase(LAS unsigned char* lds, const Gemm g, const Sched& S, const Epi& E) {
;     ...
;             PG8_LDA(At, 1, 1); PG8_STAGE(PG8_SB(1, 0), b3, voffB); PG8_STAGE(PG8_SB(1, 1), b3 + hstepB, voffB); PG8_STAGE(PG8_SA(1, 0), a3, voffA);
;             PG8_WAIT_V(8); PG8_WAIT_L(0); PG8_BAR; PG8_MMA(1, 0, At, B0); PG8_MMA(1, 1, At, B1); PG8_BAR; PG8_SCHED;
;         }
;         if (wr == 0) PG8_BAR;
	s_add_i32 s8, s12, s10
	v_lshl_add_u64 v[186:187], v[186:187], 0, s[38:39]
	s_mov_b32 m0, s8
	ds_read_b128 v[174:177], v193 offset:49152
	ds_read_b128 v[178:181], v193 offset:50176
	ds_read_b128 v[182:185], v193 offset:51200
	ds_read_b128 v[194:197], v193 offset:52224
	ds_read_b128 v[198:201], v193 offset:53248
	ds_read_b128 v[202:205], v193 offset:54272
	ds_read_b128 v[206:209], v193 offset:55296
	ds_read_b128 v[210:213], v193 offset:56320
	global_load_lds_dwordx4 v[186:187], off
	s_add_i32 m0, s8, 0x2000
	s_add_u32 s8, s62, 0x80080
	v_lshl_add_u64 v[186:187], v[214:215], 0, s[38:39]
	s_addc_u32 s9, s63, 0
	s_add_i32 s12, s13, s10
	global_load_lds_dwordx4 v[186:187], off
	v_lshl_add_u64 v[186:187], s[8:9], 0, v[164:165]
	s_mov_b32 m0, s12
	s_nop 0
	global_load_lds_dwordx4 v[186:187], off
	v_lshl_add_u64 v[186:187], s[8:9], 0, v[162:163]
	s_add_i32 m0, s12, 0x2000
	s_nop 0
	global_load_lds_dwordx4 v[186:187], off
	v_lshl_add_u64 v[186:187], v[216:217], 0, s[38:39]
	s_mov_b32 m0, s67
	s_nop 0
	global_load_lds_dwordx4 v[186:187], off
	v_lshl_add_u64 v[186:187], v[218:219], 0, s[38:39]
	s_mov_b32 m0, s78
	s_nop 0
	global_load_lds_dwordx4 v[186:187], off
	s_waitcnt vmcnt(8)
	s_waitcnt lgkmcnt(0)
	s_barrier
	s_setprio 1
	v_mfma_f32_16x16x32_bf16 v[62:65], v[130:133], v[174:177], v[62:65]
	v_mfma_f32_16x16x32_bf16 v[58:61], v[138:141], v[174:177], v[58:61]
	v_mfma_f32_16x16x32_bf16 v[54:57], v[130:133], v[182:185], v[54:57]
	v_mfma_f32_16x16x32_bf16 v[42:45], v[138:141], v[182:185], v[42:45]
	v_mfma_f32_16x16x32_bf16 v[38:41], v[130:133], v[198:201], v[38:41]
	v_mfma_f32_16x16x32_bf16 v[26:29], v[138:141], v[198:201], v[26:29]
	v_mfma_f32_16x16x32_bf16 v[22:25], v[130:133], v[206:209], v[22:25]
	v_mfma_f32_16x16x32_bf16 v[10:13], v[138:141], v[206:209], v[10:13]
	v_mfma_f32_16x16x32_bf16 v[62:65], v[134:137], v[178:181], v[62:65]
	v_mfma_f32_16x16x32_bf16 v[58:61], v[142:145], v[178:181], v[58:61]
	v_mfma_f32_16x16x32_bf16 v[54:57], v[134:137], v[194:197], v[54:57]
	v_mfma_f32_16x16x32_bf16 v[42:45], v[142:145], v[194:197], v[42:45]
	v_mfma_f32_16x16x32_bf16 v[38:41], v[134:137], v[202:205], v[38:41]
	v_mfma_f32_16x16x32_bf16 v[26:29], v[142:145], v[202:205], v[26:29]
	v_mfma_f32_16x16x32_bf16 v[22:25], v[134:137], v[210:213], v[22:25]
	v_mfma_f32_16x16x32_bf16 v[10:13], v[142:145], v[210:213], v[10:13]
	s_setprio 0
	s_setprio 1
	v_mfma_f32_16x16x32_bf16 v[50:53], v[146:149], v[174:177], v[50:53]
	v_mfma_f32_16x16x32_bf16 v[46:49], v[154:157], v[174:177], v[46:49]
	v_mfma_f32_16x16x32_bf16 v[34:37], v[146:149], v[182:185], v[34:37]
	v_mfma_f32_16x16x32_bf16 v[30:33], v[154:157], v[182:185], v[30:33]
	v_mfma_f32_16x16x32_bf16 v[18:21], v[146:149], v[198:201], v[18:21]
	v_mfma_f32_16x16x32_bf16 v[14:17], v[154:157], v[198:201], v[14:17]
	v_mfma_f32_16x16x32_bf16 v[6:9], v[146:149], v[206:209], v[6:9]
	v_mfma_f32_16x16x32_bf16 v[2:5], v[154:157], v[206:209], v[2:5]
	v_mfma_f32_16x16x32_bf16 v[50:53], v[150:153], v[178:181], v[50:53]
	v_mfma_f32_16x16x32_bf16 v[46:49], v[158:161], v[178:181], v[46:49]
	v_mfma_f32_16x16x32_bf16 v[34:37], v[150:153], v[194:197], v[34:37]
	v_mfma_f32_16x16x32_bf16 v[30:33], v[158:161], v[194:197], v[30:33]
	v_mfma_f32_16x16x32_bf16 v[18:21], v[150:153], v[202:205], v[18:21]
	v_mfma_f32_16x16x32_bf16 v[14:17], v[158:161], v[202:205], v[14:17]
	v_mfma_f32_16x16x32_bf16 v[6:9], v[150:153], v[210:213], v[6:9]
	v_mfma_f32_16x16x32_bf16 v[2:5], v[158:161], v[210:213], v[2:5]
	s_setprio 0
	s_barrier
	s_add_i32 s82, s82, 2
	s_add_u32 s60, s60, 0x100
	s_addc_u32 s61, s61, 0
	s_add_u32 s75, s75, 0x100
	s_addc_u32 s81, s81, 0
	s_cmp_gt_u32 s82, 29
	s_cbranch_scc0 .LBB0_469
	s_and_b64 vcc, exec, s[42:43]
	s_cbranch_vccz .LBB0_472
	s_barrier

; #define PG8_STAGE(bufoff, gbase, voff) do { _Pragma("unroll") for (int _i = 0; _i < 2; ++_i) \
;         __builtin_amdgcn_global_load_lds((const unsigned*)((const char*)(gbase) + (voff)[_i]), (LAS unsigned*)(lds + (bufoff) + ldsw + _i * 8192), 16, 0, 0); } while (0)
; #define PG8_LDA(dst, b, h) do { _Pragma("unroll") for (int m = 0; m < 4; ++m) _Pragma("unroll") for (int k = 0; k < 2; ++k) dst[m][k] = *(const LAS bf16x8*)(lds + PG8_SA(b, h) + aoff + m * 2048 + k * 1024); } while (0)
; #define PG8_LDB(dst, b, h) do { _Pragma("unroll") for (int n = 0; n < 2; ++n) _Pragma("unroll") for (int k = 0; k < 2; ++k) dst[n][k] = *(const LAS bf16x8*)(lds + PG8_SB(b, h) + boff + n * 2048 + k * 1024); } while (0)
; #define PG8_MMA(ai, bj, At, Bt) do { __builtin_amdgcn_s_setprio(1); _Pragma("unroll") for (int m = 0; m < 4; ++m) _Pragma("unroll") for (int n = 0; n < 2; ++n) _Pragma("unroll") for (int k = 0; k < 2; ++k) \
;         acc[ai][bj][m][n] = __builtin_amdgcn_mfma_f32_16x16x32_bf16(Bt[n][k], At[m][k], acc[ai][bj][m][n], 0, 0, 0); __builtin_amdgcn_s_setprio(0); } while (0)
; #define PG8_WAIT_V(n) asm volatile("s_waitcnt vmcnt(" #n ")" ::: "memory")
; #define PG8_WAIT_L(n) asm volatile("s_waitcnt lgkmcnt(" #n ")" ::: "memory")
; #define PG8_BAR __builtin_amdgcn_s_barrier()
; #define PG8_SCHED __builtin_amdgcn_sched_barrier(0)
; #define PG8_STAGE(bufoff, gbase, voff) do { _Pragma("unroll") for (int _i = 0; _i < 2; ++_i) \
;         __builtin_amdgcn_global_load_lds((const unsigned*)((const char*)(gbase) + (voff)[_i]), (LAS unsigned*)(lds + (bufoff) + ldsw + _i * 8192), 16, 0, 0); } while (0)
; #define PG8_LDA(dst, b, h) do { _Pragma("unroll") for (int m = 0; m < 4; ++m) PG8_LD1(dst[m], PG8_SA(b, h) + aoff0 + m * 2048, PG8_SA(b, h) + aoff1 + m * 2048); } while (0)
; #define PG8_WAIT_V(n) asm volatile("s_waitcnt vmcnt(" #n ")" ::: "memory")
;     ...
;             PG8_LDB(B0, 0, 0); PG8_LDB(B1, 0, 1); PG8_SCHED; PG8_LDA(At, 0, 0); PG8_STAGE(PG8_SA(1, 1), a1 + hstepA, voffA);
;             PG8_WAIT_V(8); PG8_WAIT_L(0); PG8_BAR; PG8_MMA(0, 0, At, B0); PG8_MMA(0, 1, At, B1); PG8_BAR; PG8_SCHED;
;             PG8_LDA(At, 0, 1); PG8_STAGE(PG8_SB(0, 0), b2, voffB); PG8_STAGE(PG8_SB(0, 1), b2 + hstepB, voffB); PG8_STAGE(PG8_SA(0, 0), a2, voffA);
;             PG8_WAIT_V(8); PG8_WAIT_L(0); PG8_BAR; PG8_MMA(1, 0, At, B0); PG8_MMA(1, 1, At, B1); PG8_BAR; PG8_SCHED;
.LBB0_594:
	ds_read_b128 v[158:161], v187
	ds_read_b128 v[146:149], v188
	ds_read_b128 v[154:157], v195
	ds_read_b128 v[150:153], v196
	ds_read_b128 v[142:145], v189
	ds_read_b128 v[130:133], v190
	ds_read_b128 v[138:141], v197
	ds_read_b128 v[134:137], v198
	s_add_u32 s58, s60, 0x100
	s_addc_u32 s59, s61, 0
	s_cmp_eq_u32 s92, 12
	s_cselect_b32 s65, s43, s59
	s_cselect_b32 s64, s45, s58
	s_cselect_b32 s63, s75, s91
	s_cselect_b32 s62, s89, s90
	v_lshl_add_u64 v[232:233], s[60:61], 0, v[170:171]
	s_add_i32 m0, s11, 0xc000
	ds_read_b128 v[178:181], v204
	ds_read_b128 v[182:185], v204 offset:2048
	ds_read_b128 v[208:211], v205
	ds_read_b128 v[212:215], v205 offset:2048
	ds_read_b128 v[216:219], v204 offset:4096
	ds_read_b128 v[220:223], v204 offset:6144
	ds_read_b128 v[224:227], v205 offset:4096
	ds_read_b128 v[228:231], v205 offset:6144
	global_load_lds_dwordx4 v[232:233], off
	v_lshl_add_u64 v[232:233], s[60:61], 0, v[172:173]
	s_add_i32 m0, s11, 0xe000
	s_nop 0
	global_load_lds_dwordx4 v[232:233], off
	s_waitcnt vmcnt(8)
	s_waitcnt lgkmcnt(0)
	s_barrier
	s_setprio 1
	v_mfma_i32_16x16x64_i8 v[126:129], v[158:161], v[178:181], v[126:129]
	v_mfma_i32_16x16x64_i8 v[122:125], v[154:157], v[178:181], v[122:125]
	v_mfma_i32_16x16x64_i8 v[118:121], v[158:161], v[182:185], v[118:121]
	v_mfma_i32_16x16x64_i8 v[110:113], v[154:157], v[182:185], v[110:113]
	v_mfma_i32_16x16x64_i8 v[102:105], v[158:161], v[216:219], v[102:105]
	v_mfma_i32_16x16x64_i8 v[94:97], v[154:157], v[216:219], v[94:97]
	v_mfma_i32_16x16x64_i8 v[86:89], v[158:161], v[220:223], v[86:89]
	v_mfma_i32_16x16x64_i8 v[78:81], v[154:157], v[220:223], v[78:81]
	s_nop 0
	v_mfma_i32_16x16x64_i8 v[126:129], v[146:149], v[208:211], v[126:129]
	v_mfma_i32_16x16x64_i8 v[122:125], v[150:153], v[208:211], v[122:125]
	v_mfma_i32_16x16x64_i8 v[118:121], v[146:149], v[212:215], v[118:121]
	v_mfma_i32_16x16x64_i8 v[110:113], v[150:153], v[212:215], v[110:113]
	v_mfma_i32_16x16x64_i8 v[102:105], v[146:149], v[224:227], v[102:105]
	v_mfma_i32_16x16x64_i8 v[94:97], v[150:153], v[224:227], v[94:97]
	v_mfma_i32_16x16x64_i8 v[86:89], v[146:149], v[228:231], v[86:89]
	v_mfma_i32_16x16x64_i8 v[78:81], v[150:153], v[228:231], v[78:81]
	s_setprio 0
	s_setprio 1
	v_mfma_i32_16x16x64_i8 v[114:117], v[142:145], v[178:181], v[114:117]
	v_mfma_i32_16x16x64_i8 v[106:109], v[138:141], v[178:181], v[106:109]
	v_mfma_i32_16x16x64_i8 v[98:101], v[142:145], v[182:185], v[98:101]
	v_mfma_i32_16x16x64_i8 v[90:93], v[138:141], v[182:185], v[90:93]
	v_mfma_i32_16x16x64_i8 v[82:85], v[142:145], v[216:219], v[82:85]
	v_mfma_i32_16x16x64_i8 v[74:77], v[138:141], v[216:219], v[74:77]
	v_mfma_i32_16x16x64_i8 v[70:73], v[142:145], v[220:223], v[70:73]
	v_mfma_i32_16x16x64_i8 v[66:69], v[138:141], v[220:223], v[66:69]
	s_nop 0
	v_mfma_i32_16x16x64_i8 v[114:117], v[130:133], v[208:211], v[114:117]
	v_mfma_i32_16x16x64_i8 v[106:109], v[134:137], v[208:211], v[106:109]
	v_mfma_i32_16x16x64_i8 v[98:101], v[130:133], v[212:215], v[98:101]
	v_mfma_i32_16x16x64_i8 v[90:93], v[134:137], v[212:215], v[90:93]
	v_mfma_i32_16x16x64_i8 v[82:85], v[130:133], v[224:227], v[82:85]
	v_mfma_i32_16x16x64_i8 v[74:77], v[134:137], v[224:227], v[74:77]
	v_mfma_i32_16x16x64_i8 v[70:73], v[130:133], v[228:231], v[70:73]
	v_mfma_i32_16x16x64_i8 v[66:69], v[134:137], v[228:231], v[66:69]
	s_setprio 0
	s_barrier
	s_mov_b32 m0, s24
	v_lshl_add_u64 v[178:179], s[62:63], 0, v[166:167]
	s_add_u32 s8, s62, 0x40000
	ds_read_b128 v[208:211], v204 offset:16384
	ds_read_b128 v[212:215], v204 offset:18432
	ds_read_b128 v[216:219], v205 offset:16384
	ds_read_b128 v[220:223], v205 offset:18432
	ds_read_b128 v[224:227], v204 offset:20480
	ds_read_b128 v[228:231], v204 offset:22528
	ds_read_b128 v[232:235], v205 offset:20480
	ds_read_b128 v[236:239], v205 offset:22528
	global_load_lds_dwordx4 v[178:179], off
	v_lshl_add_u64 v[180:181], s[62:63], 0, v[162:163]
	s_mov_b32 m0, s25
	s_addc_u32 s9, s63, 0
	global_load_lds_dwordx4 v[180:181], off
	v_lshl_add_u64 v[182:183], s[8:9], 0, v[166:167]
	s_mov_b32 m0, s66
	v_lshl_add_u64 v[184:185], s[64:65], 0, v[164:165]
	global_load_lds_dwordx4 v[182:183], off
	v_lshl_add_u64 v[182:183], s[8:9], 0, v[162:163]
	s_mov_b32 m0, s67
	s_nop 0
	global_load_lds_dwordx4 v[182:183], off
	v_lshl_add_u64 v[182:183], s[64:65], 0, v[168:169]
	s_mov_b32 m0, s11
	s_nop 0
	global_load_lds_dwordx4 v[182:183], off
	s_mov_b32 m0, s0
	s_nop 0
	global_load_lds_dwordx4 v[184:185], off
	s_waitcnt vmcnt(8)
	s_waitcnt lgkmcnt(0)
	s_barrier
	s_setprio 1
	v_mfma_i32_16x16x64_i8 v[62:65], v[158:161], v[208:211], v[62:65]
	v_mfma_i32_16x16x64_i8 v[58:61], v[154:157], v[208:211], v[58:61]
	v_mfma_i32_16x16x64_i8 v[54:57], v[158:161], v[212:215], v[54:57]
	v_mfma_i32_16x16x64_i8 v[46:49], v[154:157], v[212:215], v[46:49]
	v_mfma_i32_16x16x64_i8 v[38:41], v[158:161], v[224:227], v[38:41]
	v_mfma_i32_16x16x64_i8 v[30:33], v[154:157], v[224:227], v[30:33]
	v_mfma_i32_16x16x64_i8 v[22:25], v[158:161], v[228:231], v[22:25]
	v_mfma_i32_16x16x64_i8 v[14:17], v[154:157], v[228:231], v[14:17]
	s_nop 0
	v_mfma_i32_16x16x64_i8 v[62:65], v[146:149], v[216:219], v[62:65]
	v_mfma_i32_16x16x64_i8 v[58:61], v[150:153], v[216:219], v[58:61]
	v_mfma_i32_16x16x64_i8 v[54:57], v[146:149], v[220:223], v[54:57]
	v_mfma_i32_16x16x64_i8 v[46:49], v[150:153], v[220:223], v[46:49]
	v_mfma_i32_16x16x64_i8 v[38:41], v[146:149], v[232:235], v[38:41]
	v_mfma_i32_16x16x64_i8 v[30:33], v[150:153], v[232:235], v[30:33]
	v_mfma_i32_16x16x64_i8 v[22:25], v[146:149], v[236:239], v[22:25]
	v_mfma_i32_16x16x64_i8 v[14:17], v[150:153], v[236:239], v[14:17]
	s_setprio 0
	s_setprio 1
	v_mfma_i32_16x16x64_i8 v[50:53], v[142:145], v[208:211], v[50:53]
	v_mfma_i32_16x16x64_i8 v[42:45], v[138:141], v[208:211], v[42:45]
	v_mfma_i32_16x16x64_i8 v[34:37], v[142:145], v[212:215], v[34:37]
	v_mfma_i32_16x16x64_i8 v[26:29], v[138:141], v[212:215], v[26:29]
	v_mfma_i32_16x16x64_i8 v[18:21], v[142:145], v[224:227], v[18:21]
	v_mfma_i32_16x16x64_i8 v[10:13], v[138:141], v[224:227], v[10:13]
	v_mfma_i32_16x16x64_i8 v[6:9], v[142:145], v[228:231], v[6:9]
	v_mfma_i32_16x16x64_i8 v[2:5], v[138:141], v[228:231], v[2:5]
	s_nop 0
	v_mfma_i32_16x16x64_i8 v[50:53], v[130:133], v[216:219], v[50:53]
	v_mfma_i32_16x16x64_i8 v[42:45], v[134:137], v[216:219], v[42:45]
	v_mfma_i32_16x16x64_i8 v[34:37], v[130:133], v[220:223], v[34:37]
	v_mfma_i32_16x16x64_i8 v[26:29], v[134:137], v[220:223], v[26:29]
	v_mfma_i32_16x16x64_i8 v[18:21], v[130:133], v[232:235], v[18:21]
	v_mfma_i32_16x16x64_i8 v[10:13], v[134:137], v[232:235], v[10:13]
	v_mfma_i32_16x16x64_i8 v[6:9], v[130:133], v[236:239], v[6:9]
	v_mfma_i32_16x16x64_i8 v[2:5], v[134:137], v[236:239], v[2:5]
	s_setprio 0
	s_barrier
; #define PG8_STAGE(bufoff, gbase, voff) do { _Pragma("unroll") for (int _i = 0; _i < 2; ++_i) \
;         __builtin_amdgcn_global_load_lds((const unsigned*)((const char*)(gbase) + (voff)[_i]), (LAS unsigned*)(lds + (bufoff) + ldsw + _i * 8192), 16, 0, 0); } while (0)
; #define PG8_LDA(dst, b, h) do { _Pragma("unroll") for (int m = 0; m < 4; ++m) _Pragma("unroll") for (int k = 0; k < 2; ++k) dst[m][k] = *(const LAS bf16x8*)(lds + PG8_SA(b, h) + aoff + m * 2048 + k * 1024); } while (0)
; #define PG8_LDB(dst, b, h) do { _Pragma("unroll") for (int n = 0; n < 2; ++n) _Pragma("unroll") for (int k = 0; k < 2; ++k) dst[n][k] = *(const LAS bf16x8*)(lds + PG8_SB(b, h) + boff + n * 2048 + k * 1024); } while (0)
; #define PG8_MMA(ai, bj, At, Bt) do { __builtin_amdgcn_s_setprio(1); _Pragma("unroll") for (int m = 0; m < 4; ++m) _Pragma("unroll") for (int n = 0; n < 2; ++n) _Pragma("unroll") for (int k = 0; k < 2; ++k) \
;         acc[ai][bj][m][n] = __builtin_amdgcn_mfma_f32_16x16x32_bf16(Bt[n][k], At[m][k], acc[ai][bj][m][n], 0, 0, 0); __builtin_amdgcn_s_setprio(0); } while (0)
; #define PG8_WAIT_V(n) asm volatile("s_waitcnt vmcnt(" #n ")" ::: "memory")
; #define PG8_WAIT_L(n) asm volatile("s_waitcnt lgkmcnt(" #n ")" ::: "memory")
; #define PG8_BAR __builtin_amdgcn_s_barrier()
; #define PG8_SCHED __builtin_amdgcn_sched_barrier(0)
; #define PG8_STAGE(bufoff, gbase, voff) do { _Pragma("unroll") for (int _i = 0; _i < 2; ++_i) \
;         __builtin_amdgcn_global_load_lds((const unsigned*)((const char*)(gbase) + (voff)[_i]), (LAS unsigned*)(lds + (bufoff) + ldsw + _i * 8192), 16, 0, 0); } while (0)
; #define PG8_WAIT_V(n) asm volatile("s_waitcnt vmcnt(" #n ")" ::: "memory")
; #define PG8_WAIT_L(n) asm volatile("s_waitcnt lgkmcnt(" #n ")" ::: "memory")
;     ...
;             PG8_LDB(B0, 1, 0); PG8_LDB(B1, 1, 1); PG8_SCHED; PG8_LDA(At, 1, 0); PG8_STAGE(PG8_SA(0, 1), a2 + hstepA, voffA);
;             PG8_WAIT_V(8); PG8_WAIT_L(0); PG8_BAR; PG8_MMA(0, 0, At, B0); PG8_MMA(0, 1, At, B1); PG8_BAR; PG8_SCHED;
;             PG8_LDA(At, 1, 1); PG8_STAGE(PG8_SB(1, 0), b3, voffB); PG8_STAGE(PG8_SB(1, 1), b3 + hstepB, voffB); PG8_STAGE(PG8_SA(1, 0), a3, voffA);
;             PG8_WAIT_V(8); PG8_WAIT_L(0); PG8_BAR; PG8_MMA(1, 0, At, B0); PG8_MMA(1, 1, At, B1); PG8_BAR; PG8_SCHED;
;         }
;         asm volatile("s_nop 15\n\ts_nop 15" ::: "memory");
;         if (wr == 0) PG8_BAR;
	ds_read_b128 v[130:133], v191
	ds_read_b128 v[134:137], v192
	ds_read_b128 v[138:141], v199
	ds_read_b128 v[142:145], v200
	ds_read_b128 v[146:149], v193
	ds_read_b128 v[150:153], v194
	ds_read_b128 v[154:157], v201
	ds_read_b128 v[158:161], v202
	s_add_u32 s8, s64, 0x40000
	s_addc_u32 s9, s65, 0
	s_mov_b32 m0, s78
	v_lshl_add_u64 v[240:241], s[8:9], 0, v[168:169]
	ds_read_b128 v[208:211], v204 offset:32768
	ds_read_b128 v[212:215], v204 offset:34816
	ds_read_b128 v[216:219], v205 offset:32768
	ds_read_b128 v[220:223], v205 offset:34816
	ds_read_b128 v[224:227], v204 offset:36864
	ds_read_b128 v[228:231], v204 offset:38912
	ds_read_b128 v[232:235], v205 offset:36864
	ds_read_b128 v[236:239], v205 offset:38912
	global_load_lds_dwordx4 v[240:241], off
	v_lshl_add_u64 v[240:241], s[8:9], 0, v[164:165]
	s_mov_b32 m0, s79
	s_nop 0
	global_load_lds_dwordx4 v[240:241], off
	s_waitcnt vmcnt(8)
	s_waitcnt lgkmcnt(0)
	s_barrier
	s_setprio 1
	v_mfma_i32_16x16x64_i8 v[126:129], v[130:133], v[208:211], v[126:129]
	v_mfma_i32_16x16x64_i8 v[122:125], v[138:141], v[208:211], v[122:125]
	v_mfma_i32_16x16x64_i8 v[118:121], v[130:133], v[212:215], v[118:121]
	v_mfma_i32_16x16x64_i8 v[110:113], v[138:141], v[212:215], v[110:113]
	v_mfma_i32_16x16x64_i8 v[102:105], v[130:133], v[224:227], v[102:105]
	v_mfma_i32_16x16x64_i8 v[94:97], v[138:141], v[224:227], v[94:97]
	v_mfma_i32_16x16x64_i8 v[86:89], v[130:133], v[228:231], v[86:89]
	v_mfma_i32_16x16x64_i8 v[78:81], v[138:141], v[228:231], v[78:81]
	s_nop 0
	v_mfma_i32_16x16x64_i8 v[126:129], v[134:137], v[216:219], v[126:129]
	v_mfma_i32_16x16x64_i8 v[122:125], v[142:145], v[216:219], v[122:125]
	v_mfma_i32_16x16x64_i8 v[118:121], v[134:137], v[220:223], v[118:121]
	v_mfma_i32_16x16x64_i8 v[110:113], v[142:145], v[220:223], v[110:113]
	v_mfma_i32_16x16x64_i8 v[102:105], v[134:137], v[232:235], v[102:105]
	v_mfma_i32_16x16x64_i8 v[94:97], v[142:145], v[232:235], v[94:97]
	v_mfma_i32_16x16x64_i8 v[86:89], v[134:137], v[236:239], v[86:89]
	v_mfma_i32_16x16x64_i8 v[78:81], v[142:145], v[236:239], v[78:81]
	s_setprio 0
	s_setprio 1
	v_mfma_i32_16x16x64_i8 v[114:117], v[146:149], v[208:211], v[114:117]
	v_mfma_i32_16x16x64_i8 v[106:109], v[154:157], v[208:211], v[106:109]
	v_mfma_i32_16x16x64_i8 v[98:101], v[146:149], v[212:215], v[98:101]
	v_mfma_i32_16x16x64_i8 v[90:93], v[154:157], v[212:215], v[90:93]
	v_mfma_i32_16x16x64_i8 v[82:85], v[146:149], v[224:227], v[82:85]
	v_mfma_i32_16x16x64_i8 v[74:77], v[154:157], v[224:227], v[74:77]
	v_mfma_i32_16x16x64_i8 v[70:73], v[146:149], v[228:231], v[70:73]
	v_mfma_i32_16x16x64_i8 v[66:69], v[154:157], v[228:231], v[66:69]
	s_nop 0
	v_mfma_i32_16x16x64_i8 v[114:117], v[150:153], v[216:219], v[114:117]
	v_mfma_i32_16x16x64_i8 v[106:109], v[158:161], v[216:219], v[106:109]
	v_mfma_i32_16x16x64_i8 v[98:101], v[150:153], v[220:223], v[98:101]
	v_mfma_i32_16x16x64_i8 v[90:93], v[158:161], v[220:223], v[90:93]
	v_mfma_i32_16x16x64_i8 v[82:85], v[150:153], v[232:235], v[82:85]
	v_mfma_i32_16x16x64_i8 v[74:77], v[158:161], v[232:235], v[74:77]
	v_mfma_i32_16x16x64_i8 v[70:73], v[150:153], v[236:239], v[70:73]
	v_mfma_i32_16x16x64_i8 v[66:69], v[158:161], v[236:239], v[66:69]
	s_setprio 0
	s_barrier
	s_mov_b32 m0, s81
	v_lshl_add_u64 v[178:179], v[178:179], 0, s[38:39]
	s_add_u32 s8, s62, 0x40080
	ds_read_b128 v[208:211], v204 offset:49152
	ds_read_b128 v[212:215], v204 offset:51200
	ds_read_b128 v[216:219], v205 offset:49152
	ds_read_b128 v[220:223], v205 offset:51200
	ds_read_b128 v[224:227], v204 offset:53248
	ds_read_b128 v[228:231], v204 offset:55296
	ds_read_b128 v[232:235], v205 offset:53248
	ds_read_b128 v[236:239], v205 offset:55296
	global_load_lds_dwordx4 v[178:179], off
	v_lshl_add_u64 v[178:179], v[180:181], 0, s[38:39]
	s_mov_b32 m0, s82
	s_addc_u32 s9, s63, 0
	global_load_lds_dwordx4 v[178:179], off
	v_lshl_add_u64 v[178:179], s[8:9], 0, v[166:167]
	s_mov_b32 m0, s85
	s_nop 0
	global_load_lds_dwordx4 v[178:179], off
	v_lshl_add_u64 v[178:179], s[8:9], 0, v[162:163]
	s_mov_b32 m0, s86
	s_nop 0
	global_load_lds_dwordx4 v[178:179], off
	v_lshl_add_u64 v[178:179], v[182:183], 0, s[38:39]
	s_mov_b32 m0, s83
	s_nop 0
	global_load_lds_dwordx4 v[178:179], off
	v_lshl_add_u64 v[178:179], v[184:185], 0, s[38:39]
	s_mov_b32 m0, s84
	s_nop 0
	global_load_lds_dwordx4 v[178:179], off
	s_waitcnt vmcnt(8)
	s_waitcnt lgkmcnt(0)
	s_barrier
	s_setprio 1
	v_mfma_i32_16x16x64_i8 v[62:65], v[130:133], v[208:211], v[62:65]
	v_mfma_i32_16x16x64_i8 v[58:61], v[138:141], v[208:211], v[58:61]
	v_mfma_i32_16x16x64_i8 v[54:57], v[130:133], v[212:215], v[54:57]
	v_mfma_i32_16x16x64_i8 v[46:49], v[138:141], v[212:215], v[46:49]
	v_mfma_i32_16x16x64_i8 v[38:41], v[130:133], v[224:227], v[38:41]
	v_mfma_i32_16x16x64_i8 v[30:33], v[138:141], v[224:227], v[30:33]
	v_mfma_i32_16x16x64_i8 v[22:25], v[130:133], v[228:231], v[22:25]
	v_mfma_i32_16x16x64_i8 v[14:17], v[138:141], v[228:231], v[14:17]
	s_nop 0
	v_mfma_i32_16x16x64_i8 v[62:65], v[134:137], v[216:219], v[62:65]
	v_mfma_i32_16x16x64_i8 v[58:61], v[142:145], v[216:219], v[58:61]
	v_mfma_i32_16x16x64_i8 v[54:57], v[134:137], v[220:223], v[54:57]
	v_mfma_i32_16x16x64_i8 v[46:49], v[142:145], v[220:223], v[46:49]
	v_mfma_i32_16x16x64_i8 v[38:41], v[134:137], v[232:235], v[38:41]
	v_mfma_i32_16x16x64_i8 v[30:33], v[142:145], v[232:235], v[30:33]
	v_mfma_i32_16x16x64_i8 v[22:25], v[134:137], v[236:239], v[22:25]
	v_mfma_i32_16x16x64_i8 v[14:17], v[142:145], v[236:239], v[14:17]
	s_setprio 0
	s_setprio 1
	v_mfma_i32_16x16x64_i8 v[50:53], v[146:149], v[208:211], v[50:53]
	v_mfma_i32_16x16x64_i8 v[42:45], v[154:157], v[208:211], v[42:45]
	v_mfma_i32_16x16x64_i8 v[34:37], v[146:149], v[212:215], v[34:37]
	v_mfma_i32_16x16x64_i8 v[26:29], v[154:157], v[212:215], v[26:29]
	v_mfma_i32_16x16x64_i8 v[18:21], v[146:149], v[224:227], v[18:21]
	v_mfma_i32_16x16x64_i8 v[10:13], v[154:157], v[224:227], v[10:13]
	v_mfma_i32_16x16x64_i8 v[6:9], v[146:149], v[228:231], v[6:9]
	v_mfma_i32_16x16x64_i8 v[2:5], v[154:157], v[228:231], v[2:5]
	s_nop 0
	v_mfma_i32_16x16x64_i8 v[50:53], v[150:153], v[216:219], v[50:53]
	v_mfma_i32_16x16x64_i8 v[42:45], v[158:161], v[216:219], v[42:45]
	v_mfma_i32_16x16x64_i8 v[34:37], v[150:153], v[220:223], v[34:37]
	v_mfma_i32_16x16x64_i8 v[26:29], v[158:161], v[220:223], v[26:29]
	s_add_i32 s92, s92, 2
	s_add_u32 s90, s90, 0x100
	s_addc_u32 s91, s91, 0
	s_cmp_gt_u32 s92, 13
	s_mov_b64 s[60:61], s[58:59]
	v_mfma_i32_16x16x64_i8 v[18:21], v[150:153], v[232:235], v[18:21]
	v_mfma_i32_16x16x64_i8 v[10:13], v[158:161], v[232:235], v[10:13]
	v_mfma_i32_16x16x64_i8 v[6:9], v[150:153], v[236:239], v[6:9]
	v_mfma_i32_16x16x64_i8 v[2:5], v[158:161], v[236:239], v[2:5]
	s_setprio 0
	s_barrier
	s_cbranch_scc0 .LBB0_594
	s_nop 15
	s_nop 15
	s_and_b64 vcc, exec, s[40:41]
	s_cbranch_vccz .LBB0_597
	s_barrier

; #define PG8_STAGE(bufoff, gbase, voff) do { _Pragma("unroll") for (int _i = 0; _i < 2; ++_i) \
;         __builtin_amdgcn_global_load_lds((const unsigned*)((const char*)(gbase) + (voff)[_i]), (LAS unsigned*)(lds + (bufoff) + ldsw + _i * 8192), 16, 0, 0); } while (0)
; #define PG8_LDA(dst, b, h) do { _Pragma("unroll") for (int m = 0; m < 4; ++m) _Pragma("unroll") for (int k = 0; k < 2; ++k) dst[m][k] = *(const LAS bf16x8*)(lds + PG8_SA(b, h) + aoff + m * 2048 + k * 1024); } while (0)
; #define PG8_LDB(dst, b, h) do { _Pragma("unroll") for (int n = 0; n < 2; ++n) _Pragma("unroll") for (int k = 0; k < 2; ++k) dst[n][k] = *(const LAS bf16x8*)(lds + PG8_SB(b, h) + boff + n * 2048 + k * 1024); } while (0)
; #define PG8_MMA(ai, bj, At, Bt) do { __builtin_amdgcn_s_setprio(1); _Pragma("unroll") for (int m = 0; m < 4; ++m) _Pragma("unroll") for (int n = 0; n < 2; ++n) _Pragma("unroll") for (int k = 0; k < 2; ++k) \
;         acc[ai][bj][m][n] = __builtin_amdgcn_mfma_f32_16x16x32_bf16(Bt[n][k], At[m][k], acc[ai][bj][m][n], 0, 0, 0); __builtin_amdgcn_s_setprio(0); } while (0)
; #define PG8_WAIT_V(n) asm volatile("s_waitcnt vmcnt(" #n ")" ::: "memory")
; #define PG8_WAIT_L(n) asm volatile("s_waitcnt lgkmcnt(" #n ")" ::: "memory")
; #define PG8_BAR __builtin_amdgcn_s_barrier()
; #define PG8_SCHED __builtin_amdgcn_sched_barrier(0)
; #define PG8_STAGE(bufoff, gbase, voff) do { _Pragma("unroll") for (int _i = 0; _i < 2; ++_i) \
;         __builtin_amdgcn_global_load_lds((const unsigned*)((const char*)(gbase) + (voff)[_i]), (LAS unsigned*)(lds + (bufoff) + ldsw + _i * 8192), 16, 0, 0); } while (0)
; #define PG8_LDA(dst, b, h) do { _Pragma("unroll") for (int m = 0; m < 4; ++m) PG8_LD1(dst[m], PG8_SA(b, h) + aoff0 + m * 2048, PG8_SA(b, h) + aoff1 + m * 2048); } while (0)
; #define PG8_WAIT_V(n) asm volatile("s_waitcnt vmcnt(" #n ")" ::: "memory")
;     ...
;             PG8_LDB(B0, 0, 0); PG8_LDB(B1, 0, 1); PG8_SCHED; PG8_LDA(At, 0, 0); PG8_STAGE(PG8_SA(1, 1), a1 + hstepA, voffA);
;             PG8_WAIT_V(8); PG8_WAIT_L(0); PG8_BAR; PG8_MMA(0, 0, At, B0); PG8_MMA(0, 1, At, B1); PG8_BAR; PG8_SCHED;
;             PG8_LDA(At, 0, 1); PG8_STAGE(PG8_SB(0, 0), b2, voffB); PG8_STAGE(PG8_SB(0, 1), b2 + hstepB, voffB); PG8_STAGE(PG8_SA(0, 0), a2, voffA);
;             PG8_WAIT_V(8); PG8_WAIT_L(0); PG8_BAR; PG8_MMA(1, 0, At, B0); PG8_MMA(1, 1, At, B1); PG8_BAR; PG8_SCHED;
.LBB0_667:
	ds_read_b128 v[158:161], v217
	ds_read_b128 v[146:149], v218
	ds_read_b128 v[154:157], v225
	ds_read_b128 v[150:153], v226
	ds_read_b128 v[142:145], v219
	ds_read_b128 v[130:133], v220
	ds_read_b128 v[138:141], v227
	ds_read_b128 v[134:137], v228
	s_add_u32 s56, s54, 0x100
	s_addc_u32 s57, s55, 0
	s_cmp_eq_u32 s88, 52
	s_cselect_b32 s61, s82, s57
	s_cselect_b32 s60, s83, s56
	s_cselect_b32 s59, s84, s87
	s_cselect_b32 s58, s85, s86
	v_lshl_add_u64 v[206:207], s[54:55], 0, v[166:167]
	s_add_i32 m0, s0, 0xc000
	ds_read_b128 v[174:177], v234
	ds_read_b128 v[178:181], v234 offset:2048
	ds_read_b128 v[182:185], v235
	ds_read_b128 v[186:189], v235 offset:2048
	ds_read_b128 v[190:193], v234 offset:4096
	ds_read_b128 v[194:197], v234 offset:6144
	ds_read_b128 v[198:201], v235 offset:4096
	ds_read_b128 v[202:205], v235 offset:6144
	global_load_lds_dwordx4 v[206:207], off
	v_lshl_add_u64 v[206:207], s[54:55], 0, v[168:169]
	s_add_i32 m0, s0, 0xe000
	s_nop 0
	global_load_lds_dwordx4 v[206:207], off
	s_waitcnt vmcnt(8)
	s_waitcnt lgkmcnt(0)
	s_barrier
	s_setprio 1
	v_mfma_i32_16x16x64_i8 v[126:129], v[158:161], v[174:177], v[126:129]
	v_mfma_i32_16x16x64_i8 v[122:125], v[154:157], v[174:177], v[122:125]
	v_mfma_i32_16x16x64_i8 v[118:121], v[158:161], v[178:181], v[118:121]
	v_mfma_i32_16x16x64_i8 v[114:117], v[154:157], v[178:181], v[114:117]
	v_mfma_i32_16x16x64_i8 v[110:113], v[158:161], v[190:193], v[110:113]
	v_mfma_i32_16x16x64_i8 v[106:109], v[154:157], v[190:193], v[106:109]
	v_mfma_i32_16x16x64_i8 v[102:105], v[158:161], v[194:197], v[102:105]
	v_mfma_i32_16x16x64_i8 v[98:101], v[154:157], v[194:197], v[98:101]
	s_nop 0
	v_mfma_i32_16x16x64_i8 v[126:129], v[146:149], v[182:185], v[126:129]
	v_mfma_i32_16x16x64_i8 v[122:125], v[150:153], v[182:185], v[122:125]
	v_mfma_i32_16x16x64_i8 v[118:121], v[146:149], v[186:189], v[118:121]
	v_mfma_i32_16x16x64_i8 v[114:117], v[150:153], v[186:189], v[114:117]
	v_mfma_i32_16x16x64_i8 v[110:113], v[146:149], v[198:201], v[110:113]
	v_mfma_i32_16x16x64_i8 v[106:109], v[150:153], v[198:201], v[106:109]
	v_mfma_i32_16x16x64_i8 v[102:105], v[146:149], v[202:205], v[102:105]
	v_mfma_i32_16x16x64_i8 v[98:101], v[150:153], v[202:205], v[98:101]
	s_setprio 0
	s_setprio 1
	v_mfma_i32_16x16x64_i8 v[94:97], v[142:145], v[174:177], v[94:97]
	v_mfma_i32_16x16x64_i8 v[90:93], v[138:141], v[174:177], v[90:93]
	v_mfma_i32_16x16x64_i8 v[86:89], v[142:145], v[178:181], v[86:89]
	v_mfma_i32_16x16x64_i8 v[82:85], v[138:141], v[178:181], v[82:85]
	v_mfma_i32_16x16x64_i8 v[78:81], v[142:145], v[190:193], v[78:81]
	v_mfma_i32_16x16x64_i8 v[74:77], v[138:141], v[190:193], v[74:77]
	v_mfma_i32_16x16x64_i8 v[70:73], v[142:145], v[194:197], v[70:73]
	v_mfma_i32_16x16x64_i8 v[66:69], v[138:141], v[194:197], v[66:69]
	s_nop 0
	v_mfma_i32_16x16x64_i8 v[94:97], v[130:133], v[182:185], v[94:97]
	v_mfma_i32_16x16x64_i8 v[90:93], v[134:137], v[182:185], v[90:93]
	v_mfma_i32_16x16x64_i8 v[86:89], v[130:133], v[186:189], v[86:89]
	v_mfma_i32_16x16x64_i8 v[82:85], v[134:137], v[186:189], v[82:85]
	v_mfma_i32_16x16x64_i8 v[78:81], v[130:133], v[198:201], v[78:81]
	v_mfma_i32_16x16x64_i8 v[74:77], v[134:137], v[198:201], v[74:77]
	v_mfma_i32_16x16x64_i8 v[70:73], v[130:133], v[202:205], v[70:73]
	v_mfma_i32_16x16x64_i8 v[66:69], v[134:137], v[202:205], v[66:69]
	s_setprio 0
	s_barrier
	s_mov_b32 m0, s1
	v_lshl_add_u64 v[174:175], s[58:59], 0, v[164:165]
	s_add_u32 s8, s58, 0xe0000
	ds_read_b128 v[182:185], v234 offset:16384
	ds_read_b128 v[186:189], v234 offset:18432
	ds_read_b128 v[190:193], v235 offset:16384
	ds_read_b128 v[194:197], v235 offset:18432
	ds_read_b128 v[198:201], v234 offset:20480
	ds_read_b128 v[202:205], v234 offset:22528
	ds_read_b128 v[206:209], v235 offset:20480
	ds_read_b128 v[210:213], v235 offset:22528
	global_load_lds_dwordx4 v[174:175], off
	v_lshl_add_u64 v[176:177], s[58:59], 0, v[162:163]
	s_mov_b32 m0, s10
	s_addc_u32 s9, s59, 0
	global_load_lds_dwordx4 v[176:177], off
	v_lshl_add_u64 v[178:179], s[8:9], 0, v[164:165]
	s_mov_b32 m0, s11
	v_lshl_add_u64 v[180:181], s[60:61], 0, v[162:163]
	global_load_lds_dwordx4 v[178:179], off
	v_lshl_add_u64 v[178:179], s[8:9], 0, v[162:163]
	s_mov_b32 m0, s24
	s_nop 0
	global_load_lds_dwordx4 v[178:179], off
	v_lshl_add_u64 v[178:179], s[60:61], 0, v[164:165]
	s_mov_b32 m0, s0
	s_nop 0
	global_load_lds_dwordx4 v[178:179], off
	s_mov_b32 m0, s25
	s_nop 0
	global_load_lds_dwordx4 v[180:181], off
	s_waitcnt vmcnt(8)
	s_waitcnt lgkmcnt(0)
	s_barrier
	s_setprio 1
	v_mfma_i32_16x16x64_i8 v[62:65], v[158:161], v[182:185], v[62:65]
	v_mfma_i32_16x16x64_i8 v[58:61], v[154:157], v[182:185], v[58:61]
	v_mfma_i32_16x16x64_i8 v[54:57], v[158:161], v[186:189], v[54:57]
	v_mfma_i32_16x16x64_i8 v[50:53], v[154:157], v[186:189], v[50:53]
	v_mfma_i32_16x16x64_i8 v[46:49], v[158:161], v[198:201], v[46:49]
	v_mfma_i32_16x16x64_i8 v[42:45], v[154:157], v[198:201], v[42:45]
	v_mfma_i32_16x16x64_i8 v[38:41], v[158:161], v[202:205], v[38:41]
	v_mfma_i32_16x16x64_i8 v[34:37], v[154:157], v[202:205], v[34:37]
	s_nop 0
	v_mfma_i32_16x16x64_i8 v[62:65], v[146:149], v[190:193], v[62:65]
	v_mfma_i32_16x16x64_i8 v[58:61], v[150:153], v[190:193], v[58:61]
	v_mfma_i32_16x16x64_i8 v[54:57], v[146:149], v[194:197], v[54:57]
	v_mfma_i32_16x16x64_i8 v[50:53], v[150:153], v[194:197], v[50:53]
	v_mfma_i32_16x16x64_i8 v[46:49], v[146:149], v[206:209], v[46:49]
	v_mfma_i32_16x16x64_i8 v[42:45], v[150:153], v[206:209], v[42:45]
	v_mfma_i32_16x16x64_i8 v[38:41], v[146:149], v[210:213], v[38:41]
	v_mfma_i32_16x16x64_i8 v[34:37], v[150:153], v[210:213], v[34:37]
	s_setprio 0
	s_setprio 1
	v_mfma_i32_16x16x64_i8 v[30:33], v[142:145], v[182:185], v[30:33]
	v_mfma_i32_16x16x64_i8 v[26:29], v[138:141], v[182:185], v[26:29]
	v_mfma_i32_16x16x64_i8 v[22:25], v[142:145], v[186:189], v[22:25]
	v_mfma_i32_16x16x64_i8 v[18:21], v[138:141], v[186:189], v[18:21]
	v_mfma_i32_16x16x64_i8 v[14:17], v[142:145], v[198:201], v[14:17]
	v_mfma_i32_16x16x64_i8 v[10:13], v[138:141], v[198:201], v[10:13]
	v_mfma_i32_16x16x64_i8 v[6:9], v[142:145], v[202:205], v[6:9]
	v_mfma_i32_16x16x64_i8 v[2:5], v[138:141], v[202:205], v[2:5]
	s_nop 0
	v_mfma_i32_16x16x64_i8 v[30:33], v[130:133], v[190:193], v[30:33]
	v_mfma_i32_16x16x64_i8 v[26:29], v[134:137], v[190:193], v[26:29]
	v_mfma_i32_16x16x64_i8 v[22:25], v[130:133], v[194:197], v[22:25]
	v_mfma_i32_16x16x64_i8 v[18:21], v[134:137], v[194:197], v[18:21]
	v_mfma_i32_16x16x64_i8 v[14:17], v[130:133], v[206:209], v[14:17]
	v_mfma_i32_16x16x64_i8 v[10:13], v[134:137], v[206:209], v[10:13]
	v_mfma_i32_16x16x64_i8 v[6:9], v[130:133], v[210:213], v[6:9]
	v_mfma_i32_16x16x64_i8 v[2:5], v[134:137], v[210:213], v[2:5]
	s_setprio 0
	s_barrier
; #define PG8_STAGE(bufoff, gbase, voff) do { _Pragma("unroll") for (int _i = 0; _i < 2; ++_i) \
;         __builtin_amdgcn_global_load_lds((const unsigned*)((const char*)(gbase) + (voff)[_i]), (LAS unsigned*)(lds + (bufoff) + ldsw + _i * 8192), 16, 0, 0); } while (0)
; #define PG8_LDA(dst, b, h) do { _Pragma("unroll") for (int m = 0; m < 4; ++m) _Pragma("unroll") for (int k = 0; k < 2; ++k) dst[m][k] = *(const LAS bf16x8*)(lds + PG8_SA(b, h) + aoff + m * 2048 + k * 1024); } while (0)
; #define PG8_LDB(dst, b, h) do { _Pragma("unroll") for (int n = 0; n < 2; ++n) _Pragma("unroll") for (int k = 0; k < 2; ++k) dst[n][k] = *(const LAS bf16x8*)(lds + PG8_SB(b, h) + boff + n * 2048 + k * 1024); } while (0)
; #define PG8_MMA(ai, bj, At, Bt) do { __builtin_amdgcn_s_setprio(1); _Pragma("unroll") for (int m = 0; m < 4; ++m) _Pragma("unroll") for (int n = 0; n < 2; ++n) _Pragma("unroll") for (int k = 0; k < 2; ++k) \
;         acc[ai][bj][m][n] = __builtin_amdgcn_mfma_f32_16x16x32_bf16(Bt[n][k], At[m][k], acc[ai][bj][m][n], 0, 0, 0); __builtin_amdgcn_s_setprio(0); } while (0)
; #define PG8_WAIT_V(n) asm volatile("s_waitcnt vmcnt(" #n ")" ::: "memory")
; #define PG8_WAIT_L(n) asm volatile("s_waitcnt lgkmcnt(" #n ")" ::: "memory")
; #define PG8_BAR __builtin_amdgcn_s_barrier()
; #define PG8_SCHED __builtin_amdgcn_sched_barrier(0)
; #define PG8_STAGE(bufoff, gbase, voff) do { _Pragma("unroll") for (int _i = 0; _i < 2; ++_i) \
;         __builtin_amdgcn_global_load_lds((const unsigned*)((const char*)(gbase) + (voff)[_i]), (LAS unsigned*)(lds + (bufoff) + ldsw + _i * 8192), 16, 0, 0); } while (0)
; #define PG8_WAIT_V(n) asm volatile("s_waitcnt vmcnt(" #n ")" ::: "memory")
; #define PG8_WAIT_L(n) asm volatile("s_waitcnt lgkmcnt(" #n ")" ::: "memory")
;     ...
;             PG8_LDB(B0, 1, 0); PG8_LDB(B1, 1, 1); PG8_SCHED; PG8_LDA(At, 1, 0); PG8_STAGE(PG8_SA(0, 1), a2 + hstepA, voffA);
;             PG8_WAIT_V(8); PG8_WAIT_L(0); PG8_BAR; PG8_MMA(0, 0, At, B0); PG8_MMA(0, 1, At, B1); PG8_BAR; PG8_SCHED;
;             PG8_LDA(At, 1, 1); PG8_STAGE(PG8_SB(1, 0), b3, voffB); PG8_STAGE(PG8_SB(1, 1), b3 + hstepB, voffB); PG8_STAGE(PG8_SA(1, 0), a3, voffA);
;             PG8_WAIT_V(8); PG8_WAIT_L(0); PG8_BAR; PG8_MMA(1, 0, At, B0); PG8_MMA(1, 1, At, B1); PG8_BAR; PG8_SCHED;
;         }
;         asm volatile("s_nop 15\n\ts_nop 15" ::: "memory");
;         if (wr == 0) PG8_BAR;
	ds_read_b128 v[130:133], v221
	ds_read_b128 v[134:137], v222
	ds_read_b128 v[138:141], v229
	ds_read_b128 v[142:145], v230
	ds_read_b128 v[146:149], v223
	ds_read_b128 v[150:153], v224
	ds_read_b128 v[154:157], v231
	ds_read_b128 v[158:161], v232
	s_add_u32 s8, s60, 0xe0000
	s_addc_u32 s9, s61, 0
	s_mov_b32 m0, s33
	v_lshl_add_u64 v[214:215], s[8:9], 0, v[164:165]
	ds_read_b128 v[182:185], v234 offset:32768
	ds_read_b128 v[186:189], v234 offset:34816
	ds_read_b128 v[190:193], v235 offset:32768
	ds_read_b128 v[194:197], v235 offset:34816
	ds_read_b128 v[198:201], v234 offset:36864
	ds_read_b128 v[202:205], v234 offset:38912
	ds_read_b128 v[206:209], v235 offset:36864
	ds_read_b128 v[210:213], v235 offset:38912
	global_load_lds_dwordx4 v[214:215], off
	v_lshl_add_u64 v[214:215], s[8:9], 0, v[162:163]
	s_mov_b32 m0, s43
	s_nop 0
	global_load_lds_dwordx4 v[214:215], off
	s_waitcnt vmcnt(8)
	s_waitcnt lgkmcnt(0)
	s_barrier
	s_setprio 1
	v_mfma_i32_16x16x64_i8 v[126:129], v[130:133], v[182:185], v[126:129]
	v_mfma_i32_16x16x64_i8 v[122:125], v[138:141], v[182:185], v[122:125]
	v_mfma_i32_16x16x64_i8 v[118:121], v[130:133], v[186:189], v[118:121]
	v_mfma_i32_16x16x64_i8 v[114:117], v[138:141], v[186:189], v[114:117]
	v_mfma_i32_16x16x64_i8 v[110:113], v[130:133], v[198:201], v[110:113]
	v_mfma_i32_16x16x64_i8 v[106:109], v[138:141], v[198:201], v[106:109]
	v_mfma_i32_16x16x64_i8 v[102:105], v[130:133], v[202:205], v[102:105]
	v_mfma_i32_16x16x64_i8 v[98:101], v[138:141], v[202:205], v[98:101]
	s_nop 0
	v_mfma_i32_16x16x64_i8 v[126:129], v[134:137], v[190:193], v[126:129]
	v_mfma_i32_16x16x64_i8 v[122:125], v[142:145], v[190:193], v[122:125]
	v_mfma_i32_16x16x64_i8 v[118:121], v[134:137], v[194:197], v[118:121]
	v_mfma_i32_16x16x64_i8 v[114:117], v[142:145], v[194:197], v[114:117]
	v_mfma_i32_16x16x64_i8 v[110:113], v[134:137], v[206:209], v[110:113]
	v_mfma_i32_16x16x64_i8 v[106:109], v[142:145], v[206:209], v[106:109]
	v_mfma_i32_16x16x64_i8 v[102:105], v[134:137], v[210:213], v[102:105]
	v_mfma_i32_16x16x64_i8 v[98:101], v[142:145], v[210:213], v[98:101]
	s_setprio 0
	s_setprio 1
	v_mfma_i32_16x16x64_i8 v[94:97], v[146:149], v[182:185], v[94:97]
	v_mfma_i32_16x16x64_i8 v[90:93], v[154:157], v[182:185], v[90:93]
	v_mfma_i32_16x16x64_i8 v[86:89], v[146:149], v[186:189], v[86:89]
	v_mfma_i32_16x16x64_i8 v[82:85], v[154:157], v[186:189], v[82:85]
	v_mfma_i32_16x16x64_i8 v[78:81], v[146:149], v[198:201], v[78:81]
	v_mfma_i32_16x16x64_i8 v[74:77], v[154:157], v[198:201], v[74:77]
	v_mfma_i32_16x16x64_i8 v[70:73], v[146:149], v[202:205], v[70:73]
	v_mfma_i32_16x16x64_i8 v[66:69], v[154:157], v[202:205], v[66:69]
	s_nop 0
	v_mfma_i32_16x16x64_i8 v[94:97], v[150:153], v[190:193], v[94:97]
	v_mfma_i32_16x16x64_i8 v[90:93], v[158:161], v[190:193], v[90:93]
	v_mfma_i32_16x16x64_i8 v[86:89], v[150:153], v[194:197], v[86:89]
	v_mfma_i32_16x16x64_i8 v[82:85], v[158:161], v[194:197], v[82:85]
	v_mfma_i32_16x16x64_i8 v[78:81], v[150:153], v[206:209], v[78:81]
	v_mfma_i32_16x16x64_i8 v[74:77], v[158:161], v[206:209], v[74:77]
	v_mfma_i32_16x16x64_i8 v[70:73], v[150:153], v[210:213], v[70:73]
	v_mfma_i32_16x16x64_i8 v[66:69], v[158:161], v[210:213], v[66:69]
	s_setprio 0
	s_barrier
	s_mov_b32 m0, s63
	v_lshl_add_u64 v[174:175], v[174:175], 0, s[38:39]
	s_add_u32 s8, s58, 0xe0080
	ds_read_b128 v[182:185], v234 offset:49152
	ds_read_b128 v[186:189], v234 offset:51200
	ds_read_b128 v[190:193], v235 offset:49152
	ds_read_b128 v[194:197], v235 offset:51200
	ds_read_b128 v[198:201], v234 offset:53248
	ds_read_b128 v[202:205], v234 offset:55296
	ds_read_b128 v[206:209], v235 offset:53248
	ds_read_b128 v[210:213], v235 offset:55296
	global_load_lds_dwordx4 v[174:175], off
	v_lshl_add_u64 v[174:175], v[176:177], 0, s[38:39]
	s_mov_b32 m0, s64
	s_addc_u32 s9, s59, 0
	global_load_lds_dwordx4 v[174:175], off
	v_lshl_add_u64 v[174:175], s[8:9], 0, v[164:165]
	s_mov_b32 m0, s67
	s_nop 0
	global_load_lds_dwordx4 v[174:175], off
	v_lshl_add_u64 v[174:175], s[8:9], 0, v[162:163]
	s_mov_b32 m0, s75
	s_nop 0
	global_load_lds_dwordx4 v[174:175], off
	v_lshl_add_u64 v[174:175], v[178:179], 0, s[38:39]
	s_mov_b32 m0, s65
	s_nop 0
	global_load_lds_dwordx4 v[174:175], off
	v_lshl_add_u64 v[174:175], v[180:181], 0, s[38:39]
	s_mov_b32 m0, s66
	s_nop 0
	global_load_lds_dwordx4 v[174:175], off
	s_waitcnt vmcnt(8)
	s_waitcnt lgkmcnt(0)
	s_barrier
	s_setprio 1
	v_mfma_i32_16x16x64_i8 v[62:65], v[130:133], v[182:185], v[62:65]
	v_mfma_i32_16x16x64_i8 v[58:61], v[138:141], v[182:185], v[58:61]
	v_mfma_i32_16x16x64_i8 v[54:57], v[130:133], v[186:189], v[54:57]
	v_mfma_i32_16x16x64_i8 v[50:53], v[138:141], v[186:189], v[50:53]
	v_mfma_i32_16x16x64_i8 v[46:49], v[130:133], v[198:201], v[46:49]
	v_mfma_i32_16x16x64_i8 v[42:45], v[138:141], v[198:201], v[42:45]
	v_mfma_i32_16x16x64_i8 v[38:41], v[130:133], v[202:205], v[38:41]
	v_mfma_i32_16x16x64_i8 v[34:37], v[138:141], v[202:205], v[34:37]
	s_nop 0
	v_mfma_i32_16x16x64_i8 v[62:65], v[134:137], v[190:193], v[62:65]
	v_mfma_i32_16x16x64_i8 v[58:61], v[142:145], v[190:193], v[58:61]
	v_mfma_i32_16x16x64_i8 v[54:57], v[134:137], v[194:197], v[54:57]
	v_mfma_i32_16x16x64_i8 v[50:53], v[142:145], v[194:197], v[50:53]
	v_mfma_i32_16x16x64_i8 v[46:49], v[134:137], v[206:209], v[46:49]
	v_mfma_i32_16x16x64_i8 v[42:45], v[142:145], v[206:209], v[42:45]
	v_mfma_i32_16x16x64_i8 v[38:41], v[134:137], v[210:213], v[38:41]
	v_mfma_i32_16x16x64_i8 v[34:37], v[142:145], v[210:213], v[34:37]
	s_setprio 0
	s_setprio 1
	v_mfma_i32_16x16x64_i8 v[30:33], v[146:149], v[182:185], v[30:33]
	v_mfma_i32_16x16x64_i8 v[26:29], v[154:157], v[182:185], v[26:29]
	v_mfma_i32_16x16x64_i8 v[22:25], v[146:149], v[186:189], v[22:25]
	v_mfma_i32_16x16x64_i8 v[18:21], v[154:157], v[186:189], v[18:21]
	v_mfma_i32_16x16x64_i8 v[14:17], v[146:149], v[198:201], v[14:17]
	v_mfma_i32_16x16x64_i8 v[10:13], v[154:157], v[198:201], v[10:13]
	v_mfma_i32_16x16x64_i8 v[6:9], v[146:149], v[202:205], v[6:9]
	v_mfma_i32_16x16x64_i8 v[2:5], v[154:157], v[202:205], v[2:5]
	s_nop 0
	v_mfma_i32_16x16x64_i8 v[30:33], v[150:153], v[190:193], v[30:33]
	v_mfma_i32_16x16x64_i8 v[26:29], v[158:161], v[190:193], v[26:29]
	v_mfma_i32_16x16x64_i8 v[22:25], v[150:153], v[194:197], v[22:25]
	v_mfma_i32_16x16x64_i8 v[18:21], v[158:161], v[194:197], v[18:21]
	s_add_i32 s88, s88, 2
	s_add_u32 s86, s86, 0x100
	s_addc_u32 s87, s87, 0
	s_cmp_gt_u32 s88, 53
	s_mov_b64 s[54:55], s[56:57]
	v_mfma_i32_16x16x64_i8 v[14:17], v[150:153], v[206:209], v[14:17]
	v_mfma_i32_16x16x64_i8 v[10:13], v[158:161], v[206:209], v[10:13]
	v_mfma_i32_16x16x64_i8 v[6:9], v[150:153], v[210:213], v[6:9]
	v_mfma_i32_16x16x64_i8 v[2:5], v[158:161], v[210:213], v[2:5]
	s_setprio 0
	s_barrier
	s_cbranch_scc0 .LBB0_667
	s_nop 15
	s_nop 15
	s_and_b64 vcc, exec, s[40:41]
	s_cbranch_vccz .LBB0_670
	s_barrier

; #define PG8_STAGE(bufoff, gbase, voff) do { _Pragma("unroll") for (int _i = 0; _i < 2; ++_i) \
;         __builtin_amdgcn_global_load_lds((const unsigned*)((const char*)(gbase) + (voff)[_i]), (LAS unsigned*)(lds + (bufoff) + ldsw + _i * 8192), 16, 0, 0); } while (0)
; #define PG8_LDA(dst, b, h) do { _Pragma("unroll") for (int m = 0; m < 4; ++m) _Pragma("unroll") for (int k = 0; k < 2; ++k) dst[m][k] = *(const LAS bf16x8*)(lds + PG8_SA(b, h) + aoff + m * 2048 + k * 1024); } while (0)
; #define PG8_LDB(dst, b, h) do { _Pragma("unroll") for (int n = 0; n < 2; ++n) _Pragma("unroll") for (int k = 0; k < 2; ++k) dst[n][k] = *(const LAS bf16x8*)(lds + PG8_SB(b, h) + boff + n * 2048 + k * 1024); } while (0)
; #define PG8_MMA(ai, bj, At, Bt) do { __builtin_amdgcn_s_setprio(1); _Pragma("unroll") for (int m = 0; m < 4; ++m) _Pragma("unroll") for (int n = 0; n < 2; ++n) _Pragma("unroll") for (int k = 0; k < 2; ++k) \
;         acc[ai][bj][m][n] = __builtin_amdgcn_mfma_f32_16x16x32_bf16(Bt[n][k], At[m][k], acc[ai][bj][m][n], 0, 0, 0); __builtin_amdgcn_s_setprio(0); } while (0)
; #define PG8_WAIT_V(n) asm volatile("s_waitcnt vmcnt(" #n ")" ::: "memory")
; #define PG8_WAIT_L(n) asm volatile("s_waitcnt lgkmcnt(" #n ")" ::: "memory")
; #define PG8_BAR __builtin_amdgcn_s_barrier()
; #define PG8_SCHED __builtin_amdgcn_sched_barrier(0)
; #define PG8_STAGE(bufoff, gbase, voff) do { _Pragma("unroll") for (int _i = 0; _i < 2; ++_i) \
;         __builtin_amdgcn_global_load_lds((const unsigned*)((const char*)(gbase) + (voff)[_i]), (LAS unsigned*)(lds + (bufoff) + ldsw + _i * 8192), 16, 0, 0); } while (0)
; #define PG8_LDA(dst, b, h) do { _Pragma("unroll") for (int m = 0; m < 4; ++m) PG8_LD1(dst[m], PG8_SA(b, h) + aoff0 + m * 2048, PG8_SA(b, h) + aoff1 + m * 2048); } while (0)
; #define PG8_WAIT_V(n) asm volatile("s_waitcnt vmcnt(" #n ")" ::: "memory")
;     ...
;             PG8_LDB(B0, 0, 0); PG8_LDB(B1, 0, 1); PG8_SCHED; PG8_LDA(At, 0, 0); PG8_STAGE(PG8_SA(1, 1), a1 + hstepA, voffA);
;             PG8_WAIT_V(8); PG8_WAIT_L(0); PG8_BAR; PG8_MMA(0, 0, At, B0); PG8_MMA(0, 1, At, B1); PG8_BAR; PG8_SCHED;
;             PG8_LDA(At, 0, 1); PG8_STAGE(PG8_SB(0, 0), b2, voffB); PG8_STAGE(PG8_SB(0, 1), b2 + hstepB, voffB); PG8_STAGE(PG8_SA(0, 0), a2, voffA);
;             PG8_WAIT_V(8); PG8_WAIT_L(0); PG8_BAR; PG8_MMA(1, 0, At, B0); PG8_MMA(1, 1, At, B1); PG8_BAR; PG8_SCHED;
.LBB0_796:
	ds_read_b128 v[158:161], v187
	ds_read_b128 v[146:149], v188
	ds_read_b128 v[154:157], v195
	ds_read_b128 v[150:153], v196
	ds_read_b128 v[142:145], v189
	ds_read_b128 v[130:133], v190
	ds_read_b128 v[138:141], v197
	ds_read_b128 v[134:137], v198
	s_add_u32 s60, s58, 0x100
	s_addc_u32 s61, s59, 0
	s_cmp_eq_u32 s87, 12
	s_cselect_b32 s65, s45, s61
	s_cselect_b32 s64, s47, s60
	s_cselect_b32 s63, s83, s86
	s_cselect_b32 s62, s84, s85
	v_lshl_add_u64 v[230:231], s[58:59], 0, v[170:171]
	s_add_i32 m0, s0, 0xc000
	ds_read_b128 v[178:181], v204
	ds_read_b128 v[182:185], v204 offset:2048
	ds_read_b128 v[206:209], v205
	ds_read_b128 v[210:213], v205 offset:2048
	ds_read_b128 v[214:217], v204 offset:4096
	ds_read_b128 v[218:221], v204 offset:6144
	ds_read_b128 v[222:225], v205 offset:4096
	ds_read_b128 v[226:229], v205 offset:6144
	global_load_lds_dwordx4 v[230:231], off
	v_lshl_add_u64 v[230:231], s[58:59], 0, v[172:173]
	s_add_i32 m0, s0, 0xe000
	s_nop 0
	global_load_lds_dwordx4 v[230:231], off
	s_waitcnt vmcnt(8)
	s_waitcnt lgkmcnt(0)
	s_barrier
	s_setprio 1
	v_mfma_i32_16x16x64_i8 v[126:129], v[158:161], v[178:181], v[126:129]
	v_mfma_i32_16x16x64_i8 v[122:125], v[154:157], v[178:181], v[122:125]
	v_mfma_i32_16x16x64_i8 v[118:121], v[158:161], v[182:185], v[118:121]
	v_mfma_i32_16x16x64_i8 v[114:117], v[154:157], v[182:185], v[114:117]
	v_mfma_i32_16x16x64_i8 v[110:113], v[158:161], v[214:217], v[110:113]
	v_mfma_i32_16x16x64_i8 v[106:109], v[154:157], v[214:217], v[106:109]
	v_mfma_i32_16x16x64_i8 v[102:105], v[158:161], v[218:221], v[102:105]
	v_mfma_i32_16x16x64_i8 v[98:101], v[154:157], v[218:221], v[98:101]
	s_nop 0
	v_mfma_i32_16x16x64_i8 v[126:129], v[146:149], v[206:209], v[126:129]
	v_mfma_i32_16x16x64_i8 v[122:125], v[150:153], v[206:209], v[122:125]
	v_mfma_i32_16x16x64_i8 v[118:121], v[146:149], v[210:213], v[118:121]
	v_mfma_i32_16x16x64_i8 v[114:117], v[150:153], v[210:213], v[114:117]
	v_mfma_i32_16x16x64_i8 v[110:113], v[146:149], v[222:225], v[110:113]
	v_mfma_i32_16x16x64_i8 v[106:109], v[150:153], v[222:225], v[106:109]
	v_mfma_i32_16x16x64_i8 v[102:105], v[146:149], v[226:229], v[102:105]
	v_mfma_i32_16x16x64_i8 v[98:101], v[150:153], v[226:229], v[98:101]
	s_setprio 0
	s_setprio 1
	v_mfma_i32_16x16x64_i8 v[94:97], v[142:145], v[178:181], v[94:97]
	v_mfma_i32_16x16x64_i8 v[90:93], v[138:141], v[178:181], v[90:93]
	v_mfma_i32_16x16x64_i8 v[86:89], v[142:145], v[182:185], v[86:89]
	v_mfma_i32_16x16x64_i8 v[82:85], v[138:141], v[182:185], v[82:85]
	v_mfma_i32_16x16x64_i8 v[78:81], v[142:145], v[214:217], v[78:81]
	v_mfma_i32_16x16x64_i8 v[74:77], v[138:141], v[214:217], v[74:77]
	v_mfma_i32_16x16x64_i8 v[70:73], v[142:145], v[218:221], v[70:73]
	v_mfma_i32_16x16x64_i8 v[66:69], v[138:141], v[218:221], v[66:69]
	s_nop 0
	v_mfma_i32_16x16x64_i8 v[94:97], v[130:133], v[206:209], v[94:97]
	v_mfma_i32_16x16x64_i8 v[90:93], v[134:137], v[206:209], v[90:93]
	v_mfma_i32_16x16x64_i8 v[86:89], v[130:133], v[210:213], v[86:89]
	v_mfma_i32_16x16x64_i8 v[82:85], v[134:137], v[210:213], v[82:85]
	v_mfma_i32_16x16x64_i8 v[78:81], v[130:133], v[222:225], v[78:81]
	v_mfma_i32_16x16x64_i8 v[74:77], v[134:137], v[222:225], v[74:77]
	v_mfma_i32_16x16x64_i8 v[70:73], v[130:133], v[226:229], v[70:73]
	v_mfma_i32_16x16x64_i8 v[66:69], v[134:137], v[226:229], v[66:69]
	s_setprio 0
	s_barrier
	s_mov_b32 m0, s1
	v_lshl_add_u64 v[178:179], s[62:63], 0, v[166:167]
	s_add_u32 s8, s62, 0x40000
	ds_read_b128 v[206:209], v204 offset:16384
	ds_read_b128 v[210:213], v204 offset:18432
	ds_read_b128 v[214:217], v205 offset:16384
	ds_read_b128 v[218:221], v205 offset:18432
	ds_read_b128 v[222:225], v204 offset:20480
	ds_read_b128 v[226:229], v204 offset:22528
	ds_read_b128 v[230:233], v205 offset:20480
	ds_read_b128 v[234:237], v205 offset:22528
	global_load_lds_dwordx4 v[178:179], off
	v_lshl_add_u64 v[180:181], s[62:63], 0, v[162:163]
	s_mov_b32 m0, s10
	s_addc_u32 s9, s63, 0
	global_load_lds_dwordx4 v[180:181], off
	v_lshl_add_u64 v[182:183], s[8:9], 0, v[166:167]
	s_mov_b32 m0, s11
	v_lshl_add_u64 v[184:185], s[64:65], 0, v[164:165]
	global_load_lds_dwordx4 v[182:183], off
	v_lshl_add_u64 v[182:183], s[8:9], 0, v[162:163]
	s_mov_b32 m0, s24
	s_nop 0
	global_load_lds_dwordx4 v[182:183], off
	v_lshl_add_u64 v[182:183], s[64:65], 0, v[168:169]
	s_mov_b32 m0, s0
	s_nop 0
	global_load_lds_dwordx4 v[182:183], off
	s_mov_b32 m0, s25
	s_nop 0
	global_load_lds_dwordx4 v[184:185], off
	s_waitcnt vmcnt(8)
	s_waitcnt lgkmcnt(0)
	s_barrier
	s_setprio 1
	v_mfma_i32_16x16x64_i8 v[62:65], v[158:161], v[206:209], v[62:65]
	v_mfma_i32_16x16x64_i8 v[58:61], v[154:157], v[206:209], v[58:61]
	v_mfma_i32_16x16x64_i8 v[54:57], v[158:161], v[210:213], v[54:57]
	v_mfma_i32_16x16x64_i8 v[50:53], v[154:157], v[210:213], v[50:53]
	v_mfma_i32_16x16x64_i8 v[46:49], v[158:161], v[222:225], v[46:49]
	v_mfma_i32_16x16x64_i8 v[42:45], v[154:157], v[222:225], v[42:45]
	v_mfma_i32_16x16x64_i8 v[38:41], v[158:161], v[226:229], v[38:41]
	v_mfma_i32_16x16x64_i8 v[34:37], v[154:157], v[226:229], v[34:37]
	s_nop 0
	v_mfma_i32_16x16x64_i8 v[62:65], v[146:149], v[214:217], v[62:65]
	v_mfma_i32_16x16x64_i8 v[58:61], v[150:153], v[214:217], v[58:61]
	v_mfma_i32_16x16x64_i8 v[54:57], v[146:149], v[218:221], v[54:57]
	v_mfma_i32_16x16x64_i8 v[50:53], v[150:153], v[218:221], v[50:53]
	v_mfma_i32_16x16x64_i8 v[46:49], v[146:149], v[230:233], v[46:49]
	v_mfma_i32_16x16x64_i8 v[42:45], v[150:153], v[230:233], v[42:45]
	v_mfma_i32_16x16x64_i8 v[38:41], v[146:149], v[234:237], v[38:41]
	v_mfma_i32_16x16x64_i8 v[34:37], v[150:153], v[234:237], v[34:37]
	s_setprio 0
	s_setprio 1
	v_mfma_i32_16x16x64_i8 v[30:33], v[142:145], v[206:209], v[30:33]
	v_mfma_i32_16x16x64_i8 v[26:29], v[138:141], v[206:209], v[26:29]
	v_mfma_i32_16x16x64_i8 v[22:25], v[142:145], v[210:213], v[22:25]
	v_mfma_i32_16x16x64_i8 v[18:21], v[138:141], v[210:213], v[18:21]
	v_mfma_i32_16x16x64_i8 v[14:17], v[142:145], v[222:225], v[14:17]
	v_mfma_i32_16x16x64_i8 v[10:13], v[138:141], v[222:225], v[10:13]
	v_mfma_i32_16x16x64_i8 v[6:9], v[142:145], v[226:229], v[6:9]
	v_mfma_i32_16x16x64_i8 v[2:5], v[138:141], v[226:229], v[2:5]
	s_nop 0
	v_mfma_i32_16x16x64_i8 v[30:33], v[130:133], v[214:217], v[30:33]
	v_mfma_i32_16x16x64_i8 v[26:29], v[134:137], v[214:217], v[26:29]
	v_mfma_i32_16x16x64_i8 v[22:25], v[130:133], v[218:221], v[22:25]
	v_mfma_i32_16x16x64_i8 v[18:21], v[134:137], v[218:221], v[18:21]
	v_mfma_i32_16x16x64_i8 v[14:17], v[130:133], v[230:233], v[14:17]
	v_mfma_i32_16x16x64_i8 v[10:13], v[134:137], v[230:233], v[10:13]
	v_mfma_i32_16x16x64_i8 v[6:9], v[130:133], v[234:237], v[6:9]
	v_mfma_i32_16x16x64_i8 v[2:5], v[134:137], v[234:237], v[2:5]
	s_setprio 0
	s_barrier
; #define PG8_STAGE(bufoff, gbase, voff) do { _Pragma("unroll") for (int _i = 0; _i < 2; ++_i) \
;         __builtin_amdgcn_global_load_lds((const unsigned*)((const char*)(gbase) + (voff)[_i]), (LAS unsigned*)(lds + (bufoff) + ldsw + _i * 8192), 16, 0, 0); } while (0)
; #define PG8_LDA(dst, b, h) do { _Pragma("unroll") for (int m = 0; m < 4; ++m) _Pragma("unroll") for (int k = 0; k < 2; ++k) dst[m][k] = *(const LAS bf16x8*)(lds + PG8_SA(b, h) + aoff + m * 2048 + k * 1024); } while (0)
; #define PG8_LDB(dst, b, h) do { _Pragma("unroll") for (int n = 0; n < 2; ++n) _Pragma("unroll") for (int k = 0; k < 2; ++k) dst[n][k] = *(const LAS bf16x8*)(lds + PG8_SB(b, h) + boff + n * 2048 + k * 1024); } while (0)
; #define PG8_MMA(ai, bj, At, Bt) do { __builtin_amdgcn_s_setprio(1); _Pragma("unroll") for (int m = 0; m < 4; ++m) _Pragma("unroll") for (int n = 0; n < 2; ++n) _Pragma("unroll") for (int k = 0; k < 2; ++k) \
;         acc[ai][bj][m][n] = __builtin_amdgcn_mfma_f32_16x16x32_bf16(Bt[n][k], At[m][k], acc[ai][bj][m][n], 0, 0, 0); __builtin_amdgcn_s_setprio(0); } while (0)
; #define PG8_WAIT_V(n) asm volatile("s_waitcnt vmcnt(" #n ")" ::: "memory")
; #define PG8_WAIT_L(n) asm volatile("s_waitcnt lgkmcnt(" #n ")" ::: "memory")
; #define PG8_BAR __builtin_amdgcn_s_barrier()
; #define PG8_SCHED __builtin_amdgcn_sched_barrier(0)
; #define PG8_STAGE(bufoff, gbase, voff) do { _Pragma("unroll") for (int _i = 0; _i < 2; ++_i) \
;         __builtin_amdgcn_global_load_lds((const unsigned*)((const char*)(gbase) + (voff)[_i]), (LAS unsigned*)(lds + (bufoff) + ldsw + _i * 8192), 16, 0, 0); } while (0)
; #define PG8_WAIT_V(n) asm volatile("s_waitcnt vmcnt(" #n ")" ::: "memory")
; #define PG8_WAIT_L(n) asm volatile("s_waitcnt lgkmcnt(" #n ")" ::: "memory")
;     ...
;             PG8_LDB(B0, 1, 0); PG8_LDB(B1, 1, 1); PG8_SCHED; PG8_LDA(At, 1, 0); PG8_STAGE(PG8_SA(0, 1), a2 + hstepA, voffA);
;             PG8_WAIT_V(8); PG8_WAIT_L(0); PG8_BAR; PG8_MMA(0, 0, At, B0); PG8_MMA(0, 1, At, B1); PG8_BAR; PG8_SCHED;
;             PG8_LDA(At, 1, 1); PG8_STAGE(PG8_SB(1, 0), b3, voffB); PG8_STAGE(PG8_SB(1, 1), b3 + hstepB, voffB); PG8_STAGE(PG8_SA(1, 0), a3, voffA);
;             PG8_WAIT_V(8); PG8_WAIT_L(0); PG8_BAR; PG8_MMA(1, 0, At, B0); PG8_MMA(1, 1, At, B1); PG8_BAR; PG8_SCHED;
;         }
;         asm volatile("s_nop 15\n\ts_nop 15" ::: "memory");
;         if (wr == 0) PG8_BAR;
	ds_read_b128 v[130:133], v191
	ds_read_b128 v[134:137], v192
	ds_read_b128 v[138:141], v199
	ds_read_b128 v[142:145], v200
	ds_read_b128 v[146:149], v193
	ds_read_b128 v[150:153], v194
	ds_read_b128 v[154:157], v201
	ds_read_b128 v[158:161], v202
	s_add_u32 s8, s64, 0x40000
	s_addc_u32 s9, s65, 0
	s_mov_b32 m0, s33
	v_lshl_add_u64 v[238:239], s[8:9], 0, v[168:169]
	ds_read_b128 v[206:209], v204 offset:32768
	ds_read_b128 v[210:213], v204 offset:34816
	ds_read_b128 v[214:217], v205 offset:32768
	ds_read_b128 v[218:221], v205 offset:34816
	ds_read_b128 v[222:225], v204 offset:36864
	ds_read_b128 v[226:229], v204 offset:38912
	ds_read_b128 v[230:233], v205 offset:36864
	ds_read_b128 v[234:237], v205 offset:38912
	global_load_lds_dwordx4 v[238:239], off
	v_lshl_add_u64 v[238:239], s[8:9], 0, v[164:165]
	s_mov_b32 m0, s43
	s_nop 0
	global_load_lds_dwordx4 v[238:239], off
	s_waitcnt vmcnt(8)
	s_waitcnt lgkmcnt(0)
	s_barrier
	s_setprio 1
	v_mfma_i32_16x16x64_i8 v[126:129], v[130:133], v[206:209], v[126:129]
	v_mfma_i32_16x16x64_i8 v[122:125], v[138:141], v[206:209], v[122:125]
	v_mfma_i32_16x16x64_i8 v[118:121], v[130:133], v[210:213], v[118:121]
	v_mfma_i32_16x16x64_i8 v[114:117], v[138:141], v[210:213], v[114:117]
	v_mfma_i32_16x16x64_i8 v[110:113], v[130:133], v[222:225], v[110:113]
	v_mfma_i32_16x16x64_i8 v[106:109], v[138:141], v[222:225], v[106:109]
	v_mfma_i32_16x16x64_i8 v[102:105], v[130:133], v[226:229], v[102:105]
	v_mfma_i32_16x16x64_i8 v[98:101], v[138:141], v[226:229], v[98:101]
	s_nop 0
	v_mfma_i32_16x16x64_i8 v[126:129], v[134:137], v[214:217], v[126:129]
	v_mfma_i32_16x16x64_i8 v[122:125], v[142:145], v[214:217], v[122:125]
	v_mfma_i32_16x16x64_i8 v[118:121], v[134:137], v[218:221], v[118:121]
	v_mfma_i32_16x16x64_i8 v[114:117], v[142:145], v[218:221], v[114:117]
	v_mfma_i32_16x16x64_i8 v[110:113], v[134:137], v[230:233], v[110:113]
	v_mfma_i32_16x16x64_i8 v[106:109], v[142:145], v[230:233], v[106:109]
	v_mfma_i32_16x16x64_i8 v[102:105], v[134:137], v[234:237], v[102:105]
	v_mfma_i32_16x16x64_i8 v[98:101], v[142:145], v[234:237], v[98:101]
	s_setprio 0
	s_setprio 1
	v_mfma_i32_16x16x64_i8 v[94:97], v[146:149], v[206:209], v[94:97]
	v_mfma_i32_16x16x64_i8 v[90:93], v[154:157], v[206:209], v[90:93]
	v_mfma_i32_16x16x64_i8 v[86:89], v[146:149], v[210:213], v[86:89]
	v_mfma_i32_16x16x64_i8 v[82:85], v[154:157], v[210:213], v[82:85]
	v_mfma_i32_16x16x64_i8 v[78:81], v[146:149], v[222:225], v[78:81]
	v_mfma_i32_16x16x64_i8 v[74:77], v[154:157], v[222:225], v[74:77]
	v_mfma_i32_16x16x64_i8 v[70:73], v[146:149], v[226:229], v[70:73]
	v_mfma_i32_16x16x64_i8 v[66:69], v[154:157], v[226:229], v[66:69]
	s_nop 0
	v_mfma_i32_16x16x64_i8 v[94:97], v[150:153], v[214:217], v[94:97]
	v_mfma_i32_16x16x64_i8 v[90:93], v[158:161], v[214:217], v[90:93]
	v_mfma_i32_16x16x64_i8 v[86:89], v[150:153], v[218:221], v[86:89]
	v_mfma_i32_16x16x64_i8 v[82:85], v[158:161], v[218:221], v[82:85]
	v_mfma_i32_16x16x64_i8 v[78:81], v[150:153], v[230:233], v[78:81]
	v_mfma_i32_16x16x64_i8 v[74:77], v[158:161], v[230:233], v[74:77]
	v_mfma_i32_16x16x64_i8 v[70:73], v[150:153], v[234:237], v[70:73]
	v_mfma_i32_16x16x64_i8 v[66:69], v[158:161], v[234:237], v[66:69]
	s_setprio 0
	s_barrier
	s_mov_b32 m0, s66
	v_lshl_add_u64 v[178:179], v[178:179], 0, s[38:39]
	s_add_u32 s8, s62, 0x40080
	ds_read_b128 v[206:209], v204 offset:49152
	ds_read_b128 v[210:213], v204 offset:51200
	ds_read_b128 v[214:217], v205 offset:49152
	ds_read_b128 v[218:221], v205 offset:51200
	ds_read_b128 v[222:225], v204 offset:53248
	ds_read_b128 v[226:229], v204 offset:55296
	ds_read_b128 v[230:233], v205 offset:53248
	ds_read_b128 v[234:237], v205 offset:55296
	global_load_lds_dwordx4 v[178:179], off
	v_lshl_add_u64 v[178:179], v[180:181], 0, s[38:39]
	s_mov_b32 m0, s67
	s_addc_u32 s9, s63, 0
	global_load_lds_dwordx4 v[178:179], off
	v_lshl_add_u64 v[178:179], s[8:9], 0, v[166:167]
	s_mov_b32 m0, s79
	s_nop 0
	global_load_lds_dwordx4 v[178:179], off
	v_lshl_add_u64 v[178:179], s[8:9], 0, v[162:163]
	s_mov_b32 m0, s80
	s_nop 0
	global_load_lds_dwordx4 v[178:179], off
	v_lshl_add_u64 v[178:179], v[182:183], 0, s[38:39]
	s_mov_b32 m0, s75
	s_nop 0
	global_load_lds_dwordx4 v[178:179], off
	v_lshl_add_u64 v[178:179], v[184:185], 0, s[38:39]
	s_mov_b32 m0, s78
	s_nop 0
	global_load_lds_dwordx4 v[178:179], off
	s_waitcnt vmcnt(8)
	s_waitcnt lgkmcnt(0)
	s_barrier
	s_setprio 1
	v_mfma_i32_16x16x64_i8 v[62:65], v[130:133], v[206:209], v[62:65]
	v_mfma_i32_16x16x64_i8 v[58:61], v[138:141], v[206:209], v[58:61]
	v_mfma_i32_16x16x64_i8 v[54:57], v[130:133], v[210:213], v[54:57]
	v_mfma_i32_16x16x64_i8 v[50:53], v[138:141], v[210:213], v[50:53]
	v_mfma_i32_16x16x64_i8 v[46:49], v[130:133], v[222:225], v[46:49]
	v_mfma_i32_16x16x64_i8 v[42:45], v[138:141], v[222:225], v[42:45]
	v_mfma_i32_16x16x64_i8 v[38:41], v[130:133], v[226:229], v[38:41]
	v_mfma_i32_16x16x64_i8 v[34:37], v[138:141], v[226:229], v[34:37]
	s_nop 0
	v_mfma_i32_16x16x64_i8 v[62:65], v[134:137], v[214:217], v[62:65]
	v_mfma_i32_16x16x64_i8 v[58:61], v[142:145], v[214:217], v[58:61]
	v_mfma_i32_16x16x64_i8 v[54:57], v[134:137], v[218:221], v[54:57]
	v_mfma_i32_16x16x64_i8 v[50:53], v[142:145], v[218:221], v[50:53]
	v_mfma_i32_16x16x64_i8 v[46:49], v[134:137], v[230:233], v[46:49]
	v_mfma_i32_16x16x64_i8 v[42:45], v[142:145], v[230:233], v[42:45]
	v_mfma_i32_16x16x64_i8 v[38:41], v[134:137], v[234:237], v[38:41]
	v_mfma_i32_16x16x64_i8 v[34:37], v[142:145], v[234:237], v[34:37]
	s_setprio 0
	s_setprio 1
	v_mfma_i32_16x16x64_i8 v[30:33], v[146:149], v[206:209], v[30:33]
	v_mfma_i32_16x16x64_i8 v[26:29], v[154:157], v[206:209], v[26:29]
	v_mfma_i32_16x16x64_i8 v[22:25], v[146:149], v[210:213], v[22:25]
	v_mfma_i32_16x16x64_i8 v[18:21], v[154:157], v[210:213], v[18:21]
	v_mfma_i32_16x16x64_i8 v[14:17], v[146:149], v[222:225], v[14:17]
	v_mfma_i32_16x16x64_i8 v[10:13], v[154:157], v[222:225], v[10:13]
	v_mfma_i32_16x16x64_i8 v[6:9], v[146:149], v[226:229], v[6:9]
	v_mfma_i32_16x16x64_i8 v[2:5], v[154:157], v[226:229], v[2:5]
	s_nop 0
	v_mfma_i32_16x16x64_i8 v[30:33], v[150:153], v[214:217], v[30:33]
	v_mfma_i32_16x16x64_i8 v[26:29], v[158:161], v[214:217], v[26:29]
	v_mfma_i32_16x16x64_i8 v[22:25], v[150:153], v[218:221], v[22:25]
	v_mfma_i32_16x16x64_i8 v[18:21], v[158:161], v[218:221], v[18:21]
	s_add_i32 s87, s87, 2
	s_add_u32 s85, s85, 0x100
	s_addc_u32 s86, s86, 0
	s_cmp_gt_u32 s87, 13
	s_mov_b64 s[58:59], s[60:61]
	v_mfma_i32_16x16x64_i8 v[14:17], v[150:153], v[230:233], v[14:17]
	v_mfma_i32_16x16x64_i8 v[10:13], v[158:161], v[230:233], v[10:13]
	v_mfma_i32_16x16x64_i8 v[6:9], v[150:153], v[234:237], v[6:9]
	v_mfma_i32_16x16x64_i8 v[2:5], v[158:161], v[234:237], v[2:5]
	s_setprio 0
	s_barrier
	s_cbranch_scc0 .LBB0_796
	s_nop 15
	s_nop 15
	s_and_b64 vcc, exec, s[40:41]
	s_cbranch_vccz .LBB0_799
	s_barrier

; #define PG8_STAGE(bufoff, gbase, voff) do { _Pragma("unroll") for (int _i = 0; _i < 2; ++_i) \
;         __builtin_amdgcn_global_load_lds((const unsigned*)((const char*)(gbase) + (voff)[_i]), (LAS unsigned*)(lds + (bufoff) + ldsw + _i * 8192), 16, 0, 0); } while (0)
; #define PG8_LDA(dst, b, h) do { _Pragma("unroll") for (int m = 0; m < 4; ++m) _Pragma("unroll") for (int k = 0; k < 2; ++k) dst[m][k] = *(const LAS bf16x8*)(lds + PG8_SA(b, h) + aoff + m * 2048 + k * 1024); } while (0)
; #define PG8_LDB(dst, b, h) do { _Pragma("unroll") for (int n = 0; n < 2; ++n) _Pragma("unroll") for (int k = 0; k < 2; ++k) dst[n][k] = *(const LAS bf16x8*)(lds + PG8_SB(b, h) + boff + n * 2048 + k * 1024); } while (0)
; #define PG8_MMA(ai, bj, At, Bt) do { __builtin_amdgcn_s_setprio(1); _Pragma("unroll") for (int m = 0; m < 4; ++m) _Pragma("unroll") for (int n = 0; n < 2; ++n) _Pragma("unroll") for (int k = 0; k < 2; ++k) \
;         acc[ai][bj][m][n] = __builtin_amdgcn_mfma_f32_16x16x32_bf16(Bt[n][k], At[m][k], acc[ai][bj][m][n], 0, 0, 0); __builtin_amdgcn_s_setprio(0); } while (0)
; #define PG8_WAIT_V(n) asm volatile("s_waitcnt vmcnt(" #n ")" ::: "memory")
; #define PG8_WAIT_L(n) asm volatile("s_waitcnt lgkmcnt(" #n ")" ::: "memory")
; #define PG8_BAR __builtin_amdgcn_s_barrier()
; #define PG8_SCHED __builtin_amdgcn_sched_barrier(0)
; #define PG8_LDA(dst, b, h) do { _Pragma("unroll") for (int m = 0; m < 4; ++m) PG8_LD1(dst[m], PG8_SA(b, h) + aoff0 + m * 2048, PG8_SA(b, h) + aoff1 + m * 2048); } while (0)
;     ...
;             const bool last = (t == nt - 2);
;             const char* a1 = cA + (size_t)(t + 1) * kstep;
;             const char* a2 = last ? nA : cA + (size_t)(t + 2) * kstep; const char* b2 = last ? nB : cB + (size_t)(t + 2) * kstep;
;             const char* a3 = a2 + kstep; const char* b3 = b2 + kstep;
;             if (last && has_next) S.a_ready(nxt);
;             PG8_LDB(B0, 0, 0); PG8_LDB(B1, 0, 1); PG8_SCHED; PG8_LDA(At, 0, 0); PG8_STAGE(PG8_SA(1, 1), a1 + hstepA, voffA);
;             PG8_WAIT_V(8); PG8_WAIT_L(0); PG8_BAR; PG8_MMA(0, 0, At, B0); PG8_MMA(0, 1, At, B1); PG8_BAR; PG8_SCHED;
;             PG8_LDA(At, 0, 1); PG8_STAGE(PG8_SB(0, 0), b2, voffB); PG8_STAGE(PG8_SB(0, 1), b2 + hstepB, voffB); PG8_STAGE(PG8_SA(0, 0), a2, voffA);
;             PG8_WAIT_V(8); PG8_WAIT_L(0); PG8_BAR; PG8_MMA(1, 0, At, B0); PG8_MMA(1, 1, At, B1); PG8_BAR; PG8_SCHED;
.LBB0_812:
	s_add_u32 s12, s62, s80
	s_addc_u32 s13, s63, s81
	s_add_u32 s18, s12, 0x100
	s_addc_u32 s19, s13, 0
	s_and_b64 s[8:9], s[66:67], exec
	s_cselect_b32 s83, s45, s19
	s_cselect_b32 s82, s51, s18
	s_add_u32 s8, s58, s80
	s_addc_u32 s9, s59, s81
	s_add_u32 s18, s8, 0x100
	ds_read_b128 v[158:161], v179
	ds_read_b128 v[146:149], v180
	ds_read_b128 v[154:157], v187
	ds_read_b128 v[150:153], v188
	ds_read_b128 v[142:145], v181
	ds_read_b128 v[130:133], v182
	ds_read_b128 v[138:141], v189
	ds_read_b128 v[134:137], v190
	s_addc_u32 s19, s9, 0
	s_and_b64 s[8:9], s[66:67], exec
	s_cselect_b32 s85, s61, s19
	s_cselect_b32 s84, s93, s18
	s_add_u32 s8, s12, 0x40080
	s_addc_u32 s9, s13, 0
	s_add_i32 m0, s0, 0xc000
	s_add_i32 s12, s0, 0xe000
	s_add_u32 s86, s84, 0x40000
	s_addc_u32 s87, s85, 0
	s_add_u32 s80, s82, 0x40000
	s_addc_u32 s81, s83, 0
	s_add_u32 s66, s84, 0x40080
	s_addc_u32 s67, s85, 0
	v_lshl_add_u64 v[222:223], s[8:9], 0, v[164:165]
	ds_read_b128 v[170:173], v195
	ds_read_b128 v[174:177], v195 offset:2048
	ds_read_b128 v[198:201], v196
	ds_read_b128 v[202:205], v196 offset:2048
	ds_read_b128 v[206:209], v195 offset:4096
	ds_read_b128 v[210:213], v195 offset:6144
	ds_read_b128 v[214:217], v196 offset:4096
	ds_read_b128 v[218:221], v196 offset:6144
	global_load_lds_dwordx4 v[222:223], off
	v_lshl_add_u64 v[222:223], s[8:9], 0, v[162:163]
	s_mov_b32 m0, s12
	s_nop 0
	global_load_lds_dwordx4 v[222:223], off
	s_waitcnt vmcnt(8)
	s_waitcnt lgkmcnt(0)
	s_barrier
	s_setprio 1
	v_mfma_i32_16x16x64_i8 v[94:97], v[158:161], v[170:173], v[94:97]
	v_mfma_i32_16x16x64_i8 v[90:93], v[154:157], v[170:173], v[90:93]
	v_mfma_i32_16x16x64_i8 v[86:89], v[158:161], v[174:177], v[86:89]
	v_mfma_i32_16x16x64_i8 v[82:85], v[154:157], v[174:177], v[82:85]
	v_mfma_i32_16x16x64_i8 v[78:81], v[158:161], v[206:209], v[78:81]
	v_mfma_i32_16x16x64_i8 v[74:77], v[154:157], v[206:209], v[74:77]
	v_mfma_i32_16x16x64_i8 v[70:73], v[158:161], v[210:213], v[70:73]
	v_mfma_i32_16x16x64_i8 v[66:69], v[154:157], v[210:213], v[66:69]
	s_nop 0
	v_mfma_i32_16x16x64_i8 v[94:97], v[146:149], v[198:201], v[94:97]
	v_mfma_i32_16x16x64_i8 v[90:93], v[150:153], v[198:201], v[90:93]
	v_mfma_i32_16x16x64_i8 v[86:89], v[146:149], v[202:205], v[86:89]
	v_mfma_i32_16x16x64_i8 v[82:85], v[150:153], v[202:205], v[82:85]
	v_mfma_i32_16x16x64_i8 v[78:81], v[146:149], v[214:217], v[78:81]
	v_mfma_i32_16x16x64_i8 v[74:77], v[150:153], v[214:217], v[74:77]
	v_mfma_i32_16x16x64_i8 v[70:73], v[146:149], v[218:221], v[70:73]
	v_mfma_i32_16x16x64_i8 v[66:69], v[150:153], v[218:221], v[66:69]
	s_setprio 0
	s_setprio 1
	v_mfma_i32_16x16x64_i8 v[126:129], v[142:145], v[170:173], v[126:129]
	v_mfma_i32_16x16x64_i8 v[122:125], v[138:141], v[170:173], v[122:125]
	v_mfma_i32_16x16x64_i8 v[118:121], v[142:145], v[174:177], v[118:121]
	v_mfma_i32_16x16x64_i8 v[114:117], v[138:141], v[174:177], v[114:117]
	v_mfma_i32_16x16x64_i8 v[110:113], v[142:145], v[206:209], v[110:113]
	v_mfma_i32_16x16x64_i8 v[106:109], v[138:141], v[206:209], v[106:109]
	v_mfma_i32_16x16x64_i8 v[102:105], v[142:145], v[210:213], v[102:105]
	v_mfma_i32_16x16x64_i8 v[98:101], v[138:141], v[210:213], v[98:101]
	s_nop 0
	v_mfma_i32_16x16x64_i8 v[126:129], v[130:133], v[198:201], v[126:129]
	v_mfma_i32_16x16x64_i8 v[122:125], v[134:137], v[198:201], v[122:125]
	v_mfma_i32_16x16x64_i8 v[118:121], v[130:133], v[202:205], v[118:121]
	v_mfma_i32_16x16x64_i8 v[114:117], v[134:137], v[202:205], v[114:117]
	v_mfma_i32_16x16x64_i8 v[110:113], v[130:133], v[214:217], v[110:113]
	v_mfma_i32_16x16x64_i8 v[106:109], v[134:137], v[214:217], v[106:109]
	v_mfma_i32_16x16x64_i8 v[102:105], v[130:133], v[218:221], v[102:105]
	v_mfma_i32_16x16x64_i8 v[98:101], v[134:137], v[218:221], v[98:101]
	s_setprio 0
	s_barrier
	s_mov_b32 m0, s1
	v_lshl_add_u64 v[170:171], s[84:85], 0, v[164:165]
	ds_read_b128 v[198:201], v195 offset:16384
	ds_read_b128 v[202:205], v195 offset:18432
	ds_read_b128 v[206:209], v196 offset:16384
	ds_read_b128 v[210:213], v196 offset:18432
	ds_read_b128 v[214:217], v195 offset:20480
	ds_read_b128 v[218:221], v195 offset:22528
	ds_read_b128 v[222:225], v196 offset:20480
	ds_read_b128 v[226:229], v196 offset:22528
	global_load_lds_dwordx4 v[170:171], off
	v_lshl_add_u64 v[172:173], s[84:85], 0, v[162:163]
	s_mov_b32 m0, s10
	v_lshl_add_u64 v[174:175], s[86:87], 0, v[164:165]
	global_load_lds_dwordx4 v[172:173], off
	s_mov_b32 m0, s11
	v_lshl_add_u64 v[176:177], s[82:83], 0, v[162:163]
	global_load_lds_dwordx4 v[174:175], off
	v_lshl_add_u64 v[174:175], s[86:87], 0, v[162:163]
	s_mov_b32 m0, s24
	s_nop 0
	global_load_lds_dwordx4 v[174:175], off
	v_lshl_add_u64 v[174:175], s[82:83], 0, v[164:165]
	s_mov_b32 m0, s0
	s_nop 0
	global_load_lds_dwordx4 v[174:175], off
	s_mov_b32 m0, s25
	s_nop 0
	global_load_lds_dwordx4 v[176:177], off
	s_waitcnt vmcnt(8)
	s_waitcnt lgkmcnt(0)
	s_barrier
; #define PG8_STAGE(bufoff, gbase, voff) do { _Pragma("unroll") for (int _i = 0; _i < 2; ++_i) \
;         __builtin_amdgcn_global_load_lds((const unsigned*)((const char*)(gbase) + (voff)[_i]), (LAS unsigned*)(lds + (bufoff) + ldsw + _i * 8192), 16, 0, 0); } while (0)
; #define PG8_LDA(dst, b, h) do { _Pragma("unroll") for (int m = 0; m < 4; ++m) _Pragma("unroll") for (int k = 0; k < 2; ++k) dst[m][k] = *(const LAS bf16x8*)(lds + PG8_SA(b, h) + aoff + m * 2048 + k * 1024); } while (0)
; #define PG8_LDB(dst, b, h) do { _Pragma("unroll") for (int n = 0; n < 2; ++n) _Pragma("unroll") for (int k = 0; k < 2; ++k) dst[n][k] = *(const LAS bf16x8*)(lds + PG8_SB(b, h) + boff + n * 2048 + k * 1024); } while (0)
; #define PG8_MMA(ai, bj, At, Bt) do { __builtin_amdgcn_s_setprio(1); _Pragma("unroll") for (int m = 0; m < 4; ++m) _Pragma("unroll") for (int n = 0; n < 2; ++n) _Pragma("unroll") for (int k = 0; k < 2; ++k) \
;         acc[ai][bj][m][n] = __builtin_amdgcn_mfma_f32_16x16x32_bf16(Bt[n][k], At[m][k], acc[ai][bj][m][n], 0, 0, 0); __builtin_amdgcn_s_setprio(0); } while (0)
; #define PG8_WAIT_V(n) asm volatile("s_waitcnt vmcnt(" #n ")" ::: "memory")
; #define PG8_WAIT_L(n) asm volatile("s_waitcnt lgkmcnt(" #n ")" ::: "memory")
; #define PG8_BAR __builtin_amdgcn_s_barrier()
; #define PG8_SCHED __builtin_amdgcn_sched_barrier(0)
; #define PG8_STAGE(bufoff, gbase, voff) do { _Pragma("unroll") for (int _i = 0; _i < 2; ++_i) \
;         __builtin_amdgcn_global_load_lds((const unsigned*)((const char*)(gbase) + (voff)[_i]), (LAS unsigned*)(lds + (bufoff) + ldsw + _i * 8192), 16, 0, 0); } while (0)
; #define PG8_LDA(dst, b, h) do { _Pragma("unroll") for (int m = 0; m < 4; ++m) PG8_LD1(dst[m], PG8_SA(b, h) + aoff0 + m * 2048, PG8_SA(b, h) + aoff1 + m * 2048); } while (0)
; #define PG8_LDB(dst, b, h) do { _Pragma("unroll") for (int n = 0; n < 2; ++n) PG8_LD1(dst[n], PG8_SB(b, h) + boff0 + n * 2048, PG8_SB(b, h) + boff1 + n * 2048); } while (0)
; #define PG8_BAR __builtin_amdgcn_s_barrier()
;     ...
;             PG8_WAIT_V(8); PG8_WAIT_L(0); PG8_BAR; PG8_MMA(1, 0, At, B0); PG8_MMA(1, 1, At, B1); PG8_BAR; PG8_SCHED;
;             PG8_LDB(B0, 1, 0); PG8_LDB(B1, 1, 1); PG8_SCHED; PG8_LDA(At, 1, 0); PG8_STAGE(PG8_SA(0, 1), a2 + hstepA, voffA);
;             PG8_WAIT_V(8); PG8_WAIT_L(0); PG8_BAR; PG8_MMA(0, 0, At, B0); PG8_MMA(0, 1, At, B1); PG8_BAR; PG8_SCHED;
	s_setprio 1
	v_mfma_i32_16x16x64_i8 v[46:49], v[158:161], v[198:201], v[46:49]
	v_mfma_i32_16x16x64_i8 v[42:45], v[154:157], v[198:201], v[42:45]
	v_mfma_i32_16x16x64_i8 v[38:41], v[158:161], v[202:205], v[38:41]
	v_mfma_i32_16x16x64_i8 v[34:37], v[154:157], v[202:205], v[34:37]
	v_mfma_i32_16x16x64_i8 v[30:33], v[158:161], v[214:217], v[30:33]
	v_mfma_i32_16x16x64_i8 v[26:29], v[154:157], v[214:217], v[26:29]
	v_mfma_i32_16x16x64_i8 v[22:25], v[158:161], v[218:221], v[22:25]
	v_mfma_i32_16x16x64_i8 v[18:21], v[154:157], v[218:221], v[18:21]
	s_nop 0
	v_mfma_i32_16x16x64_i8 v[46:49], v[146:149], v[206:209], v[46:49]
	v_mfma_i32_16x16x64_i8 v[42:45], v[150:153], v[206:209], v[42:45]
	v_mfma_i32_16x16x64_i8 v[38:41], v[146:149], v[210:213], v[38:41]
	v_mfma_i32_16x16x64_i8 v[34:37], v[150:153], v[210:213], v[34:37]
	v_mfma_i32_16x16x64_i8 v[30:33], v[146:149], v[222:225], v[30:33]
	v_mfma_i32_16x16x64_i8 v[26:29], v[150:153], v[222:225], v[26:29]
	v_mfma_i32_16x16x64_i8 v[22:25], v[146:149], v[226:229], v[22:25]
	v_mfma_i32_16x16x64_i8 v[18:21], v[150:153], v[226:229], v[18:21]
	s_setprio 0
	s_setprio 1
	v_mfma_i32_16x16x64_i8 v[62:65], v[142:145], v[198:201], v[62:65]
	v_mfma_i32_16x16x64_i8 v[58:61], v[138:141], v[198:201], v[58:61]
	v_mfma_i32_16x16x64_i8 v[54:57], v[142:145], v[202:205], v[54:57]
	v_mfma_i32_16x16x64_i8 v[50:53], v[138:141], v[202:205], v[50:53]
	v_mfma_i32_16x16x64_i8 v[14:17], v[142:145], v[214:217], v[14:17]
	v_mfma_i32_16x16x64_i8 v[10:13], v[138:141], v[214:217], v[10:13]
	v_mfma_i32_16x16x64_i8 v[6:9], v[142:145], v[218:221], v[6:9]
	v_mfma_i32_16x16x64_i8 v[2:5], v[138:141], v[218:221], v[2:5]
	s_nop 0
	v_mfma_i32_16x16x64_i8 v[62:65], v[130:133], v[206:209], v[62:65]
	v_mfma_i32_16x16x64_i8 v[58:61], v[134:137], v[206:209], v[58:61]
	v_mfma_i32_16x16x64_i8 v[54:57], v[130:133], v[210:213], v[54:57]
	v_mfma_i32_16x16x64_i8 v[50:53], v[134:137], v[210:213], v[50:53]
	v_mfma_i32_16x16x64_i8 v[14:17], v[130:133], v[222:225], v[14:17]
	v_mfma_i32_16x16x64_i8 v[10:13], v[134:137], v[222:225], v[10:13]
	v_mfma_i32_16x16x64_i8 v[6:9], v[130:133], v[226:229], v[6:9]
	v_mfma_i32_16x16x64_i8 v[2:5], v[134:137], v[226:229], v[2:5]
	s_setprio 0
	s_barrier
	ds_read_b128 v[130:133], v183
	ds_read_b128 v[134:137], v184
	ds_read_b128 v[138:141], v191
	ds_read_b128 v[142:145], v192
	ds_read_b128 v[146:149], v185
	ds_read_b128 v[150:153], v186
	ds_read_b128 v[154:157], v193
	ds_read_b128 v[158:161], v194
	s_mov_b32 m0, s33
	v_lshl_add_u64 v[230:231], s[80:81], 0, v[164:165]
	ds_read_b128 v[198:201], v195 offset:32768
	ds_read_b128 v[202:205], v195 offset:34816
	ds_read_b128 v[206:209], v196 offset:32768
	ds_read_b128 v[210:213], v196 offset:34816
	ds_read_b128 v[214:217], v195 offset:36864
	ds_read_b128 v[218:221], v195 offset:38912
	ds_read_b128 v[222:225], v196 offset:36864
	ds_read_b128 v[226:229], v196 offset:38912
	global_load_lds_dwordx4 v[230:231], off
	v_lshl_add_u64 v[230:231], s[80:81], 0, v[162:163]
	s_mov_b32 m0, s43
	s_nop 0
	global_load_lds_dwordx4 v[230:231], off
	s_waitcnt vmcnt(8)
	s_waitcnt lgkmcnt(0)
	s_barrier
	s_setprio 1
	v_mfma_i32_16x16x64_i8 v[94:97], v[130:133], v[198:201], v[94:97]
	v_mfma_i32_16x16x64_i8 v[90:93], v[138:141], v[198:201], v[90:93]
	v_mfma_i32_16x16x64_i8 v[86:89], v[130:133], v[202:205], v[86:89]
	v_mfma_i32_16x16x64_i8 v[82:85], v[138:141], v[202:205], v[82:85]
	v_mfma_i32_16x16x64_i8 v[78:81], v[130:133], v[214:217], v[78:81]
	v_mfma_i32_16x16x64_i8 v[74:77], v[138:141], v[214:217], v[74:77]
	v_mfma_i32_16x16x64_i8 v[70:73], v[130:133], v[218:221], v[70:73]
	v_mfma_i32_16x16x64_i8 v[66:69], v[138:141], v[218:221], v[66:69]
	s_nop 0
	v_mfma_i32_16x16x64_i8 v[94:97], v[134:137], v[206:209], v[94:97]
	v_mfma_i32_16x16x64_i8 v[90:93], v[142:145], v[206:209], v[90:93]
	v_mfma_i32_16x16x64_i8 v[86:89], v[134:137], v[210:213], v[86:89]
	v_mfma_i32_16x16x64_i8 v[82:85], v[142:145], v[210:213], v[82:85]
	v_mfma_i32_16x16x64_i8 v[78:81], v[134:137], v[222:225], v[78:81]
	v_mfma_i32_16x16x64_i8 v[74:77], v[142:145], v[222:225], v[74:77]
	v_mfma_i32_16x16x64_i8 v[70:73], v[134:137], v[226:229], v[70:73]
	v_mfma_i32_16x16x64_i8 v[66:69], v[142:145], v[226:229], v[66:69]
	s_setprio 0
	s_setprio 1
	v_mfma_i32_16x16x64_i8 v[126:129], v[146:149], v[198:201], v[126:129]
	v_mfma_i32_16x16x64_i8 v[122:125], v[154:157], v[198:201], v[122:125]
	v_mfma_i32_16x16x64_i8 v[118:121], v[146:149], v[202:205], v[118:121]
	v_mfma_i32_16x16x64_i8 v[114:117], v[154:157], v[202:205], v[114:117]
	v_mfma_i32_16x16x64_i8 v[110:113], v[146:149], v[214:217], v[110:113]
	v_mfma_i32_16x16x64_i8 v[106:109], v[154:157], v[214:217], v[106:109]
	v_mfma_i32_16x16x64_i8 v[102:105], v[146:149], v[218:221], v[102:105]
	v_mfma_i32_16x16x64_i8 v[98:101], v[154:157], v[218:221], v[98:101]
	s_nop 0
	v_mfma_i32_16x16x64_i8 v[126:129], v[150:153], v[206:209], v[126:129]
	v_mfma_i32_16x16x64_i8 v[122:125], v[158:161], v[206:209], v[122:125]
	v_mfma_i32_16x16x64_i8 v[118:121], v[150:153], v[210:213], v[118:121]
	v_mfma_i32_16x16x64_i8 v[114:117], v[158:161], v[210:213], v[114:117]
	v_mfma_i32_16x16x64_i8 v[110:113], v[150:153], v[222:225], v[110:113]
	v_mfma_i32_16x16x64_i8 v[106:109], v[158:161], v[222:225], v[106:109]
	v_mfma_i32_16x16x64_i8 v[102:105], v[150:153], v[226:229], v[102:105]
	v_mfma_i32_16x16x64_i8 v[98:101], v[158:161], v[226:229], v[98:101]
	s_setprio 0
	s_barrier
; #define PG8_STAGE(bufoff, gbase, voff) do { _Pragma("unroll") for (int _i = 0; _i < 2; ++_i) \
;         __builtin_amdgcn_global_load_lds((const unsigned*)((const char*)(gbase) + (voff)[_i]), (LAS unsigned*)(lds + (bufoff) + ldsw + _i * 8192), 16, 0, 0); } while (0)
; #define PG8_LDA(dst, b, h) do { _Pragma("unroll") for (int m = 0; m < 4; ++m) _Pragma("unroll") for (int k = 0; k < 2; ++k) dst[m][k] = *(const LAS bf16x8*)(lds + PG8_SA(b, h) + aoff + m * 2048 + k * 1024); } while (0)
; #define PG8_MMA(ai, bj, At, Bt) do { __builtin_amdgcn_s_setprio(1); _Pragma("unroll") for (int m = 0; m < 4; ++m) _Pragma("unroll") for (int n = 0; n < 2; ++n) _Pragma("unroll") for (int k = 0; k < 2; ++k) \
;         acc[ai][bj][m][n] = __builtin_amdgcn_mfma_f32_16x16x32_bf16(Bt[n][k], At[m][k], acc[ai][bj][m][n], 0, 0, 0); __builtin_amdgcn_s_setprio(0); } while (0)
; #define PG8_WAIT_V(n) asm volatile("s_waitcnt vmcnt(" #n ")" ::: "memory")
; #define PG8_WAIT_L(n) asm volatile("s_waitcnt lgkmcnt(" #n ")" ::: "memory")
; #define PG8_BAR __builtin_amdgcn_s_barrier()
; #define PG8_SCHED __builtin_amdgcn_sched_barrier(0)
; #define PG8_STAGE(bufoff, gbase, voff) do { _Pragma("unroll") for (int _i = 0; _i < 2; ++_i) \
;         __builtin_amdgcn_global_load_lds((const unsigned*)((const char*)(gbase) + (voff)[_i]), (LAS unsigned*)(lds + (bufoff) + ldsw + _i * 8192), 16, 0, 0); } while (0)
; #define PG8_LDA(dst, b, h) do { _Pragma("unroll") for (int m = 0; m < 4; ++m) PG8_LD1(dst[m], PG8_SA(b, h) + aoff0 + m * 2048, PG8_SA(b, h) + aoff1 + m * 2048); } while (0)
; #define PG8_WAIT_V(n) asm volatile("s_waitcnt vmcnt(" #n ")" ::: "memory")
; #define PG8_WAIT_L(n) asm volatile("s_waitcnt lgkmcnt(" #n ")" ::: "memory")
; #define PG8_BAR __builtin_amdgcn_s_barrier()
; #define PG8_SCHED __builtin_amdgcn_sched_barrier(0)
;     ...
;             PG8_LDA(At, 1, 1); PG8_STAGE(PG8_SB(1, 0), b3, voffB); PG8_STAGE(PG8_SB(1, 1), b3 + hstepB, voffB); PG8_STAGE(PG8_SA(1, 0), a3, voffA);
;             PG8_WAIT_V(8); PG8_WAIT_L(0); PG8_BAR; PG8_MMA(1, 0, At, B0); PG8_MMA(1, 1, At, B1); PG8_BAR; PG8_SCHED;
;         }
;         asm volatile("s_nop 15\n\ts_nop 15" ::: "memory");
;         if (wr == 0) PG8_BAR;
	s_mov_b32 m0, s78
	v_lshl_add_u64 v[170:171], v[170:171], 0, s[22:23]
	ds_read_b128 v[198:201], v195 offset:49152
	ds_read_b128 v[202:205], v195 offset:51200
	ds_read_b128 v[206:209], v196 offset:49152
	ds_read_b128 v[210:213], v196 offset:51200
	ds_read_b128 v[214:217], v195 offset:53248
	ds_read_b128 v[218:221], v195 offset:55296
	ds_read_b128 v[222:225], v196 offset:53248
	ds_read_b128 v[226:229], v196 offset:55296
	global_load_lds_dwordx4 v[170:171], off
	v_lshl_add_u64 v[170:171], v[172:173], 0, s[22:23]
	s_mov_b32 m0, s79
	s_nop 0
	global_load_lds_dwordx4 v[170:171], off
	v_lshl_add_u64 v[170:171], s[66:67], 0, v[164:165]
	s_mov_b32 m0, s90
	s_nop 0
	global_load_lds_dwordx4 v[170:171], off
	v_lshl_add_u64 v[170:171], s[66:67], 0, v[162:163]
	s_mov_b32 m0, s91
	s_nop 0
	global_load_lds_dwordx4 v[170:171], off
	v_lshl_add_u64 v[170:171], v[174:175], 0, s[22:23]
	s_mov_b32 m0, s88
	s_nop 0
	global_load_lds_dwordx4 v[170:171], off
	v_lshl_add_u64 v[170:171], v[176:177], 0, s[22:23]
	s_mov_b32 m0, s89
	s_nop 0
	global_load_lds_dwordx4 v[170:171], off
	s_waitcnt vmcnt(8)
	s_waitcnt lgkmcnt(0)
	s_barrier
	s_setprio 1
	v_mfma_i32_16x16x64_i8 v[46:49], v[130:133], v[198:201], v[46:49]
	v_mfma_i32_16x16x64_i8 v[42:45], v[138:141], v[198:201], v[42:45]
	v_mfma_i32_16x16x64_i8 v[38:41], v[130:133], v[202:205], v[38:41]
	v_mfma_i32_16x16x64_i8 v[34:37], v[138:141], v[202:205], v[34:37]
	v_mfma_i32_16x16x64_i8 v[30:33], v[130:133], v[214:217], v[30:33]
	v_mfma_i32_16x16x64_i8 v[26:29], v[138:141], v[214:217], v[26:29]
	v_mfma_i32_16x16x64_i8 v[22:25], v[130:133], v[218:221], v[22:25]
	v_mfma_i32_16x16x64_i8 v[18:21], v[138:141], v[218:221], v[18:21]
	s_nop 0
	v_mfma_i32_16x16x64_i8 v[46:49], v[134:137], v[206:209], v[46:49]
	v_mfma_i32_16x16x64_i8 v[42:45], v[142:145], v[206:209], v[42:45]
	v_mfma_i32_16x16x64_i8 v[38:41], v[134:137], v[210:213], v[38:41]
	v_mfma_i32_16x16x64_i8 v[34:37], v[142:145], v[210:213], v[34:37]
	v_mfma_i32_16x16x64_i8 v[30:33], v[134:137], v[222:225], v[30:33]
	v_mfma_i32_16x16x64_i8 v[26:29], v[142:145], v[222:225], v[26:29]
	v_mfma_i32_16x16x64_i8 v[22:25], v[134:137], v[226:229], v[22:25]
	v_mfma_i32_16x16x64_i8 v[18:21], v[142:145], v[226:229], v[18:21]
	s_setprio 0
	s_setprio 1
	v_mfma_i32_16x16x64_i8 v[62:65], v[146:149], v[198:201], v[62:65]
	v_mfma_i32_16x16x64_i8 v[58:61], v[154:157], v[198:201], v[58:61]
	v_mfma_i32_16x16x64_i8 v[54:57], v[146:149], v[202:205], v[54:57]
	v_mfma_i32_16x16x64_i8 v[50:53], v[154:157], v[202:205], v[50:53]
	v_mfma_i32_16x16x64_i8 v[14:17], v[146:149], v[214:217], v[14:17]
	v_mfma_i32_16x16x64_i8 v[10:13], v[154:157], v[214:217], v[10:13]
	v_mfma_i32_16x16x64_i8 v[6:9], v[146:149], v[218:221], v[6:9]
	v_mfma_i32_16x16x64_i8 v[2:5], v[154:157], v[218:221], v[2:5]
	s_nop 0
	v_mfma_i32_16x16x64_i8 v[62:65], v[150:153], v[206:209], v[62:65]
	v_mfma_i32_16x16x64_i8 v[58:61], v[158:161], v[206:209], v[58:61]
	v_mfma_i32_16x16x64_i8 v[54:57], v[150:153], v[210:213], v[54:57]
	v_mfma_i32_16x16x64_i8 v[50:53], v[158:161], v[210:213], v[50:53]
	v_mfma_i32_16x16x64_i8 v[14:17], v[150:153], v[222:225], v[14:17]
	v_mfma_i32_16x16x64_i8 v[10:13], v[158:161], v[222:225], v[10:13]
	v_mfma_i32_16x16x64_i8 v[6:9], v[150:153], v[226:229], v[6:9]
	v_mfma_i32_16x16x64_i8 v[2:5], v[158:161], v[226:229], v[2:5]
	s_setprio 0
	s_barrier
	s_andn2_b64 vcc, exec, s[64:65]
	s_mov_b64 s[66:67], -1
	s_mov_b64 s[64:65], 0
	s_mov_b64 s[80:81], 0x100
	s_cbranch_vccz .LBB0_812
	s_nop 15
	s_nop 15
	s_and_b64 vcc, exec, s[38:39]
	s_cbranch_vccz .LBB0_816
	s_barrier
	s_andn2_b64 vcc, exec, s[40:41]
	s_cbranch_vccz .LBB0_817

; #define PG8_STAGE(bufoff, gbase, voff) do { _Pragma("unroll") for (int _i = 0; _i < 2; ++_i) \
;         __builtin_amdgcn_global_load_lds((const unsigned*)((const char*)(gbase) + (voff)[_i]), (LAS unsigned*)(lds + (bufoff) + ldsw + _i * 8192), 16, 0, 0); } while (0)
; #define PG8_LDA(dst, b, h) do { _Pragma("unroll") for (int m = 0; m < 4; ++m) _Pragma("unroll") for (int k = 0; k < 2; ++k) dst[m][k] = *(const LAS bf16x8*)(lds + PG8_SA(b, h) + aoff + m * 2048 + k * 1024); } while (0)
; #define PG8_LDB(dst, b, h) do { _Pragma("unroll") for (int n = 0; n < 2; ++n) _Pragma("unroll") for (int k = 0; k < 2; ++k) dst[n][k] = *(const LAS bf16x8*)(lds + PG8_SB(b, h) + boff + n * 2048 + k * 1024); } while (0)
; #define PG8_MMA(ai, bj, At, Bt) do { __builtin_amdgcn_s_setprio(1); _Pragma("unroll") for (int m = 0; m < 4; ++m) _Pragma("unroll") for (int n = 0; n < 2; ++n) _Pragma("unroll") for (int k = 0; k < 2; ++k) \
;         acc[ai][bj][m][n] = __builtin_amdgcn_mfma_f32_16x16x32_bf16(Bt[n][k], At[m][k], acc[ai][bj][m][n], 0, 0, 0); __builtin_amdgcn_s_setprio(0); } while (0)
; #define PG8_WAIT_V(n) asm volatile("s_waitcnt vmcnt(" #n ")" ::: "memory")
; #define PG8_WAIT_L(n) asm volatile("s_waitcnt lgkmcnt(" #n ")" ::: "memory")
; #define PG8_BAR __builtin_amdgcn_s_barrier()
; #define PG8_SCHED __builtin_amdgcn_sched_barrier(0)
; #define PG8_LDA(dst, b, h) do { _Pragma("unroll") for (int m = 0; m < 4; ++m) PG8_LD1(dst[m], PG8_SA(b, h) + aoff0 + m * 2048, PG8_SA(b, h) + aoff1 + m * 2048); } while (0)
;     ...
;             const bool last = (t == nt - 2);
;             const char* a1 = cA + (size_t)(t + 1) * kstep;
;             const char* a2 = last ? nA : cA + (size_t)(t + 2) * kstep; const char* b2 = last ? nB : cB + (size_t)(t + 2) * kstep;
;             const char* a3 = a2 + kstep; const char* b3 = b2 + kstep;
;             if (last && has_next) S.a_ready(nxt);
;             PG8_LDB(B0, 0, 0); PG8_LDB(B1, 0, 1); PG8_SCHED; PG8_LDA(At, 0, 0); PG8_STAGE(PG8_SA(1, 1), a1 + hstepA, voffA);
;             PG8_WAIT_V(8); PG8_WAIT_L(0); PG8_BAR; PG8_MMA(0, 0, At, B0); PG8_MMA(0, 1, At, B1); PG8_BAR; PG8_SCHED;
;             PG8_LDA(At, 0, 1); PG8_STAGE(PG8_SB(0, 0), b2, voffB); PG8_STAGE(PG8_SB(0, 1), b2 + hstepB, voffB); PG8_STAGE(PG8_SA(0, 0), a2, voffA);
;             PG8_WAIT_V(8); PG8_WAIT_L(0); PG8_BAR; PG8_MMA(1, 0, At, B0); PG8_MMA(1, 1, At, B1); PG8_BAR; PG8_SCHED;
.LBB0_940:
	s_add_u32 s20, s52, s58
	s_addc_u32 s21, s53, s59
	s_add_u32 s60, s20, 0x100
	s_addc_u32 s61, s21, 0
	s_and_b64 s[18:19], s[56:57], exec
	s_cselect_b32 s61, s31, s61
	s_cselect_b32 s60, s39, s60
	s_add_u32 s18, s50, s58
	s_addc_u32 s19, s51, s59
	s_add_u32 s58, s18, 0x100
	ds_read_b128 v[158:161], v183
	ds_read_b128 v[146:149], v184
	ds_read_b128 v[154:157], v191
	ds_read_b128 v[150:153], v192
	ds_read_b128 v[142:145], v185
	ds_read_b128 v[130:133], v186
	ds_read_b128 v[138:141], v193
	ds_read_b128 v[134:137], v194
	s_addc_u32 s59, s19, 0
	s_and_b64 s[18:19], s[56:57], exec
	s_cselect_b32 s63, s83, s59
	s_cselect_b32 s62, s84, s58
	s_add_u32 s18, s20, 0x10080
	s_addc_u32 s19, s21, 0
	s_add_i32 m0, s11, 0xc000
	s_add_i32 s20, s11, 0xe000
	s_add_u32 s64, s62, 0x10000
	s_addc_u32 s65, s63, 0
	s_add_u32 s58, s60, 0x10000
	s_addc_u32 s59, s61, 0
	s_add_u32 s56, s62, 0x10080
	s_addc_u32 s57, s63, 0
	v_lshl_add_u64 v[226:227], s[18:19], 0, v[168:169]
	ds_read_b128 v[174:177], v200
	ds_read_b128 v[178:181], v200 offset:2048
	ds_read_b128 v[202:205], v201
	ds_read_b128 v[206:209], v201 offset:2048
	ds_read_b128 v[210:213], v200 offset:4096
	ds_read_b128 v[214:217], v200 offset:6144
	ds_read_b128 v[218:221], v201 offset:4096
	ds_read_b128 v[222:225], v201 offset:6144
	global_load_lds_dwordx4 v[226:227], off
	v_lshl_add_u64 v[226:227], s[18:19], 0, v[164:165]
	s_mov_b32 m0, s20
	s_nop 0
	global_load_lds_dwordx4 v[226:227], off
	s_waitcnt vmcnt(8)
	s_waitcnt lgkmcnt(0)
	s_barrier
	s_setprio 1
	v_mfma_i32_16x16x64_i8 v[126:129], v[158:161], v[174:177], v[126:129]
	v_mfma_i32_16x16x64_i8 v[122:125], v[154:157], v[174:177], v[122:125]
	v_mfma_i32_16x16x64_i8 v[118:121], v[158:161], v[178:181], v[118:121]
	v_mfma_i32_16x16x64_i8 v[114:117], v[154:157], v[178:181], v[114:117]
	v_mfma_i32_16x16x64_i8 v[110:113], v[158:161], v[210:213], v[110:113]
	v_mfma_i32_16x16x64_i8 v[106:109], v[154:157], v[210:213], v[106:109]
	v_mfma_i32_16x16x64_i8 v[102:105], v[158:161], v[214:217], v[102:105]
	v_mfma_i32_16x16x64_i8 v[98:101], v[154:157], v[214:217], v[98:101]
	s_nop 0
	v_mfma_i32_16x16x64_i8 v[126:129], v[146:149], v[202:205], v[126:129]
	v_mfma_i32_16x16x64_i8 v[122:125], v[150:153], v[202:205], v[122:125]
	v_mfma_i32_16x16x64_i8 v[118:121], v[146:149], v[206:209], v[118:121]
	v_mfma_i32_16x16x64_i8 v[114:117], v[150:153], v[206:209], v[114:117]
	v_mfma_i32_16x16x64_i8 v[110:113], v[146:149], v[218:221], v[110:113]
	v_mfma_i32_16x16x64_i8 v[106:109], v[150:153], v[218:221], v[106:109]
	v_mfma_i32_16x16x64_i8 v[102:105], v[146:149], v[222:225], v[102:105]
	v_mfma_i32_16x16x64_i8 v[98:101], v[150:153], v[222:225], v[98:101]
	s_setprio 0
	s_setprio 1
	v_mfma_i32_16x16x64_i8 v[94:97], v[142:145], v[174:177], v[94:97]
	v_mfma_i32_16x16x64_i8 v[90:93], v[138:141], v[174:177], v[90:93]
	v_mfma_i32_16x16x64_i8 v[86:89], v[142:145], v[178:181], v[86:89]
	v_mfma_i32_16x16x64_i8 v[82:85], v[138:141], v[178:181], v[82:85]
	v_mfma_i32_16x16x64_i8 v[78:81], v[142:145], v[210:213], v[78:81]
	v_mfma_i32_16x16x64_i8 v[74:77], v[138:141], v[210:213], v[74:77]
	v_mfma_i32_16x16x64_i8 v[70:73], v[142:145], v[214:217], v[70:73]
	v_mfma_i32_16x16x64_i8 v[66:69], v[138:141], v[214:217], v[66:69]
	s_nop 0
	v_mfma_i32_16x16x64_i8 v[94:97], v[130:133], v[202:205], v[94:97]
	v_mfma_i32_16x16x64_i8 v[90:93], v[134:137], v[202:205], v[90:93]
	v_mfma_i32_16x16x64_i8 v[86:89], v[130:133], v[206:209], v[86:89]
	v_mfma_i32_16x16x64_i8 v[82:85], v[134:137], v[206:209], v[82:85]
	v_mfma_i32_16x16x64_i8 v[78:81], v[130:133], v[218:221], v[78:81]
	v_mfma_i32_16x16x64_i8 v[74:77], v[134:137], v[218:221], v[74:77]
	v_mfma_i32_16x16x64_i8 v[70:73], v[130:133], v[222:225], v[70:73]
	v_mfma_i32_16x16x64_i8 v[66:69], v[134:137], v[222:225], v[66:69]
	s_setprio 0
	s_barrier
	s_mov_b32 m0, s23
	v_lshl_add_u64 v[174:175], s[62:63], 0, v[166:167]
	ds_read_b128 v[202:205], v200 offset:16384
	ds_read_b128 v[206:209], v200 offset:18432
	ds_read_b128 v[210:213], v201 offset:16384
	ds_read_b128 v[214:217], v201 offset:18432
	ds_read_b128 v[218:221], v200 offset:20480
	ds_read_b128 v[222:225], v200 offset:22528
	ds_read_b128 v[226:229], v201 offset:20480
	ds_read_b128 v[230:233], v201 offset:22528
	global_load_lds_dwordx4 v[174:175], off
	v_lshl_add_u64 v[176:177], s[62:63], 0, v[162:163]
	s_mov_b32 m0, s24
	v_lshl_add_u64 v[178:179], s[64:65], 0, v[166:167]
	global_load_lds_dwordx4 v[176:177], off
	s_mov_b32 m0, s25
	v_lshl_add_u64 v[180:181], s[60:61], 0, v[164:165]
	global_load_lds_dwordx4 v[178:179], off
	v_lshl_add_u64 v[178:179], s[64:65], 0, v[162:163]
	s_mov_b32 m0, s33
	s_nop 0
	global_load_lds_dwordx4 v[178:179], off
	v_lshl_add_u64 v[178:179], s[60:61], 0, v[168:169]
	s_mov_b32 m0, s11
	s_nop 0
	global_load_lds_dwordx4 v[178:179], off
	s_mov_b32 m0, s35
	s_nop 0
	global_load_lds_dwordx4 v[180:181], off
	s_waitcnt vmcnt(8)
	s_waitcnt lgkmcnt(0)
	s_barrier
; #define PG8_STAGE(bufoff, gbase, voff) do { _Pragma("unroll") for (int _i = 0; _i < 2; ++_i) \
;         __builtin_amdgcn_global_load_lds((const unsigned*)((const char*)(gbase) + (voff)[_i]), (LAS unsigned*)(lds + (bufoff) + ldsw + _i * 8192), 16, 0, 0); } while (0)
; #define PG8_LDA(dst, b, h) do { _Pragma("unroll") for (int m = 0; m < 4; ++m) _Pragma("unroll") for (int k = 0; k < 2; ++k) dst[m][k] = *(const LAS bf16x8*)(lds + PG8_SA(b, h) + aoff + m * 2048 + k * 1024); } while (0)
; #define PG8_LDB(dst, b, h) do { _Pragma("unroll") for (int n = 0; n < 2; ++n) _Pragma("unroll") for (int k = 0; k < 2; ++k) dst[n][k] = *(const LAS bf16x8*)(lds + PG8_SB(b, h) + boff + n * 2048 + k * 1024); } while (0)
; #define PG8_MMA(ai, bj, At, Bt) do { __builtin_amdgcn_s_setprio(1); _Pragma("unroll") for (int m = 0; m < 4; ++m) _Pragma("unroll") for (int n = 0; n < 2; ++n) _Pragma("unroll") for (int k = 0; k < 2; ++k) \
;         acc[ai][bj][m][n] = __builtin_amdgcn_mfma_f32_16x16x32_bf16(Bt[n][k], At[m][k], acc[ai][bj][m][n], 0, 0, 0); __builtin_amdgcn_s_setprio(0); } while (0)
; #define PG8_WAIT_V(n) asm volatile("s_waitcnt vmcnt(" #n ")" ::: "memory")
; #define PG8_WAIT_L(n) asm volatile("s_waitcnt lgkmcnt(" #n ")" ::: "memory")
; #define PG8_BAR __builtin_amdgcn_s_barrier()
; #define PG8_SCHED __builtin_amdgcn_sched_barrier(0)
; #define PG8_STAGE(bufoff, gbase, voff) do { _Pragma("unroll") for (int _i = 0; _i < 2; ++_i) \
;         __builtin_amdgcn_global_load_lds((const unsigned*)((const char*)(gbase) + (voff)[_i]), (LAS unsigned*)(lds + (bufoff) + ldsw + _i * 8192), 16, 0, 0); } while (0)
; #define PG8_LDA(dst, b, h) do { _Pragma("unroll") for (int m = 0; m < 4; ++m) PG8_LD1(dst[m], PG8_SA(b, h) + aoff0 + m * 2048, PG8_SA(b, h) + aoff1 + m * 2048); } while (0)
; #define PG8_LDB(dst, b, h) do { _Pragma("unroll") for (int n = 0; n < 2; ++n) PG8_LD1(dst[n], PG8_SB(b, h) + boff0 + n * 2048, PG8_SB(b, h) + boff1 + n * 2048); } while (0)
; #define PG8_BAR __builtin_amdgcn_s_barrier()
;     ...
;             PG8_WAIT_V(8); PG8_WAIT_L(0); PG8_BAR; PG8_MMA(1, 0, At, B0); PG8_MMA(1, 1, At, B1); PG8_BAR; PG8_SCHED;
;             PG8_LDB(B0, 1, 0); PG8_LDB(B1, 1, 1); PG8_SCHED; PG8_LDA(At, 1, 0); PG8_STAGE(PG8_SA(0, 1), a2 + hstepA, voffA);
;             PG8_WAIT_V(8); PG8_WAIT_L(0); PG8_BAR; PG8_MMA(0, 0, At, B0); PG8_MMA(0, 1, At, B1); PG8_BAR; PG8_SCHED;
	s_setprio 1
	v_mfma_i32_16x16x64_i8 v[62:65], v[158:161], v[202:205], v[62:65]
	v_mfma_i32_16x16x64_i8 v[58:61], v[154:157], v[202:205], v[58:61]
	v_mfma_i32_16x16x64_i8 v[54:57], v[158:161], v[206:209], v[54:57]
	v_mfma_i32_16x16x64_i8 v[50:53], v[154:157], v[206:209], v[50:53]
	v_mfma_i32_16x16x64_i8 v[46:49], v[158:161], v[218:221], v[46:49]
	v_mfma_i32_16x16x64_i8 v[42:45], v[154:157], v[218:221], v[42:45]
	v_mfma_i32_16x16x64_i8 v[38:41], v[158:161], v[222:225], v[38:41]
	v_mfma_i32_16x16x64_i8 v[34:37], v[154:157], v[222:225], v[34:37]
	s_nop 0
	v_mfma_i32_16x16x64_i8 v[62:65], v[146:149], v[210:213], v[62:65]
	v_mfma_i32_16x16x64_i8 v[58:61], v[150:153], v[210:213], v[58:61]
	v_mfma_i32_16x16x64_i8 v[54:57], v[146:149], v[214:217], v[54:57]
	v_mfma_i32_16x16x64_i8 v[50:53], v[150:153], v[214:217], v[50:53]
	v_mfma_i32_16x16x64_i8 v[46:49], v[146:149], v[226:229], v[46:49]
	v_mfma_i32_16x16x64_i8 v[42:45], v[150:153], v[226:229], v[42:45]
	v_mfma_i32_16x16x64_i8 v[38:41], v[146:149], v[230:233], v[38:41]
	v_mfma_i32_16x16x64_i8 v[34:37], v[150:153], v[230:233], v[34:37]
	s_setprio 0
	s_setprio 1
	v_mfma_i32_16x16x64_i8 v[30:33], v[142:145], v[202:205], v[30:33]
	v_mfma_i32_16x16x64_i8 v[26:29], v[138:141], v[202:205], v[26:29]
	v_mfma_i32_16x16x64_i8 v[22:25], v[142:145], v[206:209], v[22:25]
	v_mfma_i32_16x16x64_i8 v[18:21], v[138:141], v[206:209], v[18:21]
	v_mfma_i32_16x16x64_i8 v[14:17], v[142:145], v[218:221], v[14:17]
	v_mfma_i32_16x16x64_i8 v[10:13], v[138:141], v[218:221], v[10:13]
	v_mfma_i32_16x16x64_i8 v[6:9], v[142:145], v[222:225], v[6:9]
	v_mfma_i32_16x16x64_i8 v[2:5], v[138:141], v[222:225], v[2:5]
	s_nop 0
	v_mfma_i32_16x16x64_i8 v[30:33], v[130:133], v[210:213], v[30:33]
	v_mfma_i32_16x16x64_i8 v[26:29], v[134:137], v[210:213], v[26:29]
	v_mfma_i32_16x16x64_i8 v[22:25], v[130:133], v[214:217], v[22:25]
	v_mfma_i32_16x16x64_i8 v[18:21], v[134:137], v[214:217], v[18:21]
	v_mfma_i32_16x16x64_i8 v[14:17], v[130:133], v[226:229], v[14:17]
	v_mfma_i32_16x16x64_i8 v[10:13], v[134:137], v[226:229], v[10:13]
	v_mfma_i32_16x16x64_i8 v[6:9], v[130:133], v[230:233], v[6:9]
	v_mfma_i32_16x16x64_i8 v[2:5], v[134:137], v[230:233], v[2:5]
	s_setprio 0
	s_barrier
	ds_read_b128 v[130:133], v187
	ds_read_b128 v[134:137], v188
	ds_read_b128 v[138:141], v195
	ds_read_b128 v[142:145], v196
	ds_read_b128 v[146:149], v189
	ds_read_b128 v[150:153], v190
	ds_read_b128 v[154:157], v197
	ds_read_b128 v[158:161], v198
	s_mov_b32 m0, s49
	v_lshl_add_u64 v[234:235], s[58:59], 0, v[168:169]
	ds_read_b128 v[202:205], v200 offset:32768
	ds_read_b128 v[206:209], v200 offset:34816
	ds_read_b128 v[210:213], v201 offset:32768
	ds_read_b128 v[214:217], v201 offset:34816
	ds_read_b128 v[218:221], v200 offset:36864
	ds_read_b128 v[222:225], v200 offset:38912
	ds_read_b128 v[226:229], v201 offset:36864
	ds_read_b128 v[230:233], v201 offset:38912
	global_load_lds_dwordx4 v[234:235], off
	v_lshl_add_u64 v[234:235], s[58:59], 0, v[164:165]
	s_mov_b32 m0, s66
	s_nop 0
	global_load_lds_dwordx4 v[234:235], off
	s_waitcnt vmcnt(8)
	s_waitcnt lgkmcnt(0)
	s_barrier
	s_setprio 1
	v_mfma_i32_16x16x64_i8 v[126:129], v[130:133], v[202:205], v[126:129]
	v_mfma_i32_16x16x64_i8 v[122:125], v[138:141], v[202:205], v[122:125]
	v_mfma_i32_16x16x64_i8 v[118:121], v[130:133], v[206:209], v[118:121]
	v_mfma_i32_16x16x64_i8 v[114:117], v[138:141], v[206:209], v[114:117]
	v_mfma_i32_16x16x64_i8 v[110:113], v[130:133], v[218:221], v[110:113]
	v_mfma_i32_16x16x64_i8 v[106:109], v[138:141], v[218:221], v[106:109]
	v_mfma_i32_16x16x64_i8 v[102:105], v[130:133], v[222:225], v[102:105]
	v_mfma_i32_16x16x64_i8 v[98:101], v[138:141], v[222:225], v[98:101]
	s_nop 0
	v_mfma_i32_16x16x64_i8 v[126:129], v[134:137], v[210:213], v[126:129]
	v_mfma_i32_16x16x64_i8 v[122:125], v[142:145], v[210:213], v[122:125]
	v_mfma_i32_16x16x64_i8 v[118:121], v[134:137], v[214:217], v[118:121]
	v_mfma_i32_16x16x64_i8 v[114:117], v[142:145], v[214:217], v[114:117]
	v_mfma_i32_16x16x64_i8 v[110:113], v[134:137], v[226:229], v[110:113]
	v_mfma_i32_16x16x64_i8 v[106:109], v[142:145], v[226:229], v[106:109]
	v_mfma_i32_16x16x64_i8 v[102:105], v[134:137], v[230:233], v[102:105]
	v_mfma_i32_16x16x64_i8 v[98:101], v[142:145], v[230:233], v[98:101]
	s_setprio 0
	s_setprio 1
	v_mfma_i32_16x16x64_i8 v[94:97], v[146:149], v[202:205], v[94:97]
	v_mfma_i32_16x16x64_i8 v[90:93], v[154:157], v[202:205], v[90:93]
	v_mfma_i32_16x16x64_i8 v[86:89], v[146:149], v[206:209], v[86:89]
	v_mfma_i32_16x16x64_i8 v[82:85], v[154:157], v[206:209], v[82:85]
	v_mfma_i32_16x16x64_i8 v[78:81], v[146:149], v[218:221], v[78:81]
	v_mfma_i32_16x16x64_i8 v[74:77], v[154:157], v[218:221], v[74:77]
	v_mfma_i32_16x16x64_i8 v[70:73], v[146:149], v[222:225], v[70:73]
	v_mfma_i32_16x16x64_i8 v[66:69], v[154:157], v[222:225], v[66:69]
	s_nop 0
	v_mfma_i32_16x16x64_i8 v[94:97], v[150:153], v[210:213], v[94:97]
	v_mfma_i32_16x16x64_i8 v[90:93], v[158:161], v[210:213], v[90:93]
	v_mfma_i32_16x16x64_i8 v[86:89], v[150:153], v[214:217], v[86:89]
	v_mfma_i32_16x16x64_i8 v[82:85], v[158:161], v[214:217], v[82:85]
	v_mfma_i32_16x16x64_i8 v[78:81], v[150:153], v[226:229], v[78:81]
	v_mfma_i32_16x16x64_i8 v[74:77], v[158:161], v[226:229], v[74:77]
	v_mfma_i32_16x16x64_i8 v[70:73], v[150:153], v[230:233], v[70:73]
	v_mfma_i32_16x16x64_i8 v[66:69], v[158:161], v[230:233], v[66:69]
	s_setprio 0
	s_barrier
; #define PG8_STAGE(bufoff, gbase, voff) do { _Pragma("unroll") for (int _i = 0; _i < 2; ++_i) \
;         __builtin_amdgcn_global_load_lds((const unsigned*)((const char*)(gbase) + (voff)[_i]), (LAS unsigned*)(lds + (bufoff) + ldsw + _i * 8192), 16, 0, 0); } while (0)
; #define PG8_LDA(dst, b, h) do { _Pragma("unroll") for (int m = 0; m < 4; ++m) _Pragma("unroll") for (int k = 0; k < 2; ++k) dst[m][k] = *(const LAS bf16x8*)(lds + PG8_SA(b, h) + aoff + m * 2048 + k * 1024); } while (0)
; #define PG8_MMA(ai, bj, At, Bt) do { __builtin_amdgcn_s_setprio(1); _Pragma("unroll") for (int m = 0; m < 4; ++m) _Pragma("unroll") for (int n = 0; n < 2; ++n) _Pragma("unroll") for (int k = 0; k < 2; ++k) \
;         acc[ai][bj][m][n] = __builtin_amdgcn_mfma_f32_16x16x32_bf16(Bt[n][k], At[m][k], acc[ai][bj][m][n], 0, 0, 0); __builtin_amdgcn_s_setprio(0); } while (0)
; #define PG8_WAIT_V(n) asm volatile("s_waitcnt vmcnt(" #n ")" ::: "memory")
; #define PG8_WAIT_L(n) asm volatile("s_waitcnt lgkmcnt(" #n ")" ::: "memory")
; #define PG8_BAR __builtin_amdgcn_s_barrier()
; #define PG8_SCHED __builtin_amdgcn_sched_barrier(0)
; #define PG8_STAGE(bufoff, gbase, voff) do { _Pragma("unroll") for (int _i = 0; _i < 2; ++_i) \
;         __builtin_amdgcn_global_load_lds((const unsigned*)((const char*)(gbase) + (voff)[_i]), (LAS unsigned*)(lds + (bufoff) + ldsw + _i * 8192), 16, 0, 0); } while (0)
; #define PG8_LDA(dst, b, h) do { _Pragma("unroll") for (int m = 0; m < 4; ++m) PG8_LD1(dst[m], PG8_SA(b, h) + aoff0 + m * 2048, PG8_SA(b, h) + aoff1 + m * 2048); } while (0)
; #define PG8_WAIT_V(n) asm volatile("s_waitcnt vmcnt(" #n ")" ::: "memory")
; #define PG8_WAIT_L(n) asm volatile("s_waitcnt lgkmcnt(" #n ")" ::: "memory")
; #define PG8_BAR __builtin_amdgcn_s_barrier()
; #define PG8_SCHED __builtin_amdgcn_sched_barrier(0)
;     ...
;             PG8_LDA(At, 1, 1); PG8_STAGE(PG8_SB(1, 0), b3, voffB); PG8_STAGE(PG8_SB(1, 1), b3 + hstepB, voffB); PG8_STAGE(PG8_SA(1, 0), a3, voffA);
;             PG8_WAIT_V(8); PG8_WAIT_L(0); PG8_BAR; PG8_MMA(1, 0, At, B0); PG8_MMA(1, 1, At, B1); PG8_BAR; PG8_SCHED;
;         }
;         asm volatile("s_nop 15\n\ts_nop 15" ::: "memory");
;         if (wr == 0) PG8_BAR;
	s_mov_b32 m0, s73
	v_lshl_add_u64 v[174:175], v[174:175], 0, s[12:13]
	ds_read_b128 v[202:205], v200 offset:49152
	ds_read_b128 v[206:209], v200 offset:51200
	ds_read_b128 v[210:213], v201 offset:49152
	ds_read_b128 v[214:217], v201 offset:51200
	ds_read_b128 v[218:221], v200 offset:53248
	ds_read_b128 v[222:225], v200 offset:55296
	ds_read_b128 v[226:229], v201 offset:53248
	ds_read_b128 v[230:233], v201 offset:55296
	global_load_lds_dwordx4 v[174:175], off
	v_lshl_add_u64 v[174:175], v[176:177], 0, s[12:13]
	s_mov_b32 m0, s74
	s_nop 0
	global_load_lds_dwordx4 v[174:175], off
	v_lshl_add_u64 v[174:175], s[56:57], 0, v[166:167]
	s_mov_b32 m0, s79
	s_nop 0
	global_load_lds_dwordx4 v[174:175], off
	v_lshl_add_u64 v[174:175], s[56:57], 0, v[162:163]
	s_mov_b32 m0, s80
	s_nop 0
	global_load_lds_dwordx4 v[174:175], off
	v_lshl_add_u64 v[174:175], v[178:179], 0, s[12:13]
	s_mov_b32 m0, s75
	s_nop 0
	global_load_lds_dwordx4 v[174:175], off
	v_lshl_add_u64 v[174:175], v[180:181], 0, s[12:13]
	s_mov_b32 m0, s78
	s_nop 0
	global_load_lds_dwordx4 v[174:175], off
	s_waitcnt vmcnt(8)
	s_waitcnt lgkmcnt(0)
	s_barrier
	s_setprio 1
	v_mfma_i32_16x16x64_i8 v[62:65], v[130:133], v[202:205], v[62:65]
	v_mfma_i32_16x16x64_i8 v[58:61], v[138:141], v[202:205], v[58:61]
	v_mfma_i32_16x16x64_i8 v[54:57], v[130:133], v[206:209], v[54:57]
	v_mfma_i32_16x16x64_i8 v[50:53], v[138:141], v[206:209], v[50:53]
	v_mfma_i32_16x16x64_i8 v[46:49], v[130:133], v[218:221], v[46:49]
	v_mfma_i32_16x16x64_i8 v[42:45], v[138:141], v[218:221], v[42:45]
	v_mfma_i32_16x16x64_i8 v[38:41], v[130:133], v[222:225], v[38:41]
	v_mfma_i32_16x16x64_i8 v[34:37], v[138:141], v[222:225], v[34:37]
	s_nop 0
	v_mfma_i32_16x16x64_i8 v[62:65], v[134:137], v[210:213], v[62:65]
	v_mfma_i32_16x16x64_i8 v[58:61], v[142:145], v[210:213], v[58:61]
	v_mfma_i32_16x16x64_i8 v[54:57], v[134:137], v[214:217], v[54:57]
	v_mfma_i32_16x16x64_i8 v[50:53], v[142:145], v[214:217], v[50:53]
	v_mfma_i32_16x16x64_i8 v[46:49], v[134:137], v[226:229], v[46:49]
	v_mfma_i32_16x16x64_i8 v[42:45], v[142:145], v[226:229], v[42:45]
	v_mfma_i32_16x16x64_i8 v[38:41], v[134:137], v[230:233], v[38:41]
	v_mfma_i32_16x16x64_i8 v[34:37], v[142:145], v[230:233], v[34:37]
	s_setprio 0
	s_setprio 1
	v_mfma_i32_16x16x64_i8 v[30:33], v[146:149], v[202:205], v[30:33]
	v_mfma_i32_16x16x64_i8 v[26:29], v[154:157], v[202:205], v[26:29]
	v_mfma_i32_16x16x64_i8 v[22:25], v[146:149], v[206:209], v[22:25]
	v_mfma_i32_16x16x64_i8 v[18:21], v[154:157], v[206:209], v[18:21]
	v_mfma_i32_16x16x64_i8 v[14:17], v[146:149], v[218:221], v[14:17]
	v_mfma_i32_16x16x64_i8 v[10:13], v[154:157], v[218:221], v[10:13]
	v_mfma_i32_16x16x64_i8 v[6:9], v[146:149], v[222:225], v[6:9]
	v_mfma_i32_16x16x64_i8 v[2:5], v[154:157], v[222:225], v[2:5]
	s_nop 0
	v_mfma_i32_16x16x64_i8 v[30:33], v[150:153], v[210:213], v[30:33]
	v_mfma_i32_16x16x64_i8 v[26:29], v[158:161], v[210:213], v[26:29]
	v_mfma_i32_16x16x64_i8 v[22:25], v[150:153], v[214:217], v[22:25]
	v_mfma_i32_16x16x64_i8 v[18:21], v[158:161], v[214:217], v[18:21]
	v_mfma_i32_16x16x64_i8 v[14:17], v[150:153], v[226:229], v[14:17]
	v_mfma_i32_16x16x64_i8 v[10:13], v[158:161], v[226:229], v[10:13]
	v_mfma_i32_16x16x64_i8 v[6:9], v[150:153], v[230:233], v[6:9]
	v_mfma_i32_16x16x64_i8 v[2:5], v[158:161], v[230:233], v[2:5]
	s_setprio 0
	s_barrier
	s_andn2_b64 vcc, exec, s[54:55]
	s_mov_b64 s[56:57], -1
	s_mov_b64 s[54:55], 0
	s_mov_b64 s[58:59], 0x100
	s_cbranch_vccz .LBB0_940
	s_nop 15
	s_nop 15
	s_and_b64 vcc, exec, s[14:15]
	s_cbranch_vccz .LBB0_943
	s_barrier

; #define PG8_STAGE(bufoff, gbase, voff) do { _Pragma("unroll") for (int _i = 0; _i < 2; ++_i) \
;         __builtin_amdgcn_global_load_lds((const unsigned*)((const char*)(gbase) + (voff)[_i]), (LAS unsigned*)(lds + (bufoff) + ldsw + _i * 8192), 16, 0, 0); } while (0)
; #define PG8_LDA(dst, b, h) do { _Pragma("unroll") for (int m = 0; m < 4; ++m) _Pragma("unroll") for (int k = 0; k < 2; ++k) dst[m][k] = *(const LAS bf16x8*)(lds + PG8_SA(b, h) + aoff + m * 2048 + k * 1024); } while (0)
; #define PG8_LDB(dst, b, h) do { _Pragma("unroll") for (int n = 0; n < 2; ++n) _Pragma("unroll") for (int k = 0; k < 2; ++k) dst[n][k] = *(const LAS bf16x8*)(lds + PG8_SB(b, h) + boff + n * 2048 + k * 1024); } while (0)
; #define PG8_MMA(ai, bj, At, Bt) do { __builtin_amdgcn_s_setprio(1); _Pragma("unroll") for (int m = 0; m < 4; ++m) _Pragma("unroll") for (int n = 0; n < 2; ++n) _Pragma("unroll") for (int k = 0; k < 2; ++k) \
;         acc[ai][bj][m][n] = __builtin_amdgcn_mfma_f32_16x16x32_bf16(Bt[n][k], At[m][k], acc[ai][bj][m][n], 0, 0, 0); __builtin_amdgcn_s_setprio(0); } while (0)
; #define PG8_WAIT_V(n) asm volatile("s_waitcnt vmcnt(" #n ")" ::: "memory")
; #define PG8_WAIT_L(n) asm volatile("s_waitcnt lgkmcnt(" #n ")" ::: "memory")
; #define PG8_BAR __builtin_amdgcn_s_barrier()
; #define PG8_SCHED __builtin_amdgcn_sched_barrier(0)
; #define PG8_LDA(dst, b, h) do { _Pragma("unroll") for (int m = 0; m < 4; ++m) PG8_LD1(dst[m], PG8_SA(b, h) + aoff0 + m * 2048, PG8_SA(b, h) + aoff1 + m * 2048); } while (0)
;     ...
;             const bool last = (t == nt - 2);
;             const char* a1 = cA + (size_t)(t + 1) * kstep;
;             const char* a2 = last ? nA : cA + (size_t)(t + 2) * kstep; const char* b2 = last ? nB : cB + (size_t)(t + 2) * kstep;
;             const char* a3 = a2 + kstep; const char* b3 = b2 + kstep;
;             if (last && has_next) S.a_ready(nxt);
;             PG8_LDB(B0, 0, 0); PG8_LDB(B1, 0, 1); PG8_SCHED; PG8_LDA(At, 0, 0); PG8_STAGE(PG8_SA(1, 1), a1 + hstepA, voffA);
;             PG8_WAIT_V(8); PG8_WAIT_L(0); PG8_BAR; PG8_MMA(0, 0, At, B0); PG8_MMA(0, 1, At, B1); PG8_BAR; PG8_SCHED;
;             PG8_LDA(At, 0, 1); PG8_STAGE(PG8_SB(0, 0), b2, voffB); PG8_STAGE(PG8_SB(0, 1), b2 + hstepB, voffB); PG8_STAGE(PG8_SA(0, 0), a2, voffA);
;             PG8_WAIT_V(8); PG8_WAIT_L(0); PG8_BAR; PG8_MMA(1, 0, At, B0); PG8_MMA(1, 1, At, B1); PG8_BAR; PG8_SCHED;
.LBB0_960:
	s_add_u32 s20, s52, s58
	s_addc_u32 s21, s53, s59
	s_add_u32 s60, s20, 0x100
	s_addc_u32 s61, s21, 0
	s_and_b64 s[18:19], s[56:57], exec
	s_cselect_b32 s61, s31, s61
	s_cselect_b32 s60, s39, s60
	s_add_u32 s18, s50, s58
	s_addc_u32 s19, s51, s59
	s_add_u32 s58, s18, 0x100
	ds_read_b128 v[158:161], v183
	ds_read_b128 v[146:149], v184
	ds_read_b128 v[154:157], v191
	ds_read_b128 v[150:153], v192
	ds_read_b128 v[142:145], v185
	ds_read_b128 v[130:133], v186
	ds_read_b128 v[138:141], v193
	ds_read_b128 v[134:137], v194
	s_addc_u32 s59, s19, 0
	s_and_b64 s[18:19], s[56:57], exec
	s_cselect_b32 s63, s83, s59
	s_cselect_b32 s62, s84, s58
	s_add_u32 s18, s20, 0x10080
	s_addc_u32 s19, s21, 0
	s_add_i32 m0, s23, 0xc000
	s_add_i32 s20, s23, 0xe000
	s_add_u32 s64, s62, 0x10000
	s_addc_u32 s65, s63, 0
	s_add_u32 s58, s60, 0x10000
	s_addc_u32 s59, s61, 0
	s_add_u32 s56, s62, 0x10080
	s_addc_u32 s57, s63, 0
	v_lshl_add_u64 v[226:227], s[18:19], 0, v[168:169]
	ds_read_b128 v[174:177], v200
	ds_read_b128 v[178:181], v200 offset:2048
	ds_read_b128 v[202:205], v201
	ds_read_b128 v[206:209], v201 offset:2048
	ds_read_b128 v[210:213], v200 offset:4096
	ds_read_b128 v[214:217], v200 offset:6144
	ds_read_b128 v[218:221], v201 offset:4096
	ds_read_b128 v[222:225], v201 offset:6144
	global_load_lds_dwordx4 v[226:227], off
	v_lshl_add_u64 v[226:227], s[18:19], 0, v[164:165]
	s_mov_b32 m0, s20
	s_nop 0
	global_load_lds_dwordx4 v[226:227], off
	s_waitcnt vmcnt(8)
	s_waitcnt lgkmcnt(0)
	s_barrier
	s_setprio 1
	v_mfma_i32_16x16x64_i8 v[126:129], v[158:161], v[174:177], v[126:129]
	v_mfma_i32_16x16x64_i8 v[122:125], v[154:157], v[174:177], v[122:125]
	v_mfma_i32_16x16x64_i8 v[118:121], v[158:161], v[178:181], v[118:121]
	v_mfma_i32_16x16x64_i8 v[114:117], v[154:157], v[178:181], v[114:117]
	v_mfma_i32_16x16x64_i8 v[110:113], v[158:161], v[210:213], v[110:113]
	v_mfma_i32_16x16x64_i8 v[106:109], v[154:157], v[210:213], v[106:109]
	v_mfma_i32_16x16x64_i8 v[102:105], v[158:161], v[214:217], v[102:105]
	v_mfma_i32_16x16x64_i8 v[98:101], v[154:157], v[214:217], v[98:101]
	s_nop 0
	v_mfma_i32_16x16x64_i8 v[126:129], v[146:149], v[202:205], v[126:129]
	v_mfma_i32_16x16x64_i8 v[122:125], v[150:153], v[202:205], v[122:125]
	v_mfma_i32_16x16x64_i8 v[118:121], v[146:149], v[206:209], v[118:121]
	v_mfma_i32_16x16x64_i8 v[114:117], v[150:153], v[206:209], v[114:117]
	v_mfma_i32_16x16x64_i8 v[110:113], v[146:149], v[218:221], v[110:113]
	v_mfma_i32_16x16x64_i8 v[106:109], v[150:153], v[218:221], v[106:109]
	v_mfma_i32_16x16x64_i8 v[102:105], v[146:149], v[222:225], v[102:105]
	v_mfma_i32_16x16x64_i8 v[98:101], v[150:153], v[222:225], v[98:101]
	s_setprio 0
	s_setprio 1
	v_mfma_i32_16x16x64_i8 v[94:97], v[142:145], v[174:177], v[94:97]
	v_mfma_i32_16x16x64_i8 v[90:93], v[138:141], v[174:177], v[90:93]
	v_mfma_i32_16x16x64_i8 v[86:89], v[142:145], v[178:181], v[86:89]
	v_mfma_i32_16x16x64_i8 v[82:85], v[138:141], v[178:181], v[82:85]
	v_mfma_i32_16x16x64_i8 v[78:81], v[142:145], v[210:213], v[78:81]
	v_mfma_i32_16x16x64_i8 v[74:77], v[138:141], v[210:213], v[74:77]
	v_mfma_i32_16x16x64_i8 v[70:73], v[142:145], v[214:217], v[70:73]
	v_mfma_i32_16x16x64_i8 v[66:69], v[138:141], v[214:217], v[66:69]
	s_nop 0
	v_mfma_i32_16x16x64_i8 v[94:97], v[130:133], v[202:205], v[94:97]
	v_mfma_i32_16x16x64_i8 v[90:93], v[134:137], v[202:205], v[90:93]
	v_mfma_i32_16x16x64_i8 v[86:89], v[130:133], v[206:209], v[86:89]
	v_mfma_i32_16x16x64_i8 v[82:85], v[134:137], v[206:209], v[82:85]
	v_mfma_i32_16x16x64_i8 v[78:81], v[130:133], v[218:221], v[78:81]
	v_mfma_i32_16x16x64_i8 v[74:77], v[134:137], v[218:221], v[74:77]
	v_mfma_i32_16x16x64_i8 v[70:73], v[130:133], v[222:225], v[70:73]
	v_mfma_i32_16x16x64_i8 v[66:69], v[134:137], v[222:225], v[66:69]
	s_setprio 0
	s_barrier
	s_mov_b32 m0, s24
	v_lshl_add_u64 v[174:175], s[62:63], 0, v[166:167]
	ds_read_b128 v[202:205], v200 offset:16384
	ds_read_b128 v[206:209], v200 offset:18432
	ds_read_b128 v[210:213], v201 offset:16384
	ds_read_b128 v[214:217], v201 offset:18432
	ds_read_b128 v[218:221], v200 offset:20480
	ds_read_b128 v[222:225], v200 offset:22528
	ds_read_b128 v[226:229], v201 offset:20480
	ds_read_b128 v[230:233], v201 offset:22528
	global_load_lds_dwordx4 v[174:175], off
	v_lshl_add_u64 v[176:177], s[62:63], 0, v[162:163]
	s_mov_b32 m0, s25
	v_lshl_add_u64 v[178:179], s[64:65], 0, v[166:167]
	global_load_lds_dwordx4 v[176:177], off
	s_mov_b32 m0, s33
	v_lshl_add_u64 v[180:181], s[60:61], 0, v[164:165]
	global_load_lds_dwordx4 v[178:179], off
	v_lshl_add_u64 v[178:179], s[64:65], 0, v[162:163]
	s_mov_b32 m0, s35
	s_nop 0
	global_load_lds_dwordx4 v[178:179], off
	v_lshl_add_u64 v[178:179], s[60:61], 0, v[168:169]
	s_mov_b32 m0, s23
	s_nop 0
	global_load_lds_dwordx4 v[178:179], off
	s_mov_b32 m0, s49
	s_nop 0
	global_load_lds_dwordx4 v[180:181], off
	s_waitcnt vmcnt(8)
	s_waitcnt lgkmcnt(0)
	s_barrier
; #define PG8_STAGE(bufoff, gbase, voff) do { _Pragma("unroll") for (int _i = 0; _i < 2; ++_i) \
;         __builtin_amdgcn_global_load_lds((const unsigned*)((const char*)(gbase) + (voff)[_i]), (LAS unsigned*)(lds + (bufoff) + ldsw + _i * 8192), 16, 0, 0); } while (0)
; #define PG8_LDA(dst, b, h) do { _Pragma("unroll") for (int m = 0; m < 4; ++m) _Pragma("unroll") for (int k = 0; k < 2; ++k) dst[m][k] = *(const LAS bf16x8*)(lds + PG8_SA(b, h) + aoff + m * 2048 + k * 1024); } while (0)
; #define PG8_LDB(dst, b, h) do { _Pragma("unroll") for (int n = 0; n < 2; ++n) _Pragma("unroll") for (int k = 0; k < 2; ++k) dst[n][k] = *(const LAS bf16x8*)(lds + PG8_SB(b, h) + boff + n * 2048 + k * 1024); } while (0)
; #define PG8_MMA(ai, bj, At, Bt) do { __builtin_amdgcn_s_setprio(1); _Pragma("unroll") for (int m = 0; m < 4; ++m) _Pragma("unroll") for (int n = 0; n < 2; ++n) _Pragma("unroll") for (int k = 0; k < 2; ++k) \
;         acc[ai][bj][m][n] = __builtin_amdgcn_mfma_f32_16x16x32_bf16(Bt[n][k], At[m][k], acc[ai][bj][m][n], 0, 0, 0); __builtin_amdgcn_s_setprio(0); } while (0)
; #define PG8_WAIT_V(n) asm volatile("s_waitcnt vmcnt(" #n ")" ::: "memory")
; #define PG8_WAIT_L(n) asm volatile("s_waitcnt lgkmcnt(" #n ")" ::: "memory")
; #define PG8_BAR __builtin_amdgcn_s_barrier()
; #define PG8_SCHED __builtin_amdgcn_sched_barrier(0)
; #define PG8_STAGE(bufoff, gbase, voff) do { _Pragma("unroll") for (int _i = 0; _i < 2; ++_i) \
;         __builtin_amdgcn_global_load_lds((const unsigned*)((const char*)(gbase) + (voff)[_i]), (LAS unsigned*)(lds + (bufoff) + ldsw + _i * 8192), 16, 0, 0); } while (0)
; #define PG8_LDA(dst, b, h) do { _Pragma("unroll") for (int m = 0; m < 4; ++m) PG8_LD1(dst[m], PG8_SA(b, h) + aoff0 + m * 2048, PG8_SA(b, h) + aoff1 + m * 2048); } while (0)
; #define PG8_LDB(dst, b, h) do { _Pragma("unroll") for (int n = 0; n < 2; ++n) PG8_LD1(dst[n], PG8_SB(b, h) + boff0 + n * 2048, PG8_SB(b, h) + boff1 + n * 2048); } while (0)
; #define PG8_BAR __builtin_amdgcn_s_barrier()
;     ...
;             PG8_WAIT_V(8); PG8_WAIT_L(0); PG8_BAR; PG8_MMA(1, 0, At, B0); PG8_MMA(1, 1, At, B1); PG8_BAR; PG8_SCHED;
;             PG8_LDB(B0, 1, 0); PG8_LDB(B1, 1, 1); PG8_SCHED; PG8_LDA(At, 1, 0); PG8_STAGE(PG8_SA(0, 1), a2 + hstepA, voffA);
;             PG8_WAIT_V(8); PG8_WAIT_L(0); PG8_BAR; PG8_MMA(0, 0, At, B0); PG8_MMA(0, 1, At, B1); PG8_BAR; PG8_SCHED;
	s_setprio 1
	v_mfma_i32_16x16x64_i8 v[62:65], v[158:161], v[202:205], v[62:65]
	v_mfma_i32_16x16x64_i8 v[58:61], v[154:157], v[202:205], v[58:61]
	v_mfma_i32_16x16x64_i8 v[54:57], v[158:161], v[206:209], v[54:57]
	v_mfma_i32_16x16x64_i8 v[50:53], v[154:157], v[206:209], v[50:53]
	v_mfma_i32_16x16x64_i8 v[46:49], v[158:161], v[218:221], v[46:49]
	v_mfma_i32_16x16x64_i8 v[42:45], v[154:157], v[218:221], v[42:45]
	v_mfma_i32_16x16x64_i8 v[38:41], v[158:161], v[222:225], v[38:41]
	v_mfma_i32_16x16x64_i8 v[34:37], v[154:157], v[222:225], v[34:37]
	s_nop 0
	v_mfma_i32_16x16x64_i8 v[62:65], v[146:149], v[210:213], v[62:65]
	v_mfma_i32_16x16x64_i8 v[58:61], v[150:153], v[210:213], v[58:61]
	v_mfma_i32_16x16x64_i8 v[54:57], v[146:149], v[214:217], v[54:57]
	v_mfma_i32_16x16x64_i8 v[50:53], v[150:153], v[214:217], v[50:53]
	v_mfma_i32_16x16x64_i8 v[46:49], v[146:149], v[226:229], v[46:49]
	v_mfma_i32_16x16x64_i8 v[42:45], v[150:153], v[226:229], v[42:45]
	v_mfma_i32_16x16x64_i8 v[38:41], v[146:149], v[230:233], v[38:41]
	v_mfma_i32_16x16x64_i8 v[34:37], v[150:153], v[230:233], v[34:37]
	s_setprio 0
	s_setprio 1
	v_mfma_i32_16x16x64_i8 v[30:33], v[142:145], v[202:205], v[30:33]
	v_mfma_i32_16x16x64_i8 v[26:29], v[138:141], v[202:205], v[26:29]
	v_mfma_i32_16x16x64_i8 v[22:25], v[142:145], v[206:209], v[22:25]
	v_mfma_i32_16x16x64_i8 v[18:21], v[138:141], v[206:209], v[18:21]
	v_mfma_i32_16x16x64_i8 v[14:17], v[142:145], v[218:221], v[14:17]
	v_mfma_i32_16x16x64_i8 v[10:13], v[138:141], v[218:221], v[10:13]
	v_mfma_i32_16x16x64_i8 v[6:9], v[142:145], v[222:225], v[6:9]
	v_mfma_i32_16x16x64_i8 v[2:5], v[138:141], v[222:225], v[2:5]
	s_nop 0
	v_mfma_i32_16x16x64_i8 v[30:33], v[130:133], v[210:213], v[30:33]
	v_mfma_i32_16x16x64_i8 v[26:29], v[134:137], v[210:213], v[26:29]
	v_mfma_i32_16x16x64_i8 v[22:25], v[130:133], v[214:217], v[22:25]
	v_mfma_i32_16x16x64_i8 v[18:21], v[134:137], v[214:217], v[18:21]
	v_mfma_i32_16x16x64_i8 v[14:17], v[130:133], v[226:229], v[14:17]
	v_mfma_i32_16x16x64_i8 v[10:13], v[134:137], v[226:229], v[10:13]
	v_mfma_i32_16x16x64_i8 v[6:9], v[130:133], v[230:233], v[6:9]
	v_mfma_i32_16x16x64_i8 v[2:5], v[134:137], v[230:233], v[2:5]
	s_setprio 0
	s_barrier
	ds_read_b128 v[130:133], v187
	ds_read_b128 v[134:137], v188
	ds_read_b128 v[138:141], v195
	ds_read_b128 v[142:145], v196
	ds_read_b128 v[146:149], v189
	ds_read_b128 v[150:153], v190
	ds_read_b128 v[154:157], v197
	ds_read_b128 v[158:161], v198
	s_mov_b32 m0, s66
	v_lshl_add_u64 v[234:235], s[58:59], 0, v[168:169]
	ds_read_b128 v[202:205], v200 offset:32768
	ds_read_b128 v[206:209], v200 offset:34816
	ds_read_b128 v[210:213], v201 offset:32768
	ds_read_b128 v[214:217], v201 offset:34816
	ds_read_b128 v[218:221], v200 offset:36864
	ds_read_b128 v[222:225], v200 offset:38912
	ds_read_b128 v[226:229], v201 offset:36864
	ds_read_b128 v[230:233], v201 offset:38912
	global_load_lds_dwordx4 v[234:235], off
	v_lshl_add_u64 v[234:235], s[58:59], 0, v[164:165]
	s_mov_b32 m0, s67
	s_nop 0
	global_load_lds_dwordx4 v[234:235], off
	s_waitcnt vmcnt(8)
	s_waitcnt lgkmcnt(0)
	s_barrier
	s_setprio 1
	v_mfma_i32_16x16x64_i8 v[126:129], v[130:133], v[202:205], v[126:129]
	v_mfma_i32_16x16x64_i8 v[122:125], v[138:141], v[202:205], v[122:125]
	v_mfma_i32_16x16x64_i8 v[118:121], v[130:133], v[206:209], v[118:121]
	v_mfma_i32_16x16x64_i8 v[114:117], v[138:141], v[206:209], v[114:117]
	v_mfma_i32_16x16x64_i8 v[110:113], v[130:133], v[218:221], v[110:113]
	v_mfma_i32_16x16x64_i8 v[106:109], v[138:141], v[218:221], v[106:109]
	v_mfma_i32_16x16x64_i8 v[102:105], v[130:133], v[222:225], v[102:105]
	v_mfma_i32_16x16x64_i8 v[98:101], v[138:141], v[222:225], v[98:101]
	s_nop 0
	v_mfma_i32_16x16x64_i8 v[126:129], v[134:137], v[210:213], v[126:129]
	v_mfma_i32_16x16x64_i8 v[122:125], v[142:145], v[210:213], v[122:125]
	v_mfma_i32_16x16x64_i8 v[118:121], v[134:137], v[214:217], v[118:121]
	v_mfma_i32_16x16x64_i8 v[114:117], v[142:145], v[214:217], v[114:117]
	v_mfma_i32_16x16x64_i8 v[110:113], v[134:137], v[226:229], v[110:113]
	v_mfma_i32_16x16x64_i8 v[106:109], v[142:145], v[226:229], v[106:109]
	v_mfma_i32_16x16x64_i8 v[102:105], v[134:137], v[230:233], v[102:105]
	v_mfma_i32_16x16x64_i8 v[98:101], v[142:145], v[230:233], v[98:101]
	s_setprio 0
	s_setprio 1
	v_mfma_i32_16x16x64_i8 v[94:97], v[146:149], v[202:205], v[94:97]
	v_mfma_i32_16x16x64_i8 v[90:93], v[154:157], v[202:205], v[90:93]
	v_mfma_i32_16x16x64_i8 v[86:89], v[146:149], v[206:209], v[86:89]
	v_mfma_i32_16x16x64_i8 v[82:85], v[154:157], v[206:209], v[82:85]
	v_mfma_i32_16x16x64_i8 v[78:81], v[146:149], v[218:221], v[78:81]
	v_mfma_i32_16x16x64_i8 v[74:77], v[154:157], v[218:221], v[74:77]
	v_mfma_i32_16x16x64_i8 v[70:73], v[146:149], v[222:225], v[70:73]
	v_mfma_i32_16x16x64_i8 v[66:69], v[154:157], v[222:225], v[66:69]
	s_nop 0
	v_mfma_i32_16x16x64_i8 v[94:97], v[150:153], v[210:213], v[94:97]
	v_mfma_i32_16x16x64_i8 v[90:93], v[158:161], v[210:213], v[90:93]
	v_mfma_i32_16x16x64_i8 v[86:89], v[150:153], v[214:217], v[86:89]
	v_mfma_i32_16x16x64_i8 v[82:85], v[158:161], v[214:217], v[82:85]
	v_mfma_i32_16x16x64_i8 v[78:81], v[150:153], v[226:229], v[78:81]
	v_mfma_i32_16x16x64_i8 v[74:77], v[158:161], v[226:229], v[74:77]
	v_mfma_i32_16x16x64_i8 v[70:73], v[150:153], v[230:233], v[70:73]
	v_mfma_i32_16x16x64_i8 v[66:69], v[158:161], v[230:233], v[66:69]
	s_setprio 0
	s_barrier
; #define PG8_STAGE(bufoff, gbase, voff) do { _Pragma("unroll") for (int _i = 0; _i < 2; ++_i) \
;         __builtin_amdgcn_global_load_lds((const unsigned*)((const char*)(gbase) + (voff)[_i]), (LAS unsigned*)(lds + (bufoff) + ldsw + _i * 8192), 16, 0, 0); } while (0)
; #define PG8_LDA(dst, b, h) do { _Pragma("unroll") for (int m = 0; m < 4; ++m) _Pragma("unroll") for (int k = 0; k < 2; ++k) dst[m][k] = *(const LAS bf16x8*)(lds + PG8_SA(b, h) + aoff + m * 2048 + k * 1024); } while (0)
; #define PG8_MMA(ai, bj, At, Bt) do { __builtin_amdgcn_s_setprio(1); _Pragma("unroll") for (int m = 0; m < 4; ++m) _Pragma("unroll") for (int n = 0; n < 2; ++n) _Pragma("unroll") for (int k = 0; k < 2; ++k) \
;         acc[ai][bj][m][n] = __builtin_amdgcn_mfma_f32_16x16x32_bf16(Bt[n][k], At[m][k], acc[ai][bj][m][n], 0, 0, 0); __builtin_amdgcn_s_setprio(0); } while (0)
; #define PG8_WAIT_V(n) asm volatile("s_waitcnt vmcnt(" #n ")" ::: "memory")
; #define PG8_WAIT_L(n) asm volatile("s_waitcnt lgkmcnt(" #n ")" ::: "memory")
; #define PG8_BAR __builtin_amdgcn_s_barrier()
; #define PG8_SCHED __builtin_amdgcn_sched_barrier(0)
; #define PG8_STAGE(bufoff, gbase, voff) do { _Pragma("unroll") for (int _i = 0; _i < 2; ++_i) \
;         __builtin_amdgcn_global_load_lds((const unsigned*)((const char*)(gbase) + (voff)[_i]), (LAS unsigned*)(lds + (bufoff) + ldsw + _i * 8192), 16, 0, 0); } while (0)
; #define PG8_LDA(dst, b, h) do { _Pragma("unroll") for (int m = 0; m < 4; ++m) PG8_LD1(dst[m], PG8_SA(b, h) + aoff0 + m * 2048, PG8_SA(b, h) + aoff1 + m * 2048); } while (0)
; #define PG8_WAIT_V(n) asm volatile("s_waitcnt vmcnt(" #n ")" ::: "memory")
; #define PG8_WAIT_L(n) asm volatile("s_waitcnt lgkmcnt(" #n ")" ::: "memory")
; #define PG8_BAR __builtin_amdgcn_s_barrier()
; #define PG8_SCHED __builtin_amdgcn_sched_barrier(0)
;     ...
;             PG8_LDA(At, 1, 1); PG8_STAGE(PG8_SB(1, 0), b3, voffB); PG8_STAGE(PG8_SB(1, 1), b3 + hstepB, voffB); PG8_STAGE(PG8_SA(1, 0), a3, voffA);
;             PG8_WAIT_V(8); PG8_WAIT_L(0); PG8_BAR; PG8_MMA(1, 0, At, B0); PG8_MMA(1, 1, At, B1); PG8_BAR; PG8_SCHED;
;         }
;         asm volatile("s_nop 15\n\ts_nop 15" ::: "memory");
;         if (wr == 0) PG8_BAR;
	s_mov_b32 m0, s74
	v_lshl_add_u64 v[174:175], v[174:175], 0, s[10:11]
	ds_read_b128 v[202:205], v200 offset:49152
	ds_read_b128 v[206:209], v200 offset:51200
	ds_read_b128 v[210:213], v201 offset:49152
	ds_read_b128 v[214:217], v201 offset:51200
	ds_read_b128 v[218:221], v200 offset:53248
	ds_read_b128 v[222:225], v200 offset:55296
	ds_read_b128 v[226:229], v201 offset:53248
	ds_read_b128 v[230:233], v201 offset:55296
	global_load_lds_dwordx4 v[174:175], off
	v_lshl_add_u64 v[174:175], v[176:177], 0, s[10:11]
	s_mov_b32 m0, s75
	s_nop 0
	global_load_lds_dwordx4 v[174:175], off
	v_lshl_add_u64 v[174:175], s[56:57], 0, v[166:167]
	s_mov_b32 m0, s80
	s_nop 0
	global_load_lds_dwordx4 v[174:175], off
	v_lshl_add_u64 v[174:175], s[56:57], 0, v[162:163]
	s_mov_b32 m0, s81
	s_nop 0
	global_load_lds_dwordx4 v[174:175], off
	v_lshl_add_u64 v[174:175], v[178:179], 0, s[10:11]
	s_mov_b32 m0, s78
	s_nop 0
	global_load_lds_dwordx4 v[174:175], off
	v_lshl_add_u64 v[174:175], v[180:181], 0, s[10:11]
	s_mov_b32 m0, s79
	s_nop 0
	global_load_lds_dwordx4 v[174:175], off
	s_waitcnt vmcnt(8)
	s_waitcnt lgkmcnt(0)
	s_barrier
	s_setprio 1
	v_mfma_i32_16x16x64_i8 v[62:65], v[130:133], v[202:205], v[62:65]
	v_mfma_i32_16x16x64_i8 v[58:61], v[138:141], v[202:205], v[58:61]
	v_mfma_i32_16x16x64_i8 v[54:57], v[130:133], v[206:209], v[54:57]
	v_mfma_i32_16x16x64_i8 v[50:53], v[138:141], v[206:209], v[50:53]
	v_mfma_i32_16x16x64_i8 v[46:49], v[130:133], v[218:221], v[46:49]
	v_mfma_i32_16x16x64_i8 v[42:45], v[138:141], v[218:221], v[42:45]
	v_mfma_i32_16x16x64_i8 v[38:41], v[130:133], v[222:225], v[38:41]
	v_mfma_i32_16x16x64_i8 v[34:37], v[138:141], v[222:225], v[34:37]
	s_nop 0
	v_mfma_i32_16x16x64_i8 v[62:65], v[134:137], v[210:213], v[62:65]
	v_mfma_i32_16x16x64_i8 v[58:61], v[142:145], v[210:213], v[58:61]
	v_mfma_i32_16x16x64_i8 v[54:57], v[134:137], v[214:217], v[54:57]
	v_mfma_i32_16x16x64_i8 v[50:53], v[142:145], v[214:217], v[50:53]
	v_mfma_i32_16x16x64_i8 v[46:49], v[134:137], v[226:229], v[46:49]
	v_mfma_i32_16x16x64_i8 v[42:45], v[142:145], v[226:229], v[42:45]
	v_mfma_i32_16x16x64_i8 v[38:41], v[134:137], v[230:233], v[38:41]
	v_mfma_i32_16x16x64_i8 v[34:37], v[142:145], v[230:233], v[34:37]
	s_setprio 0
	s_setprio 1
	v_mfma_i32_16x16x64_i8 v[30:33], v[146:149], v[202:205], v[30:33]
	v_mfma_i32_16x16x64_i8 v[26:29], v[154:157], v[202:205], v[26:29]
	v_mfma_i32_16x16x64_i8 v[22:25], v[146:149], v[206:209], v[22:25]
	v_mfma_i32_16x16x64_i8 v[18:21], v[154:157], v[206:209], v[18:21]
	v_mfma_i32_16x16x64_i8 v[14:17], v[146:149], v[218:221], v[14:17]
	v_mfma_i32_16x16x64_i8 v[10:13], v[154:157], v[218:221], v[10:13]
	v_mfma_i32_16x16x64_i8 v[6:9], v[146:149], v[222:225], v[6:9]
	v_mfma_i32_16x16x64_i8 v[2:5], v[154:157], v[222:225], v[2:5]
	s_nop 0
	v_mfma_i32_16x16x64_i8 v[30:33], v[150:153], v[210:213], v[30:33]
	v_mfma_i32_16x16x64_i8 v[26:29], v[158:161], v[210:213], v[26:29]
	v_mfma_i32_16x16x64_i8 v[22:25], v[150:153], v[214:217], v[22:25]
	v_mfma_i32_16x16x64_i8 v[18:21], v[158:161], v[214:217], v[18:21]
	v_mfma_i32_16x16x64_i8 v[14:17], v[150:153], v[226:229], v[14:17]
	v_mfma_i32_16x16x64_i8 v[10:13], v[158:161], v[226:229], v[10:13]
	v_mfma_i32_16x16x64_i8 v[6:9], v[150:153], v[230:233], v[6:9]
	v_mfma_i32_16x16x64_i8 v[2:5], v[158:161], v[230:233], v[2:5]
	s_setprio 0
	s_barrier
	s_andn2_b64 vcc, exec, s[54:55]
	s_mov_b64 s[56:57], -1
	s_mov_b64 s[54:55], 0
	s_mov_b64 s[58:59], 0x100
	s_cbranch_vccz .LBB0_960
	s_nop 15
	s_nop 15
	s_and_b64 vcc, exec, s[14:15]
	s_cbranch_vccz .LBB0_963
	s_barrier

; #define PG8_STAGE(bufoff, gbase, voff) do { _Pragma("unroll") for (int _i = 0; _i < 2; ++_i) \
;         __builtin_amdgcn_global_load_lds((const unsigned*)((const char*)(gbase) + (voff)[_i]), (LAS unsigned*)(lds + (bufoff) + ldsw + _i * 8192), 16, 0, 0); } while (0)
; #define PG8_LDA(dst, b, h) do { _Pragma("unroll") for (int m = 0; m < 4; ++m) _Pragma("unroll") for (int k = 0; k < 2; ++k) dst[m][k] = *(const LAS bf16x8*)(lds + PG8_SA(b, h) + aoff + m * 2048 + k * 1024); } while (0)
; #define PG8_LDB(dst, b, h) do { _Pragma("unroll") for (int n = 0; n < 2; ++n) _Pragma("unroll") for (int k = 0; k < 2; ++k) dst[n][k] = *(const LAS bf16x8*)(lds + PG8_SB(b, h) + boff + n * 2048 + k * 1024); } while (0)
; #define PG8_MMA(ai, bj, At, Bt) do { __builtin_amdgcn_s_setprio(1); _Pragma("unroll") for (int m = 0; m < 4; ++m) _Pragma("unroll") for (int n = 0; n < 2; ++n) _Pragma("unroll") for (int k = 0; k < 2; ++k) \
;         acc[ai][bj][m][n] = __builtin_amdgcn_mfma_f32_16x16x32_bf16(Bt[n][k], At[m][k], acc[ai][bj][m][n], 0, 0, 0); __builtin_amdgcn_s_setprio(0); } while (0)
; #define PG8_WAIT_V(n) asm volatile("s_waitcnt vmcnt(" #n ")" ::: "memory")
; #define PG8_WAIT_L(n) asm volatile("s_waitcnt lgkmcnt(" #n ")" ::: "memory")
; #define PG8_BAR __builtin_amdgcn_s_barrier()
; #define PG8_SCHED __builtin_amdgcn_sched_barrier(0)
; #define PG8_STAGE(bufoff, gbase, voff) do { _Pragma("unroll") for (int _i = 0; _i < 2; ++_i) \
;         __builtin_amdgcn_global_load_lds((const unsigned*)((const char*)(gbase) + (voff)[_i]), (LAS unsigned*)(lds + (bufoff) + ldsw + _i * 8192), 16, 0, 0); } while (0)
; #define PG8_LDA(dst, b, h) do { _Pragma("unroll") for (int m = 0; m < 4; ++m) PG8_LD1(dst[m], PG8_SA(b, h) + aoff0 + m * 2048, PG8_SA(b, h) + aoff1 + m * 2048); } while (0)
; #define PG8_WAIT_V(n) asm volatile("s_waitcnt vmcnt(" #n ")" ::: "memory")
;     ...
;             PG8_LDB(B0, 0, 0); PG8_LDB(B1, 0, 1); PG8_SCHED; PG8_LDA(At, 0, 0); PG8_STAGE(PG8_SA(1, 1), a1 + hstepA, voffA);
;             PG8_WAIT_V(8); PG8_WAIT_L(0); PG8_BAR; PG8_MMA(0, 0, At, B0); PG8_MMA(0, 1, At, B1); PG8_BAR; PG8_SCHED;
;             PG8_LDA(At, 0, 1); PG8_STAGE(PG8_SB(0, 0), b2, voffB); PG8_STAGE(PG8_SB(0, 1), b2 + hstepB, voffB); PG8_STAGE(PG8_SA(0, 0), a2, voffA);
;             PG8_WAIT_V(8); PG8_WAIT_L(0); PG8_BAR; PG8_MMA(1, 0, At, B0); PG8_MMA(1, 1, At, B1); PG8_BAR; PG8_SCHED;
.LBB0_1121:
	ds_read_b128 v[18:21], v183
	ds_read_b128 v[22:25], v184
	ds_read_b128 v[26:29], v191
	ds_read_b128 v[30:33], v192
	ds_read_b128 v[2:5], v185
	ds_read_b128 v[6:9], v186
	ds_read_b128 v[10:13], v193
	ds_read_b128 v[14:17], v194
	s_add_u32 s56, s54, 0x100
	s_addc_u32 s57, s55, 0
	s_cmp_eq_u32 s83, 12
	s_cselect_b32 s61, s41, s57
	s_cselect_b32 s60, s43, s56
	s_cselect_b32 s59, s79, s82
	s_cselect_b32 s58, s80, s81
	v_lshl_add_u64 v[226:227], s[54:55], 0, v[166:167]
	s_add_i32 m0, s15, 0xc000
	ds_read_b128 v[174:177], v200
	ds_read_b128 v[202:205], v200 offset:2048
	ds_read_b128 v[178:181], v201
	ds_read_b128 v[206:209], v201 offset:2048
	ds_read_b128 v[210:213], v200 offset:4096
	ds_read_b128 v[218:221], v200 offset:6144
	ds_read_b128 v[214:217], v201 offset:4096
	ds_read_b128 v[222:225], v201 offset:6144
	global_load_lds_dwordx4 v[226:227], off
	v_lshl_add_u64 v[226:227], s[54:55], 0, v[168:169]
	s_add_i32 m0, s15, 0xe000
	s_nop 0
	global_load_lds_dwordx4 v[226:227], off
	s_waitcnt vmcnt(8)
	s_waitcnt lgkmcnt(0)
	s_barrier
	s_setprio 1
	v_mfma_f32_16x16x128_f8f6f4 v[158:161], v[18:25], v[174:181], v[158:161]
	v_mfma_f32_16x16x128_f8f6f4 v[154:157], v[26:33], v[174:181], v[154:157]
	v_mfma_f32_16x16x128_f8f6f4 v[150:153], v[18:25], v[202:209], v[150:153]
	v_mfma_f32_16x16x128_f8f6f4 v[146:149], v[26:33], v[202:209], v[146:149]
	v_mfma_f32_16x16x128_f8f6f4 v[126:129], v[18:25], v[210:217], v[126:129]
	v_mfma_f32_16x16x128_f8f6f4 v[122:125], v[26:33], v[210:217], v[122:125]
	v_mfma_f32_16x16x128_f8f6f4 v[118:121], v[18:25], v[218:225], v[118:121]
	v_mfma_f32_16x16x128_f8f6f4 v[114:117], v[26:33], v[218:225], v[114:117]
	s_setprio 0
	s_setprio 1
	v_mfma_f32_16x16x128_f8f6f4 v[142:145], v[2:9], v[174:181], v[142:145]
	v_mfma_f32_16x16x128_f8f6f4 v[138:141], v[10:17], v[174:181], v[138:141]
	v_mfma_f32_16x16x128_f8f6f4 v[134:137], v[2:9], v[202:209], v[134:137]
	v_mfma_f32_16x16x128_f8f6f4 v[130:133], v[10:17], v[202:209], v[130:133]
	v_mfma_f32_16x16x128_f8f6f4 v[110:113], v[2:9], v[210:217], v[110:113]
	v_mfma_f32_16x16x128_f8f6f4 v[106:109], v[10:17], v[210:217], v[106:109]
	v_mfma_f32_16x16x128_f8f6f4 v[102:105], v[2:9], v[218:225], v[102:105]
	v_mfma_f32_16x16x128_f8f6f4 v[98:101], v[10:17], v[218:225], v[98:101]
	s_setprio 0
	s_barrier
	s_mov_b32 m0, s24
	v_lshl_add_u64 v[174:175], s[58:59], 0, v[164:165]
	s_add_u32 s18, s58, 0x40000
	ds_read_b128 v[202:205], v200 offset:16384
	ds_read_b128 v[210:213], v200 offset:18432
	ds_read_b128 v[206:209], v201 offset:16384
	ds_read_b128 v[214:217], v201 offset:18432
	ds_read_b128 v[218:221], v200 offset:20480
	ds_read_b128 v[226:229], v200 offset:22528
	ds_read_b128 v[222:225], v201 offset:20480
	ds_read_b128 v[230:233], v201 offset:22528
	global_load_lds_dwordx4 v[174:175], off
	v_lshl_add_u64 v[176:177], s[58:59], 0, v[162:163]
	s_mov_b32 m0, s25
	s_addc_u32 s19, s59, 0
	global_load_lds_dwordx4 v[176:177], off
	v_lshl_add_u64 v[178:179], s[18:19], 0, v[164:165]
	s_mov_b32 m0, s33
	v_lshl_add_u64 v[180:181], s[60:61], 0, v[162:163]
	global_load_lds_dwordx4 v[178:179], off
	v_lshl_add_u64 v[178:179], s[18:19], 0, v[162:163]
	s_mov_b32 m0, s35
	s_nop 0
	global_load_lds_dwordx4 v[178:179], off
	v_lshl_add_u64 v[178:179], s[60:61], 0, v[164:165]
	s_mov_b32 m0, s15
	s_nop 0
	global_load_lds_dwordx4 v[178:179], off
	s_mov_b32 m0, s62
	s_nop 0
	global_load_lds_dwordx4 v[180:181], off
	s_waitcnt vmcnt(8)
	s_waitcnt lgkmcnt(0)
	s_barrier
	s_setprio 1
	v_mfma_f32_16x16x128_f8f6f4 v[94:97], v[18:25], v[202:209], v[94:97]
	v_mfma_f32_16x16x128_f8f6f4 v[90:93], v[26:33], v[202:209], v[90:93]
	v_mfma_f32_16x16x128_f8f6f4 v[86:89], v[18:25], v[210:217], v[86:89]
	v_mfma_f32_16x16x128_f8f6f4 v[78:81], v[26:33], v[210:217], v[78:81]
	v_mfma_f32_16x16x128_f8f6f4 v[70:73], v[18:25], v[218:225], v[70:73]
	v_mfma_f32_16x16x128_f8f6f4 v[62:65], v[26:33], v[218:225], v[62:65]
	v_mfma_f32_16x16x128_f8f6f4 v[54:57], v[18:25], v[226:233], v[54:57]
	v_mfma_f32_16x16x128_f8f6f4 v[46:49], v[26:33], v[226:233], v[46:49]
	s_setprio 0
	s_setprio 1
	v_mfma_f32_16x16x128_f8f6f4 v[82:85], v[2:9], v[202:209], v[82:85]
	v_mfma_f32_16x16x128_f8f6f4 v[74:77], v[10:17], v[202:209], v[74:77]
	v_mfma_f32_16x16x128_f8f6f4 v[66:69], v[2:9], v[210:217], v[66:69]
	v_mfma_f32_16x16x128_f8f6f4 v[58:61], v[10:17], v[210:217], v[58:61]
	v_mfma_f32_16x16x128_f8f6f4 v[50:53], v[2:9], v[218:225], v[50:53]
	v_mfma_f32_16x16x128_f8f6f4 v[42:45], v[10:17], v[218:225], v[42:45]
	v_mfma_f32_16x16x128_f8f6f4 v[38:41], v[2:9], v[226:233], v[38:41]
	v_mfma_f32_16x16x128_f8f6f4 v[34:37], v[10:17], v[226:233], v[34:37]
	s_setprio 0
	s_barrier
; #define PG8_STAGE(bufoff, gbase, voff) do { _Pragma("unroll") for (int _i = 0; _i < 2; ++_i) \
;         __builtin_amdgcn_global_load_lds((const unsigned*)((const char*)(gbase) + (voff)[_i]), (LAS unsigned*)(lds + (bufoff) + ldsw + _i * 8192), 16, 0, 0); } while (0)
; #define PG8_LDA(dst, b, h) do { _Pragma("unroll") for (int m = 0; m < 4; ++m) _Pragma("unroll") for (int k = 0; k < 2; ++k) dst[m][k] = *(const LAS bf16x8*)(lds + PG8_SA(b, h) + aoff + m * 2048 + k * 1024); } while (0)
; #define PG8_LDB(dst, b, h) do { _Pragma("unroll") for (int n = 0; n < 2; ++n) _Pragma("unroll") for (int k = 0; k < 2; ++k) dst[n][k] = *(const LAS bf16x8*)(lds + PG8_SB(b, h) + boff + n * 2048 + k * 1024); } while (0)
; #define PG8_MMA(ai, bj, At, Bt) do { __builtin_amdgcn_s_setprio(1); _Pragma("unroll") for (int m = 0; m < 4; ++m) _Pragma("unroll") for (int n = 0; n < 2; ++n) _Pragma("unroll") for (int k = 0; k < 2; ++k) \
;         acc[ai][bj][m][n] = __builtin_amdgcn_mfma_f32_16x16x32_bf16(Bt[n][k], At[m][k], acc[ai][bj][m][n], 0, 0, 0); __builtin_amdgcn_s_setprio(0); } while (0)
; #define PG8_WAIT_V(n) asm volatile("s_waitcnt vmcnt(" #n ")" ::: "memory")
; #define PG8_WAIT_L(n) asm volatile("s_waitcnt lgkmcnt(" #n ")" ::: "memory")
; #define PG8_BAR __builtin_amdgcn_s_barrier()
; #define PG8_SCHED __builtin_amdgcn_sched_barrier(0)
; #define PG8_STAGE(bufoff, gbase, voff) do { _Pragma("unroll") for (int _i = 0; _i < 2; ++_i) \
;         __builtin_amdgcn_global_load_lds((const unsigned*)((const char*)(gbase) + (voff)[_i]), (LAS unsigned*)(lds + (bufoff) + ldsw + _i * 8192), 16, 0, 0); } while (0)
; #define PG8_WAIT_V(n) asm volatile("s_waitcnt vmcnt(" #n ")" ::: "memory")
; #define PG8_WAIT_L(n) asm volatile("s_waitcnt lgkmcnt(" #n ")" ::: "memory")
;     ...
;             PG8_LDB(B0, 1, 0); PG8_LDB(B1, 1, 1); PG8_SCHED; PG8_LDA(At, 1, 0); PG8_STAGE(PG8_SA(0, 1), a2 + hstepA, voffA);
;             PG8_WAIT_V(8); PG8_WAIT_L(0); PG8_BAR; PG8_MMA(0, 0, At, B0); PG8_MMA(0, 1, At, B1); PG8_BAR; PG8_SCHED;
;             PG8_LDA(At, 1, 1); PG8_STAGE(PG8_SB(1, 0), b3, voffB); PG8_STAGE(PG8_SB(1, 1), b3 + hstepB, voffB); PG8_STAGE(PG8_SA(1, 0), a3, voffA);
;             PG8_WAIT_V(8); PG8_WAIT_L(0); PG8_BAR; PG8_MMA(1, 0, At, B0); PG8_MMA(1, 1, At, B1); PG8_BAR; PG8_SCHED;
;         }
;         asm volatile("s_nop 15\n\ts_nop 15" ::: "memory");
;         if (wr == 0) PG8_BAR;
	ds_read_b128 v[2:5], v187
	ds_read_b128 v[6:9], v188
	ds_read_b128 v[10:13], v195
	ds_read_b128 v[14:17], v196
	ds_read_b128 v[18:21], v189
	ds_read_b128 v[22:25], v190
	ds_read_b128 v[26:29], v197
	ds_read_b128 v[30:33], v198
	s_add_u32 s18, s60, 0x40000
	s_addc_u32 s19, s61, 0
	s_mov_b32 m0, s63
	v_lshl_add_u64 v[234:235], s[18:19], 0, v[164:165]
	ds_read_b128 v[202:205], v200 offset:32768
	ds_read_b128 v[210:213], v200 offset:34816
	ds_read_b128 v[206:209], v201 offset:32768
	ds_read_b128 v[214:217], v201 offset:34816
	ds_read_b128 v[218:221], v200 offset:36864
	ds_read_b128 v[226:229], v200 offset:38912
	ds_read_b128 v[222:225], v201 offset:36864
	ds_read_b128 v[230:233], v201 offset:38912
	global_load_lds_dwordx4 v[234:235], off
	v_lshl_add_u64 v[234:235], s[18:19], 0, v[162:163]
	s_mov_b32 m0, s64
	s_nop 0
	global_load_lds_dwordx4 v[234:235], off
	s_waitcnt vmcnt(8)
	s_waitcnt lgkmcnt(0)
	s_barrier
	s_setprio 1
	v_mfma_f32_16x16x128_f8f6f4 v[158:161], v[2:9], v[202:209], v[158:161]
	v_mfma_f32_16x16x128_f8f6f4 v[154:157], v[10:17], v[202:209], v[154:157]
	v_mfma_f32_16x16x128_f8f6f4 v[150:153], v[2:9], v[210:217], v[150:153]
	v_mfma_f32_16x16x128_f8f6f4 v[146:149], v[10:17], v[210:217], v[146:149]
	v_mfma_f32_16x16x128_f8f6f4 v[126:129], v[2:9], v[218:225], v[126:129]
	v_mfma_f32_16x16x128_f8f6f4 v[122:125], v[10:17], v[218:225], v[122:125]
	v_mfma_f32_16x16x128_f8f6f4 v[118:121], v[2:9], v[226:233], v[118:121]
	v_mfma_f32_16x16x128_f8f6f4 v[114:117], v[10:17], v[226:233], v[114:117]
	s_setprio 0
	s_setprio 1
	v_mfma_f32_16x16x128_f8f6f4 v[142:145], v[18:25], v[202:209], v[142:145]
	v_mfma_f32_16x16x128_f8f6f4 v[138:141], v[26:33], v[202:209], v[138:141]
	v_mfma_f32_16x16x128_f8f6f4 v[134:137], v[18:25], v[210:217], v[134:137]
	v_mfma_f32_16x16x128_f8f6f4 v[130:133], v[26:33], v[210:217], v[130:133]
	v_mfma_f32_16x16x128_f8f6f4 v[110:113], v[18:25], v[218:225], v[110:113]
	v_mfma_f32_16x16x128_f8f6f4 v[106:109], v[26:33], v[218:225], v[106:109]
	v_mfma_f32_16x16x128_f8f6f4 v[102:105], v[18:25], v[226:233], v[102:105]
	v_mfma_f32_16x16x128_f8f6f4 v[98:101], v[26:33], v[226:233], v[98:101]
	s_setprio 0
	s_barrier
	s_mov_b32 m0, s66
	v_lshl_add_u64 v[174:175], v[174:175], 0, s[10:11]
	s_add_u32 s18, s58, 0x40080
	ds_read_b128 v[202:205], v200 offset:49152
	ds_read_b128 v[210:213], v200 offset:51200
	ds_read_b128 v[206:209], v201 offset:49152
	ds_read_b128 v[214:217], v201 offset:51200
	ds_read_b128 v[218:221], v200 offset:53248
	ds_read_b128 v[226:229], v200 offset:55296
	ds_read_b128 v[222:225], v201 offset:53248
	ds_read_b128 v[230:233], v201 offset:55296
	global_load_lds_dwordx4 v[174:175], off
	v_lshl_add_u64 v[174:175], v[176:177], 0, s[10:11]
	s_mov_b32 m0, s67
	s_addc_u32 s19, s59, 0
	global_load_lds_dwordx4 v[174:175], off
	v_lshl_add_u64 v[174:175], s[18:19], 0, v[164:165]
	s_mov_b32 m0, s75
	s_nop 0
	global_load_lds_dwordx4 v[174:175], off
	v_lshl_add_u64 v[174:175], s[18:19], 0, v[162:163]
	s_mov_b32 m0, s78
	s_nop 0
	global_load_lds_dwordx4 v[174:175], off
	v_lshl_add_u64 v[174:175], v[178:179], 0, s[10:11]
	s_mov_b32 m0, s73
	s_nop 0
	global_load_lds_dwordx4 v[174:175], off
	v_lshl_add_u64 v[174:175], v[180:181], 0, s[10:11]
	s_mov_b32 m0, s74
	s_nop 0
	global_load_lds_dwordx4 v[174:175], off
	s_waitcnt vmcnt(8)
	s_waitcnt lgkmcnt(0)
	s_barrier
	s_setprio 1
	v_mfma_f32_16x16x128_f8f6f4 v[94:97], v[2:9], v[202:209], v[94:97]
	v_mfma_f32_16x16x128_f8f6f4 v[90:93], v[10:17], v[202:209], v[90:93]
	v_mfma_f32_16x16x128_f8f6f4 v[86:89], v[2:9], v[210:217], v[86:89]
	v_mfma_f32_16x16x128_f8f6f4 v[78:81], v[10:17], v[210:217], v[78:81]
	v_mfma_f32_16x16x128_f8f6f4 v[70:73], v[2:9], v[218:225], v[70:73]
	v_mfma_f32_16x16x128_f8f6f4 v[62:65], v[10:17], v[218:225], v[62:65]
	v_mfma_f32_16x16x128_f8f6f4 v[54:57], v[2:9], v[226:233], v[54:57]
	v_mfma_f32_16x16x128_f8f6f4 v[46:49], v[10:17], v[226:233], v[46:49]
	s_setprio 0
	s_setprio 1
	v_mfma_f32_16x16x128_f8f6f4 v[82:85], v[18:25], v[202:209], v[82:85]
	v_mfma_f32_16x16x128_f8f6f4 v[74:77], v[26:33], v[202:209], v[74:77]
	v_mfma_f32_16x16x128_f8f6f4 v[66:69], v[18:25], v[210:217], v[66:69]
	v_mfma_f32_16x16x128_f8f6f4 v[58:61], v[26:33], v[210:217], v[58:61]
	s_add_i32 s83, s83, 2
	s_add_u32 s81, s81, 0x100
	s_addc_u32 s82, s82, 0
	s_cmp_gt_u32 s83, 13
	s_mov_b64 s[54:55], s[56:57]
	v_mfma_f32_16x16x128_f8f6f4 v[50:53], v[18:25], v[218:225], v[50:53]
	v_mfma_f32_16x16x128_f8f6f4 v[42:45], v[26:33], v[218:225], v[42:45]
	v_mfma_f32_16x16x128_f8f6f4 v[38:41], v[18:25], v[226:233], v[38:41]
	v_mfma_f32_16x16x128_f8f6f4 v[34:37], v[26:33], v[226:233], v[34:37]
	s_setprio 0
	s_barrier
	s_cbranch_scc0 .LBB0_1121
	s_nop 15
	s_nop 15
	s_and_b64 vcc, exec, s[12:13]
	s_cbranch_vccz .LBB0_1124
	s_barrier

; #define PG8_STAGE(bufoff, gbase, voff) do { _Pragma("unroll") for (int _i = 0; _i < 2; ++_i) \
;         __builtin_amdgcn_global_load_lds((const unsigned*)((const char*)(gbase) + (voff)[_i]), (LAS unsigned*)(lds + (bufoff) + ldsw + _i * 8192), 16, 0, 0); } while (0)
; #define PG8_LDA(dst, b, h) do { _Pragma("unroll") for (int m = 0; m < 4; ++m) _Pragma("unroll") for (int k = 0; k < 2; ++k) dst[m][k] = *(const LAS bf16x8*)(lds + PG8_SA(b, h) + aoff + m * 2048 + k * 1024); } while (0)
; #define PG8_LDB(dst, b, h) do { _Pragma("unroll") for (int n = 0; n < 2; ++n) _Pragma("unroll") for (int k = 0; k < 2; ++k) dst[n][k] = *(const LAS bf16x8*)(lds + PG8_SB(b, h) + boff + n * 2048 + k * 1024); } while (0)
; #define PG8_MMA(ai, bj, At, Bt) do { __builtin_amdgcn_s_setprio(1); _Pragma("unroll") for (int m = 0; m < 4; ++m) _Pragma("unroll") for (int n = 0; n < 2; ++n) _Pragma("unroll") for (int k = 0; k < 2; ++k) \
;         acc[ai][bj][m][n] = __builtin_amdgcn_mfma_f32_16x16x32_bf16(Bt[n][k], At[m][k], acc[ai][bj][m][n], 0, 0, 0); __builtin_amdgcn_s_setprio(0); } while (0)
; #define PG8_WAIT_V(n) asm volatile("s_waitcnt vmcnt(" #n ")" ::: "memory")
; #define PG8_WAIT_L(n) asm volatile("s_waitcnt lgkmcnt(" #n ")" ::: "memory")
; #define PG8_BAR __builtin_amdgcn_s_barrier()
; #define PG8_SCHED __builtin_amdgcn_sched_barrier(0)
; #define PG8_STAGE(bufoff, gbase, voff) do { _Pragma("unroll") for (int _i = 0; _i < 2; ++_i) \
;         __builtin_amdgcn_global_load_lds((const unsigned*)((const char*)(gbase) + (voff)[_i]), (LAS unsigned*)(lds + (bufoff) + ldsw + _i * 8192), 16, 0, 0); } while (0)
; #define PG8_LDA(dst, b, h) do { _Pragma("unroll") for (int m = 0; m < 4; ++m) PG8_LD1(dst[m], PG8_SA(b, h) + aoff0 + m * 2048, PG8_SA(b, h) + aoff1 + m * 2048); } while (0)
; #define PG8_WAIT_V(n) asm volatile("s_waitcnt vmcnt(" #n ")" ::: "memory")
;     ...
;             PG8_LDB(B0, 0, 0); PG8_LDB(B1, 0, 1); PG8_SCHED; PG8_LDA(At, 0, 0); PG8_STAGE(PG8_SA(1, 1), a1 + hstepA, voffA);
;             PG8_WAIT_V(8); PG8_WAIT_L(0); PG8_BAR; PG8_MMA(0, 0, At, B0); PG8_MMA(0, 1, At, B1); PG8_BAR; PG8_SCHED;
;             PG8_LDA(At, 0, 1); PG8_STAGE(PG8_SB(0, 0), b2, voffB); PG8_STAGE(PG8_SB(0, 1), b2 + hstepB, voffB); PG8_STAGE(PG8_SA(0, 0), a2, voffA);
;             PG8_WAIT_V(8); PG8_WAIT_L(0); PG8_BAR; PG8_MMA(1, 0, At, B0); PG8_MMA(1, 1, At, B1); PG8_BAR; PG8_SCHED;
.LBB0_1409:
	ds_read_b128 v[14:17], v176
	ds_read_b64 v[18:19], v177
	ds_read_b128 v[20:23], v190
	ds_read_b64 v[24:25], v191
	ds_read_b128 v[2:5], v178
	ds_read_b64 v[6:7], v179
	ds_read_b128 v[8:11], v192
	ds_read_b64 v[12:13], v193
	s_add_u32 s46, s44, 0x100
	s_addc_u32 s47, s45, 0
	s_cmp_eq_u32 s80, 12
	s_cselect_b32 s51, s21, s47
	s_cselect_b32 s50, s73, s46
	s_cselect_b32 s49, s74, s79
	s_cselect_b32 s48, s75, s78
	ds_read_b64 v[212:213], v200
	ds_read_b64 v[172:173], v200 offset:2048
	ds_read_b64 v[218:219], v200 offset:4096
	ds_read_b64 v[206:207], v200 offset:6144
	v_lshl_add_u64 v[174:175], s[44:45], 0, v[164:165]
	s_add_i32 m0, s35, 0xc000
	ds_read_b128 v[208:211], v199
	ds_read_b128 v[168:171], v199 offset:2048
	ds_read_b128 v[214:217], v199 offset:4096
	ds_read_b128 v[202:205], v199 offset:6144
	global_load_lds_dwordx4 v[174:175], off
	v_lshl_add_u64 v[174:175], s[44:45], 0, v[166:167]
	s_add_i32 m0, s35, 0xe000
	s_nop 0
	global_load_lds_dwordx4 v[174:175], off
	s_waitcnt vmcnt(8)
	s_waitcnt lgkmcnt(0)
	s_barrier
	s_setprio 1
	v_mfma_f32_16x16x128_f8f6f4 v[150:153], v[14:19], v[208:213], v[150:153] cbsz:2 blgp:2
	v_mfma_f32_16x16x128_f8f6f4 v[142:145], v[20:25], v[208:213], v[142:145] cbsz:2 blgp:2
	v_mfma_f32_16x16x128_f8f6f4 v[134:137], v[14:19], v[168:173], v[134:137] cbsz:2 blgp:2
	v_mfma_f32_16x16x128_f8f6f4 v[126:129], v[20:25], v[168:173], v[126:129] cbsz:2 blgp:2
	v_mfma_f32_16x16x128_f8f6f4 v[118:121], v[14:19], v[214:219], v[118:121] cbsz:2 blgp:2
	v_mfma_f32_16x16x128_f8f6f4 v[110:113], v[20:25], v[214:219], v[110:113] cbsz:2 blgp:2
	v_mfma_f32_16x16x128_f8f6f4 v[102:105], v[14:19], v[202:207], v[102:105] cbsz:2 blgp:2
	v_mfma_f32_16x16x128_f8f6f4 v[94:97], v[20:25], v[202:207], v[94:97] cbsz:2 blgp:2
	s_setprio 0
	s_setprio 1
	v_mfma_f32_16x16x128_f8f6f4 v[146:149], v[2:7], v[208:213], v[146:149] cbsz:2 blgp:2
	v_mfma_f32_16x16x128_f8f6f4 v[138:141], v[8:13], v[208:213], v[138:141] cbsz:2 blgp:2
	v_mfma_f32_16x16x128_f8f6f4 v[130:133], v[2:7], v[168:173], v[130:133] cbsz:2 blgp:2
	v_mfma_f32_16x16x128_f8f6f4 v[122:125], v[8:13], v[168:173], v[122:125] cbsz:2 blgp:2
	v_mfma_f32_16x16x128_f8f6f4 v[114:117], v[2:7], v[214:219], v[114:117] cbsz:2 blgp:2
	v_mfma_f32_16x16x128_f8f6f4 v[106:109], v[8:13], v[214:219], v[106:109] cbsz:2 blgp:2
	v_mfma_f32_16x16x128_f8f6f4 v[98:101], v[2:7], v[202:207], v[98:101] cbsz:2 blgp:2
	v_mfma_f32_16x16x128_f8f6f4 v[86:89], v[8:13], v[202:207], v[86:89] cbsz:2 blgp:2
	s_setprio 0
	s_barrier
	ds_read_b64 v[218:219], v200 offset:16384
	ds_read_b64 v[206:207], v200 offset:18432
	ds_read_b64 v[224:225], v200 offset:20480
	ds_read_b64 v[212:213], v200 offset:22528
	s_mov_b32 m0, s43
	v_lshl_add_u64 v[168:169], s[48:49], 0, v[160:161]
	s_add_u32 s44, s48, 0x40000
	ds_read_b128 v[214:217], v199 offset:16384
	ds_read_b128 v[202:205], v199 offset:18432
	ds_read_b128 v[220:223], v199 offset:20480
	ds_read_b128 v[208:211], v199 offset:22528
	global_load_lds_dwordx4 v[168:169], off
	v_lshl_add_u64 v[170:171], s[48:49], 0, v[156:157]
	s_mov_b32 m0, s52
	s_addc_u32 s45, s49, 0
	global_load_lds_dwordx4 v[170:171], off
	v_lshl_add_u64 v[172:173], s[44:45], 0, v[160:161]
	s_mov_b32 m0, s53
	v_lshl_add_u64 v[174:175], s[50:51], 0, v[158:159]
	global_load_lds_dwordx4 v[172:173], off
	v_lshl_add_u64 v[172:173], s[44:45], 0, v[156:157]
	s_mov_b32 m0, s54
	s_nop 0
	global_load_lds_dwordx4 v[172:173], off
	v_lshl_add_u64 v[172:173], s[50:51], 0, v[162:163]
	s_mov_b32 m0, s35
	s_nop 0
	global_load_lds_dwordx4 v[172:173], off
	s_mov_b32 m0, s55
	s_nop 0
	global_load_lds_dwordx4 v[174:175], off
	s_waitcnt vmcnt(8)
	s_waitcnt lgkmcnt(0)
	s_barrier
	s_setprio 1
	v_mfma_f32_16x16x128_f8f6f4 v[78:81], v[14:19], v[214:219], v[78:81] cbsz:2 blgp:2
	v_mfma_f32_16x16x128_f8f6f4 v[70:73], v[20:25], v[214:219], v[70:73] cbsz:2 blgp:2
	v_mfma_f32_16x16x128_f8f6f4 v[58:61], v[14:19], v[202:207], v[58:61] cbsz:2 blgp:2
	v_mfma_f32_16x16x128_f8f6f4 v[50:53], v[20:25], v[202:207], v[50:53] cbsz:2 blgp:2
	v_mfma_f32_16x16x128_f8f6f4 v[42:45], v[14:19], v[220:225], v[42:45] cbsz:2 blgp:2
	v_mfma_f32_16x16x128_f8f6f4 v[34:37], v[20:25], v[220:225], v[34:37] cbsz:2 blgp:2
	v_mfma_f32_16x16x128_f8f6f4 v[30:33], v[14:19], v[208:213], v[30:33] cbsz:2 blgp:2
	v_mfma_f32_16x16x128_f8f6f4 v[26:29], v[20:25], v[208:213], v[26:29] cbsz:2 blgp:2
	s_setprio 0
	s_setprio 1
	v_mfma_f32_16x16x128_f8f6f4 v[90:93], v[2:7], v[214:219], v[90:93] cbsz:2 blgp:2
	v_mfma_f32_16x16x128_f8f6f4 v[82:85], v[8:13], v[214:219], v[82:85] cbsz:2 blgp:2
	v_mfma_f32_16x16x128_f8f6f4 v[74:77], v[2:7], v[202:207], v[74:77] cbsz:2 blgp:2
	v_mfma_f32_16x16x128_f8f6f4 v[66:69], v[8:13], v[202:207], v[66:69] cbsz:2 blgp:2
	v_mfma_f32_16x16x128_f8f6f4 v[62:65], v[2:7], v[220:225], v[62:65] cbsz:2 blgp:2
	v_mfma_f32_16x16x128_f8f6f4 v[54:57], v[8:13], v[220:225], v[54:57] cbsz:2 blgp:2
	v_mfma_f32_16x16x128_f8f6f4 v[46:49], v[2:7], v[208:213], v[46:49] cbsz:2 blgp:2
	v_mfma_f32_16x16x128_f8f6f4 v[38:41], v[8:13], v[208:213], v[38:41] cbsz:2 blgp:2
	s_setprio 0
	s_barrier
; #define PG8_STAGE(bufoff, gbase, voff) do { _Pragma("unroll") for (int _i = 0; _i < 2; ++_i) \
;         __builtin_amdgcn_global_load_lds((const unsigned*)((const char*)(gbase) + (voff)[_i]), (LAS unsigned*)(lds + (bufoff) + ldsw + _i * 8192), 16, 0, 0); } while (0)
; #define PG8_LDA(dst, b, h) do { _Pragma("unroll") for (int m = 0; m < 4; ++m) _Pragma("unroll") for (int k = 0; k < 2; ++k) dst[m][k] = *(const LAS bf16x8*)(lds + PG8_SA(b, h) + aoff + m * 2048 + k * 1024); } while (0)
; #define PG8_LDB(dst, b, h) do { _Pragma("unroll") for (int n = 0; n < 2; ++n) _Pragma("unroll") for (int k = 0; k < 2; ++k) dst[n][k] = *(const LAS bf16x8*)(lds + PG8_SB(b, h) + boff + n * 2048 + k * 1024); } while (0)
; #define PG8_MMA(ai, bj, At, Bt) do { __builtin_amdgcn_s_setprio(1); _Pragma("unroll") for (int m = 0; m < 4; ++m) _Pragma("unroll") for (int n = 0; n < 2; ++n) _Pragma("unroll") for (int k = 0; k < 2; ++k) \
;         acc[ai][bj][m][n] = __builtin_amdgcn_mfma_f32_16x16x32_bf16(Bt[n][k], At[m][k], acc[ai][bj][m][n], 0, 0, 0); __builtin_amdgcn_s_setprio(0); } while (0)
; #define PG8_WAIT_V(n) asm volatile("s_waitcnt vmcnt(" #n ")" ::: "memory")
; #define PG8_WAIT_L(n) asm volatile("s_waitcnt lgkmcnt(" #n ")" ::: "memory")
; #define PG8_BAR __builtin_amdgcn_s_barrier()
; #define PG8_SCHED __builtin_amdgcn_sched_barrier(0)
; #define PG8_STAGE(bufoff, gbase, voff) do { _Pragma("unroll") for (int _i = 0; _i < 2; ++_i) \
;         __builtin_amdgcn_global_load_lds((const unsigned*)((const char*)(gbase) + (voff)[_i]), (LAS unsigned*)(lds + (bufoff) + ldsw + _i * 8192), 16, 0, 0); } while (0)
; #define PG8_WAIT_V(n) asm volatile("s_waitcnt vmcnt(" #n ")" ::: "memory")
; #define PG8_WAIT_L(n) asm volatile("s_waitcnt lgkmcnt(" #n ")" ::: "memory")
;     ...
;             PG8_LDB(B0, 1, 0); PG8_LDB(B1, 1, 1); PG8_SCHED; PG8_LDA(At, 1, 0); PG8_STAGE(PG8_SA(0, 1), a2 + hstepA, voffA);
;             PG8_WAIT_V(8); PG8_WAIT_L(0); PG8_BAR; PG8_MMA(0, 0, At, B0); PG8_MMA(0, 1, At, B1); PG8_BAR; PG8_SCHED;
;             PG8_LDA(At, 1, 1); PG8_STAGE(PG8_SB(1, 0), b3, voffB); PG8_STAGE(PG8_SB(1, 1), b3 + hstepB, voffB); PG8_STAGE(PG8_SA(1, 0), a3, voffA);
;             PG8_WAIT_V(8); PG8_WAIT_L(0); PG8_BAR; PG8_MMA(1, 0, At, B0); PG8_MMA(1, 1, At, B1); PG8_BAR; PG8_SCHED;
;         }
;         asm volatile("s_nop 15\n\ts_nop 15" ::: "memory");
;         if (wr == 0) PG8_BAR;
	ds_read_b128 v[2:5], v180
	ds_read_b64 v[6:7], v181
	ds_read_b128 v[8:11], v194
	ds_read_b64 v[12:13], v195
	ds_read_b128 v[14:17], v182
	ds_read_b64 v[18:19], v183
	ds_read_b128 v[20:23], v196
	ds_read_b64 v[24:25], v197
	ds_read_b64 v[218:219], v200 offset:32768
	ds_read_b64 v[206:207], v200 offset:34816
	ds_read_b64 v[224:225], v200 offset:36864
	ds_read_b64 v[212:213], v200 offset:38912
	s_add_u32 s44, s50, 0x40000
	s_addc_u32 s45, s51, 0
	s_mov_b32 m0, s56
	v_lshl_add_u64 v[226:227], s[44:45], 0, v[162:163]
	ds_read_b128 v[214:217], v199 offset:32768
	ds_read_b128 v[202:205], v199 offset:34816
	ds_read_b128 v[220:223], v199 offset:36864
	ds_read_b128 v[208:211], v199 offset:38912
	global_load_lds_dwordx4 v[226:227], off
	v_lshl_add_u64 v[226:227], s[44:45], 0, v[158:159]
	s_mov_b32 m0, s57
	s_nop 0
	global_load_lds_dwordx4 v[226:227], off
	s_waitcnt vmcnt(8)
	s_waitcnt lgkmcnt(0)
	s_barrier
	s_setprio 1
	v_mfma_f32_16x16x128_f8f6f4 v[150:153], v[2:7], v[214:219], v[150:153] cbsz:2 blgp:2
	v_mfma_f32_16x16x128_f8f6f4 v[142:145], v[8:13], v[214:219], v[142:145] cbsz:2 blgp:2
	v_mfma_f32_16x16x128_f8f6f4 v[134:137], v[2:7], v[202:207], v[134:137] cbsz:2 blgp:2
	v_mfma_f32_16x16x128_f8f6f4 v[126:129], v[8:13], v[202:207], v[126:129] cbsz:2 blgp:2
	v_mfma_f32_16x16x128_f8f6f4 v[118:121], v[2:7], v[220:225], v[118:121] cbsz:2 blgp:2
	v_mfma_f32_16x16x128_f8f6f4 v[110:113], v[8:13], v[220:225], v[110:113] cbsz:2 blgp:2
	v_mfma_f32_16x16x128_f8f6f4 v[102:105], v[2:7], v[208:213], v[102:105] cbsz:2 blgp:2
	v_mfma_f32_16x16x128_f8f6f4 v[94:97], v[8:13], v[208:213], v[94:97] cbsz:2 blgp:2
	s_setprio 0
	s_setprio 1
	v_mfma_f32_16x16x128_f8f6f4 v[146:149], v[14:19], v[214:219], v[146:149] cbsz:2 blgp:2
	v_mfma_f32_16x16x128_f8f6f4 v[138:141], v[20:25], v[214:219], v[138:141] cbsz:2 blgp:2
	v_mfma_f32_16x16x128_f8f6f4 v[130:133], v[14:19], v[202:207], v[130:133] cbsz:2 blgp:2
	v_mfma_f32_16x16x128_f8f6f4 v[122:125], v[20:25], v[202:207], v[122:125] cbsz:2 blgp:2
	v_mfma_f32_16x16x128_f8f6f4 v[114:117], v[14:19], v[220:225], v[114:117] cbsz:2 blgp:2
	v_mfma_f32_16x16x128_f8f6f4 v[106:109], v[20:25], v[220:225], v[106:109] cbsz:2 blgp:2
	v_mfma_f32_16x16x128_f8f6f4 v[98:101], v[14:19], v[208:213], v[98:101] cbsz:2 blgp:2
	v_mfma_f32_16x16x128_f8f6f4 v[86:89], v[20:25], v[208:213], v[86:89] cbsz:2 blgp:2
	s_setprio 0
	s_barrier
	ds_read_b64 v[218:219], v200 offset:49152
	ds_read_b64 v[206:207], v200 offset:51200
	ds_read_b64 v[224:225], v200 offset:53248
	ds_read_b64 v[212:213], v200 offset:55296
	s_mov_b32 m0, s58
	v_lshl_add_u64 v[168:169], v[168:169], 0, s[16:17]
	s_add_u32 s44, s48, 0x40080
	ds_read_b128 v[214:217], v199 offset:49152
	ds_read_b128 v[202:205], v199 offset:51200
	ds_read_b128 v[220:223], v199 offset:53248
	ds_read_b128 v[208:211], v199 offset:55296
	global_load_lds_dwordx4 v[168:169], off
	v_lshl_add_u64 v[168:169], v[170:171], 0, s[16:17]
	s_mov_b32 m0, s59
	s_addc_u32 s45, s49, 0
	global_load_lds_dwordx4 v[168:169], off
	v_lshl_add_u64 v[168:169], s[44:45], 0, v[160:161]
	s_mov_b32 m0, s62
	s_nop 0
	global_load_lds_dwordx4 v[168:169], off
	v_lshl_add_u64 v[168:169], s[44:45], 0, v[156:157]
	s_mov_b32 m0, s63
	s_nop 0
	global_load_lds_dwordx4 v[168:169], off
	v_lshl_add_u64 v[168:169], v[172:173], 0, s[16:17]
	s_mov_b32 m0, s60
	s_nop 0
	global_load_lds_dwordx4 v[168:169], off
	v_lshl_add_u64 v[168:169], v[174:175], 0, s[16:17]
	s_mov_b32 m0, s61
	s_nop 0
	global_load_lds_dwordx4 v[168:169], off
	s_waitcnt vmcnt(8)
	s_waitcnt lgkmcnt(0)
	s_barrier
	s_setprio 1
	v_mfma_f32_16x16x128_f8f6f4 v[78:81], v[2:7], v[214:219], v[78:81] cbsz:2 blgp:2
	v_mfma_f32_16x16x128_f8f6f4 v[70:73], v[8:13], v[214:219], v[70:73] cbsz:2 blgp:2
	v_mfma_f32_16x16x128_f8f6f4 v[58:61], v[2:7], v[202:207], v[58:61] cbsz:2 blgp:2
	v_mfma_f32_16x16x128_f8f6f4 v[50:53], v[8:13], v[202:207], v[50:53] cbsz:2 blgp:2
	v_mfma_f32_16x16x128_f8f6f4 v[42:45], v[2:7], v[220:225], v[42:45] cbsz:2 blgp:2
	v_mfma_f32_16x16x128_f8f6f4 v[34:37], v[8:13], v[220:225], v[34:37] cbsz:2 blgp:2
	v_mfma_f32_16x16x128_f8f6f4 v[30:33], v[2:7], v[208:213], v[30:33] cbsz:2 blgp:2
	v_mfma_f32_16x16x128_f8f6f4 v[26:29], v[8:13], v[208:213], v[26:29] cbsz:2 blgp:2
	s_setprio 0
	s_setprio 1
	v_mfma_f32_16x16x128_f8f6f4 v[90:93], v[14:19], v[214:219], v[90:93] cbsz:2 blgp:2
	v_mfma_f32_16x16x128_f8f6f4 v[82:85], v[20:25], v[214:219], v[82:85] cbsz:2 blgp:2
	v_mfma_f32_16x16x128_f8f6f4 v[74:77], v[14:19], v[202:207], v[74:77] cbsz:2 blgp:2
	v_mfma_f32_16x16x128_f8f6f4 v[66:69], v[20:25], v[202:207], v[66:69] cbsz:2 blgp:2
	s_add_i32 s80, s80, 2
	s_add_u32 s78, s78, 0x100
	s_addc_u32 s79, s79, 0
	s_cmp_gt_u32 s80, 13
	s_mov_b64 s[44:45], s[46:47]
	v_mfma_f32_16x16x128_f8f6f4 v[62:65], v[14:19], v[220:225], v[62:65] cbsz:2 blgp:2
	v_mfma_f32_16x16x128_f8f6f4 v[54:57], v[20:25], v[220:225], v[54:57] cbsz:2 blgp:2
	v_mfma_f32_16x16x128_f8f6f4 v[46:49], v[14:19], v[208:213], v[46:49] cbsz:2 blgp:2
	v_mfma_f32_16x16x128_f8f6f4 v[38:41], v[20:25], v[208:213], v[38:41] cbsz:2 blgp:2
	s_setprio 0
	s_barrier
	s_cbranch_scc0 .LBB0_1409
	s_nop 15
	s_nop 15
	s_and_b64 vcc, exec, s[18:19]
	s_cbranch_vccz .LBB0_1412
	s_barrier

; #define PG8_STAGE(bufoff, gbase, voff) do { _Pragma("unroll") for (int _i = 0; _i < 2; ++_i) \
;         __builtin_amdgcn_global_load_lds((const unsigned*)((const char*)(gbase) + (voff)[_i]), (LAS unsigned*)(lds + (bufoff) + ldsw + _i * 8192), 16, 0, 0); } while (0)
; #define PG8_LDA(dst, b, h) do { _Pragma("unroll") for (int m = 0; m < 4; ++m) _Pragma("unroll") for (int k = 0; k < 2; ++k) dst[m][k] = *(const LAS bf16x8*)(lds + PG8_SA(b, h) + aoff + m * 2048 + k * 1024); } while (0)
; #define PG8_LDB(dst, b, h) do { _Pragma("unroll") for (int n = 0; n < 2; ++n) _Pragma("unroll") for (int k = 0; k < 2; ++k) dst[n][k] = *(const LAS bf16x8*)(lds + PG8_SB(b, h) + boff + n * 2048 + k * 1024); } while (0)
; #define PG8_MMA(ai, bj, At, Bt) do { __builtin_amdgcn_s_setprio(1); _Pragma("unroll") for (int m = 0; m < 4; ++m) _Pragma("unroll") for (int n = 0; n < 2; ++n) _Pragma("unroll") for (int k = 0; k < 2; ++k) \
;         acc[ai][bj][m][n] = __builtin_amdgcn_mfma_f32_16x16x32_bf16(Bt[n][k], At[m][k], acc[ai][bj][m][n], 0, 0, 0); __builtin_amdgcn_s_setprio(0); } while (0)
; #define PG8_WAIT_V(n) asm volatile("s_waitcnt vmcnt(" #n ")" ::: "memory")
; #define PG8_WAIT_L(n) asm volatile("s_waitcnt lgkmcnt(" #n ")" ::: "memory")
; #define PG8_BAR __builtin_amdgcn_s_barrier()
; #define PG8_SCHED __builtin_amdgcn_sched_barrier(0)
; #define PG8_STAGE(bufoff, gbase, voff) do { _Pragma("unroll") for (int _i = 0; _i < 2; ++_i) \
;         __builtin_amdgcn_global_load_lds((const unsigned*)((const char*)(gbase) + (voff)[_i]), (LAS unsigned*)(lds + (bufoff) + ldsw + _i * 8192), 16, 0, 0); } while (0)
; #define PG8_LDA(dst, b, h) do { _Pragma("unroll") for (int m = 0; m < 4; ++m) PG8_LD1(dst[m], PG8_SA(b, h) + aoff0 + m * 2048, PG8_SA(b, h) + aoff1 + m * 2048); } while (0)
; #define PG8_WAIT_V(n) asm volatile("s_waitcnt vmcnt(" #n ")" ::: "memory")
;     ...
;             PG8_LDB(B0, 0, 0); PG8_LDB(B1, 0, 1); PG8_SCHED; PG8_LDA(At, 0, 0); PG8_STAGE(PG8_SA(1, 1), a1 + hstepA, voffA);
;             PG8_WAIT_V(8); PG8_WAIT_L(0); PG8_BAR; PG8_MMA(0, 0, At, B0); PG8_MMA(0, 1, At, B1); PG8_BAR; PG8_SCHED;
;             PG8_LDA(At, 0, 1); PG8_STAGE(PG8_SB(0, 0), b2, voffB); PG8_STAGE(PG8_SB(0, 1), b2 + hstepB, voffB); PG8_STAGE(PG8_SA(0, 0), a2, voffA);
;             PG8_WAIT_V(8); PG8_WAIT_L(0); PG8_BAR; PG8_MMA(1, 0, At, B0); PG8_MMA(1, 1, At, B1); PG8_BAR; PG8_SCHED;
.LBB0_1480:
	ds_read_b128 v[18:21], v190
	ds_read_b128 v[22:25], v191
	ds_read_b128 v[26:29], v198
	ds_read_b128 v[30:33], v199
	ds_read_b128 v[2:5], v192
	ds_read_b128 v[6:9], v193
	ds_read_b128 v[10:13], v200
	ds_read_b128 v[14:17], v201
	s_add_u32 s48, s46, 0x100
	s_addc_u32 s49, s47, 0
	s_cmp_eq_u32 s86, 52
	s_cselect_b32 s53, s80, s49
	s_cselect_b32 s52, s81, s48
	s_cselect_b32 s51, s82, s85
	s_cselect_b32 s50, s83, s84
	v_lshl_add_u64 v[234:235], s[46:47], 0, v[170:171]
	s_add_i32 m0, s0, 0xc000
	ds_read_b128 v[176:179], v207
	ds_read_b128 v[210:213], v207 offset:2048
	ds_read_b128 v[180:183], v208
	ds_read_b128 v[214:217], v208 offset:2048
	ds_read_b128 v[218:221], v207 offset:4096
	ds_read_b128 v[226:229], v207 offset:6144
	ds_read_b128 v[222:225], v208 offset:4096
	ds_read_b128 v[230:233], v208 offset:6144
	global_load_lds_dwordx4 v[234:235], off
	v_lshl_add_u64 v[234:235], s[46:47], 0, v[172:173]
	s_add_i32 m0, s0, 0xe000
	s_nop 0
	global_load_lds_dwordx4 v[234:235], off
	s_waitcnt vmcnt(8)
	s_waitcnt lgkmcnt(0)
	s_barrier
	s_setprio 1
	v_mfma_f32_16x16x128_f8f6f4 v[158:161], v[18:25], v[176:183], v[158:161]
	v_mfma_f32_16x16x128_f8f6f4 v[154:157], v[26:33], v[176:183], v[154:157]
	v_mfma_f32_16x16x128_f8f6f4 v[146:149], v[18:25], v[210:217], v[146:149]
	v_mfma_f32_16x16x128_f8f6f4 v[138:141], v[26:33], v[210:217], v[138:141]
	v_mfma_f32_16x16x128_f8f6f4 v[130:133], v[18:25], v[218:225], v[130:133]
	v_mfma_f32_16x16x128_f8f6f4 v[122:125], v[26:33], v[218:225], v[122:125]
	v_mfma_f32_16x16x128_f8f6f4 v[114:117], v[18:25], v[226:233], v[114:117]
	v_mfma_f32_16x16x128_f8f6f4 v[106:109], v[26:33], v[226:233], v[106:109]
	s_setprio 0
	s_setprio 1
	v_mfma_f32_16x16x128_f8f6f4 v[150:153], v[2:9], v[176:183], v[150:153]
	v_mfma_f32_16x16x128_f8f6f4 v[142:145], v[10:17], v[176:183], v[142:145]
	v_mfma_f32_16x16x128_f8f6f4 v[134:137], v[2:9], v[210:217], v[134:137]
	v_mfma_f32_16x16x128_f8f6f4 v[126:129], v[10:17], v[210:217], v[126:129]
	v_mfma_f32_16x16x128_f8f6f4 v[118:121], v[2:9], v[218:225], v[118:121]
	v_mfma_f32_16x16x128_f8f6f4 v[110:113], v[10:17], v[218:225], v[110:113]
	v_mfma_f32_16x16x128_f8f6f4 v[102:105], v[2:9], v[226:233], v[102:105]
	v_mfma_f32_16x16x128_f8f6f4 v[98:101], v[10:17], v[226:233], v[98:101]
	s_setprio 0
	s_barrier
	s_mov_b32 m0, s1
	v_lshl_add_u64 v[176:177], s[50:51], 0, v[166:167]
	s_add_u32 s46, s50, 0xe0000
	ds_read_b128 v[210:213], v207 offset:16384
	ds_read_b128 v[218:221], v207 offset:18432
	ds_read_b128 v[214:217], v208 offset:16384
	ds_read_b128 v[222:225], v208 offset:18432
	ds_read_b128 v[226:229], v207 offset:20480
	ds_read_b128 v[234:237], v207 offset:22528
	ds_read_b128 v[230:233], v208 offset:20480
	ds_read_b128 v[238:241], v208 offset:22528
	global_load_lds_dwordx4 v[176:177], off
	v_lshl_add_u64 v[178:179], s[50:51], 0, v[162:163]
	s_mov_b32 m0, s33
	s_addc_u32 s47, s51, 0
	global_load_lds_dwordx4 v[178:179], off
	v_lshl_add_u64 v[180:181], s[46:47], 0, v[166:167]
	s_mov_b32 m0, s35
	v_lshl_add_u64 v[182:183], s[52:53], 0, v[164:165]
	global_load_lds_dwordx4 v[180:181], off
	v_lshl_add_u64 v[180:181], s[46:47], 0, v[162:163]
	s_mov_b32 m0, s54
	s_nop 0
	global_load_lds_dwordx4 v[180:181], off
	v_lshl_add_u64 v[180:181], s[52:53], 0, v[168:169]
	s_mov_b32 m0, s0
	s_nop 0
	global_load_lds_dwordx4 v[180:181], off
	s_mov_b32 m0, s55
	s_nop 0
	global_load_lds_dwordx4 v[182:183], off
	s_waitcnt vmcnt(8)
	s_waitcnt lgkmcnt(0)
	s_barrier
	s_setprio 1
	v_mfma_f32_16x16x128_f8f6f4 v[94:97], v[18:25], v[210:217], v[94:97]
	v_mfma_f32_16x16x128_f8f6f4 v[90:93], v[26:33], v[210:217], v[90:93]
	v_mfma_f32_16x16x128_f8f6f4 v[82:85], v[18:25], v[218:225], v[82:85]
	v_mfma_f32_16x16x128_f8f6f4 v[74:77], v[26:33], v[218:225], v[74:77]
	v_mfma_f32_16x16x128_f8f6f4 v[66:69], v[18:25], v[226:233], v[66:69]
	v_mfma_f32_16x16x128_f8f6f4 v[58:61], v[26:33], v[226:233], v[58:61]
	v_mfma_f32_16x16x128_f8f6f4 v[50:53], v[18:25], v[234:241], v[50:53]
	v_mfma_f32_16x16x128_f8f6f4 v[42:45], v[26:33], v[234:241], v[42:45]
	s_setprio 0
	s_setprio 1
	v_mfma_f32_16x16x128_f8f6f4 v[86:89], v[2:9], v[210:217], v[86:89]
	v_mfma_f32_16x16x128_f8f6f4 v[78:81], v[10:17], v[210:217], v[78:81]
	v_mfma_f32_16x16x128_f8f6f4 v[70:73], v[2:9], v[218:225], v[70:73]
	v_mfma_f32_16x16x128_f8f6f4 v[62:65], v[10:17], v[218:225], v[62:65]
	v_mfma_f32_16x16x128_f8f6f4 v[54:57], v[2:9], v[226:233], v[54:57]
	v_mfma_f32_16x16x128_f8f6f4 v[46:49], v[10:17], v[226:233], v[46:49]
	v_mfma_f32_16x16x128_f8f6f4 v[38:41], v[2:9], v[234:241], v[38:41]
	v_mfma_f32_16x16x128_f8f6f4 v[34:37], v[10:17], v[234:241], v[34:37]
	s_setprio 0
	s_barrier
; #define PG8_STAGE(bufoff, gbase, voff) do { _Pragma("unroll") for (int _i = 0; _i < 2; ++_i) \
;         __builtin_amdgcn_global_load_lds((const unsigned*)((const char*)(gbase) + (voff)[_i]), (LAS unsigned*)(lds + (bufoff) + ldsw + _i * 8192), 16, 0, 0); } while (0)
; #define PG8_LDA(dst, b, h) do { _Pragma("unroll") for (int m = 0; m < 4; ++m) _Pragma("unroll") for (int k = 0; k < 2; ++k) dst[m][k] = *(const LAS bf16x8*)(lds + PG8_SA(b, h) + aoff + m * 2048 + k * 1024); } while (0)
; #define PG8_LDB(dst, b, h) do { _Pragma("unroll") for (int n = 0; n < 2; ++n) _Pragma("unroll") for (int k = 0; k < 2; ++k) dst[n][k] = *(const LAS bf16x8*)(lds + PG8_SB(b, h) + boff + n * 2048 + k * 1024); } while (0)
; #define PG8_MMA(ai, bj, At, Bt) do { __builtin_amdgcn_s_setprio(1); _Pragma("unroll") for (int m = 0; m < 4; ++m) _Pragma("unroll") for (int n = 0; n < 2; ++n) _Pragma("unroll") for (int k = 0; k < 2; ++k) \
;         acc[ai][bj][m][n] = __builtin_amdgcn_mfma_f32_16x16x32_bf16(Bt[n][k], At[m][k], acc[ai][bj][m][n], 0, 0, 0); __builtin_amdgcn_s_setprio(0); } while (0)
; #define PG8_WAIT_V(n) asm volatile("s_waitcnt vmcnt(" #n ")" ::: "memory")
; #define PG8_WAIT_L(n) asm volatile("s_waitcnt lgkmcnt(" #n ")" ::: "memory")
; #define PG8_BAR __builtin_amdgcn_s_barrier()
; #define PG8_SCHED __builtin_amdgcn_sched_barrier(0)
; #define PG8_STAGE(bufoff, gbase, voff) do { _Pragma("unroll") for (int _i = 0; _i < 2; ++_i) \
;         __builtin_amdgcn_global_load_lds((const unsigned*)((const char*)(gbase) + (voff)[_i]), (LAS unsigned*)(lds + (bufoff) + ldsw + _i * 8192), 16, 0, 0); } while (0)
; #define PG8_WAIT_V(n) asm volatile("s_waitcnt vmcnt(" #n ")" ::: "memory")
; #define PG8_WAIT_L(n) asm volatile("s_waitcnt lgkmcnt(" #n ")" ::: "memory")
;     ...
;             PG8_LDB(B0, 1, 0); PG8_LDB(B1, 1, 1); PG8_SCHED; PG8_LDA(At, 1, 0); PG8_STAGE(PG8_SA(0, 1), a2 + hstepA, voffA);
;             PG8_WAIT_V(8); PG8_WAIT_L(0); PG8_BAR; PG8_MMA(0, 0, At, B0); PG8_MMA(0, 1, At, B1); PG8_BAR; PG8_SCHED;
;             PG8_LDA(At, 1, 1); PG8_STAGE(PG8_SB(1, 0), b3, voffB); PG8_STAGE(PG8_SB(1, 1), b3 + hstepB, voffB); PG8_STAGE(PG8_SA(1, 0), a3, voffA);
;             PG8_WAIT_V(8); PG8_WAIT_L(0); PG8_BAR; PG8_MMA(1, 0, At, B0); PG8_MMA(1, 1, At, B1); PG8_BAR; PG8_SCHED;
;         }
;         asm volatile("s_nop 15\n\ts_nop 15" ::: "memory");
;         if (wr == 0) PG8_BAR;
	ds_read_b128 v[2:5], v194
	ds_read_b128 v[6:9], v195
	ds_read_b128 v[10:13], v202
	ds_read_b128 v[14:17], v203
	ds_read_b128 v[18:21], v196
	ds_read_b128 v[22:25], v197
	ds_read_b128 v[26:29], v204
	ds_read_b128 v[30:33], v205
	s_add_u32 s46, s52, 0xe0000
	s_addc_u32 s47, s53, 0
	s_mov_b32 m0, s56
	v_lshl_add_u64 v[242:243], s[46:47], 0, v[168:169]
	ds_read_b128 v[210:213], v207 offset:32768
	ds_read_b128 v[218:221], v207 offset:34816
	ds_read_b128 v[214:217], v208 offset:32768
	ds_read_b128 v[222:225], v208 offset:34816
	ds_read_b128 v[226:229], v207 offset:36864
	ds_read_b128 v[234:237], v207 offset:38912
	ds_read_b128 v[230:233], v208 offset:36864
	ds_read_b128 v[238:241], v208 offset:38912
	global_load_lds_dwordx4 v[242:243], off
	v_lshl_add_u64 v[242:243], s[46:47], 0, v[164:165]
	s_mov_b32 m0, s57
	s_nop 0
	global_load_lds_dwordx4 v[242:243], off
	s_waitcnt vmcnt(8)
	s_waitcnt lgkmcnt(0)
	s_barrier
	s_setprio 1
	v_mfma_f32_16x16x128_f8f6f4 v[158:161], v[2:9], v[210:217], v[158:161]
	v_mfma_f32_16x16x128_f8f6f4 v[154:157], v[10:17], v[210:217], v[154:157]
	v_mfma_f32_16x16x128_f8f6f4 v[146:149], v[2:9], v[218:225], v[146:149]
	v_mfma_f32_16x16x128_f8f6f4 v[138:141], v[10:17], v[218:225], v[138:141]
	v_mfma_f32_16x16x128_f8f6f4 v[130:133], v[2:9], v[226:233], v[130:133]
	v_mfma_f32_16x16x128_f8f6f4 v[122:125], v[10:17], v[226:233], v[122:125]
	v_mfma_f32_16x16x128_f8f6f4 v[114:117], v[2:9], v[234:241], v[114:117]
	v_mfma_f32_16x16x128_f8f6f4 v[106:109], v[10:17], v[234:241], v[106:109]
	s_setprio 0
	s_setprio 1
	v_mfma_f32_16x16x128_f8f6f4 v[150:153], v[18:25], v[210:217], v[150:153]
	v_mfma_f32_16x16x128_f8f6f4 v[142:145], v[26:33], v[210:217], v[142:145]
	v_mfma_f32_16x16x128_f8f6f4 v[134:137], v[18:25], v[218:225], v[134:137]
	v_mfma_f32_16x16x128_f8f6f4 v[126:129], v[26:33], v[218:225], v[126:129]
	v_mfma_f32_16x16x128_f8f6f4 v[118:121], v[18:25], v[226:233], v[118:121]
	v_mfma_f32_16x16x128_f8f6f4 v[110:113], v[26:33], v[226:233], v[110:113]
	v_mfma_f32_16x16x128_f8f6f4 v[102:105], v[18:25], v[234:241], v[102:105]
	v_mfma_f32_16x16x128_f8f6f4 v[98:101], v[26:33], v[234:241], v[98:101]
	s_setprio 0
	s_barrier
	s_mov_b32 m0, s58
	v_lshl_add_u64 v[176:177], v[176:177], 0, s[14:15]
	s_add_u32 s46, s50, 0xe0080
	ds_read_b128 v[210:213], v207 offset:49152
	ds_read_b128 v[218:221], v207 offset:51200
	ds_read_b128 v[214:217], v208 offset:49152
	ds_read_b128 v[222:225], v208 offset:51200
	ds_read_b128 v[226:229], v207 offset:53248
	ds_read_b128 v[234:237], v207 offset:55296
	ds_read_b128 v[230:233], v208 offset:53248
	ds_read_b128 v[238:241], v208 offset:55296
	global_load_lds_dwordx4 v[176:177], off
	v_lshl_add_u64 v[176:177], v[178:179], 0, s[14:15]
	s_mov_b32 m0, s59
	s_addc_u32 s47, s51, 0
	global_load_lds_dwordx4 v[176:177], off
	v_lshl_add_u64 v[176:177], s[46:47], 0, v[166:167]
	s_mov_b32 m0, s62
	s_nop 0
	global_load_lds_dwordx4 v[176:177], off
	v_lshl_add_u64 v[176:177], s[46:47], 0, v[162:163]
	s_mov_b32 m0, s63
	s_nop 0
	global_load_lds_dwordx4 v[176:177], off
	v_lshl_add_u64 v[176:177], v[180:181], 0, s[14:15]
	s_mov_b32 m0, s60
	s_nop 0
	global_load_lds_dwordx4 v[176:177], off
	v_lshl_add_u64 v[176:177], v[182:183], 0, s[14:15]
	s_mov_b32 m0, s61
	s_nop 0
	global_load_lds_dwordx4 v[176:177], off
	s_waitcnt vmcnt(8)
	s_waitcnt lgkmcnt(0)
	s_barrier
	s_setprio 1
	v_mfma_f32_16x16x128_f8f6f4 v[94:97], v[2:9], v[210:217], v[94:97]
	v_mfma_f32_16x16x128_f8f6f4 v[90:93], v[10:17], v[210:217], v[90:93]
	v_mfma_f32_16x16x128_f8f6f4 v[82:85], v[2:9], v[218:225], v[82:85]
	v_mfma_f32_16x16x128_f8f6f4 v[74:77], v[10:17], v[218:225], v[74:77]
	v_mfma_f32_16x16x128_f8f6f4 v[66:69], v[2:9], v[226:233], v[66:69]
	v_mfma_f32_16x16x128_f8f6f4 v[58:61], v[10:17], v[226:233], v[58:61]
	v_mfma_f32_16x16x128_f8f6f4 v[50:53], v[2:9], v[234:241], v[50:53]
	v_mfma_f32_16x16x128_f8f6f4 v[42:45], v[10:17], v[234:241], v[42:45]
	s_setprio 0
	s_setprio 1
	v_mfma_f32_16x16x128_f8f6f4 v[86:89], v[18:25], v[210:217], v[86:89]
	v_mfma_f32_16x16x128_f8f6f4 v[78:81], v[26:33], v[210:217], v[78:81]
	v_mfma_f32_16x16x128_f8f6f4 v[70:73], v[18:25], v[218:225], v[70:73]
	v_mfma_f32_16x16x128_f8f6f4 v[62:65], v[26:33], v[218:225], v[62:65]
	s_add_i32 s86, s86, 2
	s_add_u32 s84, s84, 0x100
	s_addc_u32 s85, s85, 0
	s_cmp_gt_u32 s86, 53
	s_mov_b64 s[46:47], s[48:49]
	v_mfma_f32_16x16x128_f8f6f4 v[54:57], v[18:25], v[226:233], v[54:57]
	v_mfma_f32_16x16x128_f8f6f4 v[46:49], v[26:33], v[226:233], v[46:49]
	v_mfma_f32_16x16x128_f8f6f4 v[38:41], v[18:25], v[234:241], v[38:41]
	v_mfma_f32_16x16x128_f8f6f4 v[34:37], v[26:33], v[234:241], v[34:37]
	s_setprio 0
	s_barrier
	s_cbranch_scc0 .LBB0_1480
	s_nop 15
	s_nop 15
	s_and_b64 vcc, exec, s[16:17]
	s_cbranch_vccz .LBB0_1483
	s_barrier

; #define PG8_STAGE(bufoff, gbase, voff) do { _Pragma("unroll") for (int _i = 0; _i < 2; ++_i) \
;         __builtin_amdgcn_global_load_lds((const unsigned*)((const char*)(gbase) + (voff)[_i]), (LAS unsigned*)(lds + (bufoff) + ldsw + _i * 8192), 16, 0, 0); } while (0)
; #define PG8_LDA(dst, b, h) do { _Pragma("unroll") for (int m = 0; m < 4; ++m) _Pragma("unroll") for (int k = 0; k < 2; ++k) dst[m][k] = *(const LAS bf16x8*)(lds + PG8_SA(b, h) + aoff + m * 2048 + k * 1024); } while (0)
; #define PG8_LDB(dst, b, h) do { _Pragma("unroll") for (int n = 0; n < 2; ++n) _Pragma("unroll") for (int k = 0; k < 2; ++k) dst[n][k] = *(const LAS bf16x8*)(lds + PG8_SB(b, h) + boff + n * 2048 + k * 1024); } while (0)
; #define PG8_MMA(ai, bj, At, Bt) do { __builtin_amdgcn_s_setprio(1); _Pragma("unroll") for (int m = 0; m < 4; ++m) _Pragma("unroll") for (int n = 0; n < 2; ++n) _Pragma("unroll") for (int k = 0; k < 2; ++k) \
;         acc[ai][bj][m][n] = __builtin_amdgcn_mfma_f32_16x16x32_bf16(Bt[n][k], At[m][k], acc[ai][bj][m][n], 0, 0, 0); __builtin_amdgcn_s_setprio(0); } while (0)
; #define PG8_WAIT_V(n) asm volatile("s_waitcnt vmcnt(" #n ")" ::: "memory")
; #define PG8_WAIT_L(n) asm volatile("s_waitcnt lgkmcnt(" #n ")" ::: "memory")
; #define PG8_BAR __builtin_amdgcn_s_barrier()
; #define PG8_SCHED __builtin_amdgcn_sched_barrier(0)
; #define PG8_STAGE(bufoff, gbase, voff) do { _Pragma("unroll") for (int _i = 0; _i < 2; ++_i) \
;         __builtin_amdgcn_global_load_lds((const unsigned*)((const char*)(gbase) + (voff)[_i]), (LAS unsigned*)(lds + (bufoff) + ldsw + _i * 8192), 16, 0, 0); } while (0)
; #define PG8_LDA(dst, b, h) do { _Pragma("unroll") for (int m = 0; m < 4; ++m) PG8_LD1(dst[m], PG8_SA(b, h) + aoff0 + m * 2048, PG8_SA(b, h) + aoff1 + m * 2048); } while (0)
; #define PG8_WAIT_V(n) asm volatile("s_waitcnt vmcnt(" #n ")" ::: "memory")
;     ...
;             PG8_LDB(B0, 0, 0); PG8_LDB(B1, 0, 1); PG8_SCHED; PG8_LDA(At, 0, 0); PG8_STAGE(PG8_SA(1, 1), a1 + hstepA, voffA);
;             PG8_WAIT_V(8); PG8_WAIT_L(0); PG8_BAR; PG8_MMA(0, 0, At, B0); PG8_MMA(0, 1, At, B1); PG8_BAR; PG8_SCHED;
;             PG8_LDA(At, 0, 1); PG8_STAGE(PG8_SB(0, 0), b2, voffB); PG8_STAGE(PG8_SB(0, 1), b2 + hstepB, voffB); PG8_STAGE(PG8_SA(0, 0), a2, voffA);
;             PG8_WAIT_V(8); PG8_WAIT_L(0); PG8_BAR; PG8_MMA(1, 0, At, B0); PG8_MMA(1, 1, At, B1); PG8_BAR; PG8_SCHED;
.LBB0_1497:
	ds_read_b128 v[18:21], v190
	ds_read_b128 v[22:25], v191
	ds_read_b128 v[26:29], v198
	ds_read_b128 v[30:33], v199
	ds_read_b128 v[2:5], v192
	ds_read_b128 v[6:9], v193
	ds_read_b128 v[10:13], v200
	ds_read_b128 v[14:17], v201
	s_add_u32 s48, s46, 0x100
	s_addc_u32 s49, s47, 0
	s_cmp_eq_u32 s88, 10
	s_cselect_b32 s53, s82, s49
	s_cselect_b32 s52, s83, s48
	s_cselect_b32 s51, s84, s87
	s_cselect_b32 s50, s85, s86
	v_lshl_add_u64 v[234:235], s[46:47], 0, v[172:173]
	s_add_i32 m0, s25, 0xc000
	ds_read_b128 v[176:179], v207
	ds_read_b128 v[210:213], v207 offset:2048
	ds_read_b128 v[180:183], v208
	ds_read_b128 v[214:217], v208 offset:2048
	ds_read_b128 v[218:221], v207 offset:4096
	ds_read_b128 v[226:229], v207 offset:6144
	ds_read_b128 v[222:225], v208 offset:4096
	ds_read_b128 v[230:233], v208 offset:6144
	global_load_lds_dwordx4 v[234:235], off
	v_lshl_add_u64 v[234:235], s[46:47], 0, v[174:175]
	s_add_i32 m0, s25, 0xe000
	s_nop 0
	global_load_lds_dwordx4 v[234:235], off
	s_waitcnt vmcnt(8)
	s_waitcnt lgkmcnt(0)
	s_barrier
	s_setprio 1
	v_mfma_f32_16x16x128_f8f6f4 v[158:161], v[18:25], v[176:183], v[158:161]
	v_mfma_f32_16x16x128_f8f6f4 v[154:157], v[26:33], v[176:183], v[154:157]
	v_mfma_f32_16x16x128_f8f6f4 v[146:149], v[18:25], v[210:217], v[146:149]
	v_mfma_f32_16x16x128_f8f6f4 v[138:141], v[26:33], v[210:217], v[138:141]
	v_mfma_f32_16x16x128_f8f6f4 v[130:133], v[18:25], v[218:225], v[130:133]
	v_mfma_f32_16x16x128_f8f6f4 v[122:125], v[26:33], v[218:225], v[122:125]
	v_mfma_f32_16x16x128_f8f6f4 v[114:117], v[18:25], v[226:233], v[114:117]
	v_mfma_f32_16x16x128_f8f6f4 v[106:109], v[26:33], v[226:233], v[106:109]
	s_setprio 0
	s_setprio 1
	v_mfma_f32_16x16x128_f8f6f4 v[150:153], v[2:9], v[176:183], v[150:153]
	v_mfma_f32_16x16x128_f8f6f4 v[142:145], v[10:17], v[176:183], v[142:145]
	v_mfma_f32_16x16x128_f8f6f4 v[134:137], v[2:9], v[210:217], v[134:137]
	v_mfma_f32_16x16x128_f8f6f4 v[126:129], v[10:17], v[210:217], v[126:129]
	v_mfma_f32_16x16x128_f8f6f4 v[118:121], v[2:9], v[218:225], v[118:121]
	v_mfma_f32_16x16x128_f8f6f4 v[110:113], v[10:17], v[218:225], v[110:113]
	v_mfma_f32_16x16x128_f8f6f4 v[102:105], v[2:9], v[226:233], v[102:105]
	v_mfma_f32_16x16x128_f8f6f4 v[98:101], v[10:17], v[226:233], v[98:101]
	s_setprio 0
	s_barrier
	s_mov_b32 m0, s33
	v_lshl_add_u64 v[176:177], s[50:51], 0, v[166:167]
	s_add_u32 s46, s50, 0xe0000
	ds_read_b128 v[210:213], v207 offset:16384
	ds_read_b128 v[218:221], v207 offset:18432
	ds_read_b128 v[214:217], v208 offset:16384
	ds_read_b128 v[222:225], v208 offset:18432
	ds_read_b128 v[226:229], v207 offset:20480
	ds_read_b128 v[234:237], v207 offset:22528
	ds_read_b128 v[230:233], v208 offset:20480
	ds_read_b128 v[238:241], v208 offset:22528
	global_load_lds_dwordx4 v[176:177], off
	v_lshl_add_u64 v[178:179], s[50:51], 0, v[162:163]
	s_mov_b32 m0, s35
	s_addc_u32 s47, s51, 0
	global_load_lds_dwordx4 v[178:179], off
	v_lshl_add_u64 v[180:181], s[46:47], 0, v[166:167]
	s_mov_b32 m0, s54
	v_lshl_add_u64 v[182:183], s[52:53], 0, v[164:165]
	global_load_lds_dwordx4 v[180:181], off
	v_lshl_add_u64 v[180:181], s[46:47], 0, v[162:163]
	s_mov_b32 m0, s55
	s_nop 0
	global_load_lds_dwordx4 v[180:181], off
	v_lshl_add_u64 v[180:181], s[52:53], 0, v[168:169]
	s_mov_b32 m0, s25
	s_nop 0
	global_load_lds_dwordx4 v[180:181], off
	s_mov_b32 m0, s56
	s_nop 0
	global_load_lds_dwordx4 v[182:183], off
	s_waitcnt vmcnt(8)
	s_waitcnt lgkmcnt(0)
	s_barrier
	s_setprio 1
	v_mfma_f32_16x16x128_f8f6f4 v[94:97], v[18:25], v[210:217], v[94:97]
	v_mfma_f32_16x16x128_f8f6f4 v[90:93], v[26:33], v[210:217], v[90:93]
	v_mfma_f32_16x16x128_f8f6f4 v[82:85], v[18:25], v[218:225], v[82:85]
	v_mfma_f32_16x16x128_f8f6f4 v[74:77], v[26:33], v[218:225], v[74:77]
	v_mfma_f32_16x16x128_f8f6f4 v[66:69], v[18:25], v[226:233], v[66:69]
	v_mfma_f32_16x16x128_f8f6f4 v[58:61], v[26:33], v[226:233], v[58:61]
	v_mfma_f32_16x16x128_f8f6f4 v[50:53], v[18:25], v[234:241], v[50:53]
	v_mfma_f32_16x16x128_f8f6f4 v[42:45], v[26:33], v[234:241], v[42:45]
	s_setprio 0
	s_setprio 1
	v_mfma_f32_16x16x128_f8f6f4 v[86:89], v[2:9], v[210:217], v[86:89]
	v_mfma_f32_16x16x128_f8f6f4 v[78:81], v[10:17], v[210:217], v[78:81]
	v_mfma_f32_16x16x128_f8f6f4 v[70:73], v[2:9], v[218:225], v[70:73]
	v_mfma_f32_16x16x128_f8f6f4 v[62:65], v[10:17], v[218:225], v[62:65]
	v_mfma_f32_16x16x128_f8f6f4 v[54:57], v[2:9], v[226:233], v[54:57]
	v_mfma_f32_16x16x128_f8f6f4 v[46:49], v[10:17], v[226:233], v[46:49]
	v_mfma_f32_16x16x128_f8f6f4 v[38:41], v[2:9], v[234:241], v[38:41]
	v_mfma_f32_16x16x128_f8f6f4 v[34:37], v[10:17], v[234:241], v[34:37]
	s_setprio 0
	s_barrier
; #define PG8_STAGE(bufoff, gbase, voff) do { _Pragma("unroll") for (int _i = 0; _i < 2; ++_i) \
;         __builtin_amdgcn_global_load_lds((const unsigned*)((const char*)(gbase) + (voff)[_i]), (LAS unsigned*)(lds + (bufoff) + ldsw + _i * 8192), 16, 0, 0); } while (0)
; #define PG8_LDA(dst, b, h) do { _Pragma("unroll") for (int m = 0; m < 4; ++m) _Pragma("unroll") for (int k = 0; k < 2; ++k) dst[m][k] = *(const LAS bf16x8*)(lds + PG8_SA(b, h) + aoff + m * 2048 + k * 1024); } while (0)
; #define PG8_LDB(dst, b, h) do { _Pragma("unroll") for (int n = 0; n < 2; ++n) _Pragma("unroll") for (int k = 0; k < 2; ++k) dst[n][k] = *(const LAS bf16x8*)(lds + PG8_SB(b, h) + boff + n * 2048 + k * 1024); } while (0)
; #define PG8_MMA(ai, bj, At, Bt) do { __builtin_amdgcn_s_setprio(1); _Pragma("unroll") for (int m = 0; m < 4; ++m) _Pragma("unroll") for (int n = 0; n < 2; ++n) _Pragma("unroll") for (int k = 0; k < 2; ++k) \
;         acc[ai][bj][m][n] = __builtin_amdgcn_mfma_f32_16x16x32_bf16(Bt[n][k], At[m][k], acc[ai][bj][m][n], 0, 0, 0); __builtin_amdgcn_s_setprio(0); } while (0)
; #define PG8_WAIT_V(n) asm volatile("s_waitcnt vmcnt(" #n ")" ::: "memory")
; #define PG8_WAIT_L(n) asm volatile("s_waitcnt lgkmcnt(" #n ")" ::: "memory")
; #define PG8_BAR __builtin_amdgcn_s_barrier()
; #define PG8_SCHED __builtin_amdgcn_sched_barrier(0)
; #define PG8_STAGE(bufoff, gbase, voff) do { _Pragma("unroll") for (int _i = 0; _i < 2; ++_i) \
;         __builtin_amdgcn_global_load_lds((const unsigned*)((const char*)(gbase) + (voff)[_i]), (LAS unsigned*)(lds + (bufoff) + ldsw + _i * 8192), 16, 0, 0); } while (0)
; #define PG8_WAIT_V(n) asm volatile("s_waitcnt vmcnt(" #n ")" ::: "memory")
; #define PG8_WAIT_L(n) asm volatile("s_waitcnt lgkmcnt(" #n ")" ::: "memory")
;     ...
;             PG8_LDB(B0, 1, 0); PG8_LDB(B1, 1, 1); PG8_SCHED; PG8_LDA(At, 1, 0); PG8_STAGE(PG8_SA(0, 1), a2 + hstepA, voffA);
;             PG8_WAIT_V(8); PG8_WAIT_L(0); PG8_BAR; PG8_MMA(0, 0, At, B0); PG8_MMA(0, 1, At, B1); PG8_BAR; PG8_SCHED;
;             PG8_LDA(At, 1, 1); PG8_STAGE(PG8_SB(1, 0), b3, voffB); PG8_STAGE(PG8_SB(1, 1), b3 + hstepB, voffB); PG8_STAGE(PG8_SA(1, 0), a3, voffA);
;             PG8_WAIT_V(8); PG8_WAIT_L(0); PG8_BAR; PG8_MMA(1, 0, At, B0); PG8_MMA(1, 1, At, B1); PG8_BAR; PG8_SCHED;
;         }
;         asm volatile("s_nop 15\n\ts_nop 15" ::: "memory");
;         if (wr == 0) PG8_BAR;
	ds_read_b128 v[2:5], v194
	ds_read_b128 v[6:9], v195
	ds_read_b128 v[10:13], v202
	ds_read_b128 v[14:17], v203
	ds_read_b128 v[18:21], v196
	ds_read_b128 v[22:25], v197
	ds_read_b128 v[26:29], v204
	ds_read_b128 v[30:33], v205
	s_add_u32 s46, s52, 0xe0000
	s_addc_u32 s47, s53, 0
	s_mov_b32 m0, s57
	v_lshl_add_u64 v[242:243], s[46:47], 0, v[168:169]
	ds_read_b128 v[210:213], v207 offset:32768
	ds_read_b128 v[218:221], v207 offset:34816
	ds_read_b128 v[214:217], v208 offset:32768
	ds_read_b128 v[222:225], v208 offset:34816
	ds_read_b128 v[226:229], v207 offset:36864
	ds_read_b128 v[234:237], v207 offset:38912
	ds_read_b128 v[230:233], v208 offset:36864
	ds_read_b128 v[238:241], v208 offset:38912
	global_load_lds_dwordx4 v[242:243], off
	v_lshl_add_u64 v[242:243], s[46:47], 0, v[164:165]
	s_mov_b32 m0, s58
	s_nop 0
	global_load_lds_dwordx4 v[242:243], off
	s_waitcnt vmcnt(8)
	s_waitcnt lgkmcnt(0)
	s_barrier
	s_setprio 1
	v_mfma_f32_16x16x128_f8f6f4 v[158:161], v[2:9], v[210:217], v[158:161]
	v_mfma_f32_16x16x128_f8f6f4 v[154:157], v[10:17], v[210:217], v[154:157]
	v_mfma_f32_16x16x128_f8f6f4 v[146:149], v[2:9], v[218:225], v[146:149]
	v_mfma_f32_16x16x128_f8f6f4 v[138:141], v[10:17], v[218:225], v[138:141]
	v_mfma_f32_16x16x128_f8f6f4 v[130:133], v[2:9], v[226:233], v[130:133]
	v_mfma_f32_16x16x128_f8f6f4 v[122:125], v[10:17], v[226:233], v[122:125]
	v_mfma_f32_16x16x128_f8f6f4 v[114:117], v[2:9], v[234:241], v[114:117]
	v_mfma_f32_16x16x128_f8f6f4 v[106:109], v[10:17], v[234:241], v[106:109]
	s_setprio 0
	s_setprio 1
	v_mfma_f32_16x16x128_f8f6f4 v[150:153], v[18:25], v[210:217], v[150:153]
	v_mfma_f32_16x16x128_f8f6f4 v[142:145], v[26:33], v[210:217], v[142:145]
	v_mfma_f32_16x16x128_f8f6f4 v[134:137], v[18:25], v[218:225], v[134:137]
	v_mfma_f32_16x16x128_f8f6f4 v[126:129], v[26:33], v[218:225], v[126:129]
	v_mfma_f32_16x16x128_f8f6f4 v[118:121], v[18:25], v[226:233], v[118:121]
	v_mfma_f32_16x16x128_f8f6f4 v[110:113], v[26:33], v[226:233], v[110:113]
	v_mfma_f32_16x16x128_f8f6f4 v[102:105], v[18:25], v[234:241], v[102:105]
	v_mfma_f32_16x16x128_f8f6f4 v[98:101], v[26:33], v[234:241], v[98:101]
	s_setprio 0
	s_barrier
	s_mov_b32 m0, s62
	v_lshl_add_u64 v[176:177], v[176:177], 0, s[12:13]
	s_add_u32 s46, s50, 0xe0080
	ds_read_b128 v[210:213], v207 offset:49152
	ds_read_b128 v[218:221], v207 offset:51200
	ds_read_b128 v[214:217], v208 offset:49152
	ds_read_b128 v[222:225], v208 offset:51200
	ds_read_b128 v[226:229], v207 offset:53248
	ds_read_b128 v[234:237], v207 offset:55296
	ds_read_b128 v[230:233], v208 offset:53248
	ds_read_b128 v[238:241], v208 offset:55296
	global_load_lds_dwordx4 v[176:177], off
	v_lshl_add_u64 v[176:177], v[178:179], 0, s[12:13]
	s_mov_b32 m0, s63
	s_addc_u32 s47, s51, 0
	global_load_lds_dwordx4 v[176:177], off
	v_lshl_add_u64 v[176:177], s[46:47], 0, v[166:167]
	s_mov_b32 m0, s66
	s_nop 0
	global_load_lds_dwordx4 v[176:177], off
	v_lshl_add_u64 v[176:177], s[46:47], 0, v[162:163]
	s_mov_b32 m0, s67
	s_nop 0
	global_load_lds_dwordx4 v[176:177], off
	v_lshl_add_u64 v[176:177], v[180:181], 0, s[12:13]
	s_mov_b32 m0, s64
	s_nop 0
	global_load_lds_dwordx4 v[176:177], off
	v_lshl_add_u64 v[176:177], v[182:183], 0, s[12:13]
	s_mov_b32 m0, s65
	s_nop 0
	global_load_lds_dwordx4 v[176:177], off
	s_waitcnt vmcnt(8)
	s_waitcnt lgkmcnt(0)
	s_barrier
	s_setprio 1
	v_mfma_f32_16x16x128_f8f6f4 v[94:97], v[2:9], v[210:217], v[94:97]
	v_mfma_f32_16x16x128_f8f6f4 v[90:93], v[10:17], v[210:217], v[90:93]
	v_mfma_f32_16x16x128_f8f6f4 v[82:85], v[2:9], v[218:225], v[82:85]
	v_mfma_f32_16x16x128_f8f6f4 v[74:77], v[10:17], v[218:225], v[74:77]
	v_mfma_f32_16x16x128_f8f6f4 v[66:69], v[2:9], v[226:233], v[66:69]
	v_mfma_f32_16x16x128_f8f6f4 v[58:61], v[10:17], v[226:233], v[58:61]
	v_mfma_f32_16x16x128_f8f6f4 v[50:53], v[2:9], v[234:241], v[50:53]
	v_mfma_f32_16x16x128_f8f6f4 v[42:45], v[10:17], v[234:241], v[42:45]
	s_setprio 0
	s_setprio 1
	v_mfma_f32_16x16x128_f8f6f4 v[86:89], v[18:25], v[210:217], v[86:89]
	v_mfma_f32_16x16x128_f8f6f4 v[78:81], v[26:33], v[210:217], v[78:81]
	v_mfma_f32_16x16x128_f8f6f4 v[70:73], v[18:25], v[218:225], v[70:73]
	v_mfma_f32_16x16x128_f8f6f4 v[62:65], v[26:33], v[218:225], v[62:65]
	s_add_i32 s88, s88, 2
	s_add_u32 s86, s86, 0x100
	s_addc_u32 s87, s87, 0
	s_cmp_gt_u32 s88, 11
	s_mov_b64 s[46:47], s[48:49]
	v_mfma_f32_16x16x128_f8f6f4 v[54:57], v[18:25], v[226:233], v[54:57]
	v_mfma_f32_16x16x128_f8f6f4 v[46:49], v[26:33], v[226:233], v[46:49]
	v_mfma_f32_16x16x128_f8f6f4 v[38:41], v[18:25], v[234:241], v[38:41]
	v_mfma_f32_16x16x128_f8f6f4 v[34:37], v[26:33], v[234:241], v[34:37]
	s_setprio 0
	s_barrier
	s_cbranch_scc0 .LBB0_1497
	s_nop 15
	s_nop 15
	s_and_b64 vcc, exec, s[14:15]
	s_cbranch_vccz .LBB0_1500
	s_barrier
